# MoE-down: non-temporal hint on the Y row stores (never re-read in the phase)
# speedup vs baseline: 1.0065x; 1.0002x over previous
; #define MD_GLDS_A(buf, tau) do { _Pragma("unroll") for (int i = 0; i < 5; ++i) if (amask & (1u << i)) \
;         __builtin_amdgcn_global_load_lds((const unsigned*)((const char*)HIDp + aoff[i] + (size_t)((tau) & 7) * 128), (PG8_LAS unsigned*)(MD_SA(buf) + wid * 1024 + i * 8192), 16, 0, 0); } while (0)
; #define MD_B_ISSUE(sb, tau) do { const char* kb_ = Bb + (size_t)((tau) >> 3) * 512 + (size_t)((tau) & 7) * (64 * (size_t)RB); _Pragma("unroll") for (int j = 0; j < 8; ++j) { const char* p_ = kb_ + (size_t)j * RB; \
;         asm volatile("global_load_dwordx2 %0, %1, off" : "=&v"(sb[j]) : "v"(p_) : "memory"); } } while (0)
; #define MD_B_WAIT(sb, N) asm volatile("s_waitcnt vmcnt(%8)" : "+v"(sb[0]), "+v"(sb[1]), "+v"(sb[2]), "+v"(sb[3]), "+v"(sb[4]), "+v"(sb[5]), "+v"(sb[6]), "+v"(sb[7]) : "n"(N) : "memory")
; __device__ __forceinline__ void moe_down_stream(PG8_LAS unsigned char* lds, int e, int cb0, int slot0, int nv, const bf16_t* HIDp, const float* Wd, bf16_t* Y, const float* slot_w, const int* slot_dst) {
;     ...
;     f32x4 acc[DNM][4];
; #pragma unroll
;     for (int m = 0; m < DNM; ++m)
; #pragma unroll
;         for (int n = 0; n < 4; ++n) acc[m][n] = (f32x4){0.f, 0.f, 0.f, 0.f};
;     f32x2 s0[8], s1[8];
;     MD_GLDS_A(0, 0); MD_B_ISSUE(s0, 0); MD_B_ISSUE(s1, 1);
;     MD_B_WAIT(s0, 8); MD_B_WRITE(s0, 0); __builtin_amdgcn_sched_barrier(0); MD_B_ISSUE(s0, 2);
;     asm volatile("s_waitcnt vmcnt(16)" ::: "memory");
;     asm volatile("s_waitcnt lgkmcnt(0)" ::: "memory"); __builtin_amdgcn_s_barrier(); asm volatile("" ::: "memory");
; #pragma unroll 1
;     for (int t = 0; t < NT; t += 2) {
;         if (t + 2 < NT) MD_B_WAIT(s1, 8); else MD_B_WAIT(s1, 0);
;         MD_B_WRITE(s1, 1); __builtin_amdgcn_sched_barrier(0); MD_GLDS_A(1, t + 1); __builtin_amdgcn_sched_barrier(0);
;         if (t + 3 < NT) MD_B_ISSUE(s1, t + 3);
;         MD_COMPUTE(0);
;         MD_END(t + 3 >= NT);
;         if (t + 2 < NT) { MD_B_WAIT(s0, 8); MD_B_WRITE(s0, 0); __builtin_amdgcn_sched_barrier(0); MD_GLDS_A(0, t + 2); __builtin_amdgcn_sched_barrier(0); }
;         if (t + 4 < NT) MD_B_ISSUE(s0, t + 4);
;         MD_COMPUTE(1);
;         MD_END(t + 4 >= NT);
.Lmd_loop_X:
	v_cvt_pk_bf16_f32 v172, v114, v116
	v_cvt_pk_bf16_f32 v173, v118, v120
	v_cvt_pk_bf16_f32 v174, v122, v124
	v_cvt_pk_bf16_f32 v175, v126, v128
	v_cvt_pk_bf16_f32 v176, v115, v117
	v_cvt_pk_bf16_f32 v177, v119, v121
	v_cvt_pk_bf16_f32 v178, v123, v125
	v_cvt_pk_bf16_f32 v179, v127, v129
	ds_write_b128 v95, v[172:175] offset:19456
	ds_write_b128 v95, v[176:179] offset:19584
	v_add_u32_e32 v91, s46, v135
	v_add_u32_e32 v93, s46, v137
	ds_read_b128 v[238:241], v139 offset:0
	ds_read_b128 v[242:245], v139 offset:2048
	ds_read_b128 v[246:249], v139 offset:4096
	ds_read_b128 v[250:253], v139 offset:6144
	ds_read_b128 v[218:221], v91 offset:0
	ds_read_b128 v[222:225], v91 offset:2048
	ds_read_b128 v[226:229], v91 offset:4096
	ds_read_b128 v[230:233], v91 offset:6144
	ds_read_b128 v[234:237], v91 offset:8192
	s_add_i32 s49, s48, s74
	s_add_i32 s52, s52, 1
	s_and_b32 s54, s52, 7
	s_cmp_eq_u32 s54, 0
	s_cselect_b32 s54, s53, s32
	s_cselect_b32 s55, -1, 0
	s_add_u32 s30, s30, s54
	s_addc_u32 s31, s31, s55
	s_waitcnt lgkmcnt(0)
	v_mfma_f32_16x16x32_bf16 v[78:81], v[238:241], v[218:221], v[78:81]
	v_mfma_f32_16x16x32_bf16 v[74:77], v[242:245], v[218:221], v[74:77]
	v_mfma_f32_16x16x32_bf16 v[70:73], v[246:249], v[218:221], v[70:73]
	v_mfma_f32_16x16x32_bf16 v[66:69], v[250:253], v[218:221], v[66:69]
	ds_read_b128 v[218:221], v93 offset:0
	ds_read_b128 v[142:145], v141 offset:0
	s_mov_b32 m0, s49
	s_nop 0
	global_load_lds_dwordx4 v88, s[30:31]
	v_mfma_f32_16x16x32_bf16 v[62:65], v[238:241], v[222:225], v[62:65]
	v_mfma_f32_16x16x32_bf16 v[58:61], v[242:245], v[222:225], v[58:61]
	v_mfma_f32_16x16x32_bf16 v[54:57], v[246:249], v[222:225], v[54:57]
	v_mfma_f32_16x16x32_bf16 v[50:53], v[250:253], v[222:225], v[50:53]
	ds_read_b128 v[222:225], v93 offset:2048
	ds_read_b128 v[146:149], v141 offset:2048
	s_add_i32 m0, s49, 0x2000
	s_nop 0
	global_load_lds_dwordx4 v90, s[30:31]
	v_mfma_f32_16x16x32_bf16 v[46:49], v[238:241], v[226:229], v[46:49]
	v_mfma_f32_16x16x32_bf16 v[42:45], v[242:245], v[226:229], v[42:45]
	v_mfma_f32_16x16x32_bf16 v[38:41], v[246:249], v[226:229], v[38:41]
	v_mfma_f32_16x16x32_bf16 v[34:37], v[250:253], v[226:229], v[34:37]
	ds_read_b128 v[226:229], v93 offset:4096
	ds_read_b128 v[156:159], v141 offset:4096
	s_add_i32 m0, s49, 0x4000
	s_nop 0
	global_load_lds_dwordx4 v92, s[30:31]
	v_mfma_f32_16x16x32_bf16 v[18:21], v[238:241], v[230:233], v[18:21]
	v_mfma_f32_16x16x32_bf16 v[22:25], v[242:245], v[230:233], v[22:25]
	v_mfma_f32_16x16x32_bf16 v[26:29], v[246:249], v[230:233], v[26:29]
	v_mfma_f32_16x16x32_bf16 v[30:33], v[250:253], v[230:233], v[30:33]
	ds_read_b128 v[230:233], v93 offset:6144
	ds_read_b128 v[160:163], v141 offset:6144
	s_add_i32 m0, s49, 0x6000
	s_nop 0
	global_load_lds_dwordx4 v94, s[30:31]
	v_mfma_f32_16x16x32_bf16 v[2:5], v[238:241], v[234:237], v[2:5]
	v_mfma_f32_16x16x32_bf16 v[6:9], v[242:245], v[234:237], v[6:9]
	v_mfma_f32_16x16x32_bf16 v[10:13], v[246:249], v[234:237], v[10:13]
	v_mfma_f32_16x16x32_bf16 v[14:17], v[250:253], v[234:237], v[14:17]
	ds_read_b128 v[234:237], v93 offset:8192
	s_add_i32 m0, s49, 0x8000
	s_nop 0
	global_load_lds_dwordx4 v96, s[30:31]
	s_waitcnt lgkmcnt(0)
	v_mfma_f32_16x16x32_bf16 v[78:81], v[142:145], v[218:221], v[78:81]
	v_mfma_f32_16x16x32_bf16 v[74:77], v[146:149], v[218:221], v[74:77]
	v_mfma_f32_16x16x32_bf16 v[70:73], v[156:159], v[218:221], v[70:73]
	v_mfma_f32_16x16x32_bf16 v[66:69], v[160:163], v[218:221], v[66:69]
	s_add_i32 s51, s51, 1
	s_and_b32 s54, s51, 7
	s_cmp_eq_u32 s54, 0
	s_cselect_b32 s44, s34, s35
	s_cselect_b32 s45, -1, 0
	v_lshl_add_u64 v[132:133], v[132:133], 0, s[44:45]
	global_load_dwordx2 v[114:115], v[132:133], off
	v_lshl_add_u64 v[180:181], v[132:133], 0, s[24:25]
	global_load_dwordx2 v[116:117], v[180:181], off
	v_mfma_f32_16x16x32_bf16 v[62:65], v[142:145], v[222:225], v[62:65]
	v_mfma_f32_16x16x32_bf16 v[58:61], v[146:149], v[222:225], v[58:61]
	v_mfma_f32_16x16x32_bf16 v[54:57], v[156:159], v[222:225], v[54:57]
	v_mfma_f32_16x16x32_bf16 v[50:53], v[160:163], v[222:225], v[50:53]
	v_lshl_add_u64 v[180:181], v[132:133], 0, s[26:27]
	global_load_dwordx2 v[118:119], v[180:181], off
	v_lshl_add_u64 v[180:181], v[132:133], 0, s[28:29]
	global_load_dwordx2 v[120:121], v[180:181], off
	v_mfma_f32_16x16x32_bf16 v[46:49], v[142:145], v[226:229], v[46:49]
	v_mfma_f32_16x16x32_bf16 v[42:45], v[146:149], v[226:229], v[42:45]
	v_mfma_f32_16x16x32_bf16 v[38:41], v[156:159], v[226:229], v[38:41]
	v_mfma_f32_16x16x32_bf16 v[34:37], v[160:163], v[226:229], v[34:37]
	v_lshl_add_u64 v[180:181], v[132:133], 0, s[36:37]
	global_load_dwordx2 v[122:123], v[180:181], off
	v_lshl_add_u64 v[180:181], v[132:133], 0, s[38:39]
	global_load_dwordx2 v[124:125], v[180:181], off
	v_mfma_f32_16x16x32_bf16 v[18:21], v[142:145], v[230:233], v[18:21]
	v_mfma_f32_16x16x32_bf16 v[22:25], v[146:149], v[230:233], v[22:25]
	v_mfma_f32_16x16x32_bf16 v[26:29], v[156:159], v[230:233], v[26:29]
	v_mfma_f32_16x16x32_bf16 v[30:33], v[160:163], v[230:233], v[30:33]
	v_lshl_add_u64 v[180:181], v[132:133], 0, s[40:41]
	global_load_dwordx2 v[126:127], v[180:181], off
	v_lshl_add_u64 v[180:181], v[132:133], 0, s[42:43]
	global_load_dwordx2 v[128:129], v[180:181], off
	v_mfma_f32_16x16x32_bf16 v[2:5], v[142:145], v[234:237], v[2:5]
	v_mfma_f32_16x16x32_bf16 v[6:9], v[146:149], v[234:237], v[6:9]
	v_mfma_f32_16x16x32_bf16 v[10:13], v[156:159], v[234:237], v[10:13]
	v_mfma_f32_16x16x32_bf16 v[14:17], v[160:163], v[234:237], v[14:17]
	s_waitcnt vmcnt(21)
	s_waitcnt lgkmcnt(0)
	s_barrier
; #define MD_GLDS_A(buf, tau) do { _Pragma("unroll") for (int i = 0; i < 5; ++i) if (amask & (1u << i)) \
;         __builtin_amdgcn_global_load_lds((const unsigned*)((const char*)HIDp + aoff[i] + (size_t)((tau) & 7) * 128), (PG8_LAS unsigned*)(MD_SA(buf) + wid * 1024 + i * 8192), 16, 0, 0); } while (0)
; #define MD_B_ISSUE(sb, tau) do { const char* kb_ = Bb + (size_t)((tau) >> 3) * 512 + (size_t)((tau) & 7) * (64 * (size_t)RB); _Pragma("unroll") for (int j = 0; j < 8; ++j) { const char* p_ = kb_ + (size_t)j * RB; \
;         asm volatile("global_load_dwordx2 %0, %1, off" : "=&v"(sb[j]) : "v"(p_) : "memory"); } } while (0)
; #define MD_B_WAIT(sb, N) asm volatile("s_waitcnt vmcnt(%8)" : "+v"(sb[0]), "+v"(sb[1]), "+v"(sb[2]), "+v"(sb[3]), "+v"(sb[4]), "+v"(sb[5]), "+v"(sb[6]), "+v"(sb[7]) : "n"(N) : "memory")
; __device__ __forceinline__ void moe_down_stream(PG8_LAS unsigned char* lds, int e, int cb0, int slot0, int nv, const bf16_t* HIDp, const float* Wd, bf16_t* Y, const float* slot_w, const int* slot_dst) {
;     ...
;     f32x4 acc[DNM][4];
; #pragma unroll
;     for (int m = 0; m < DNM; ++m)
; #pragma unroll
;         for (int n = 0; n < 4; ++n) acc[m][n] = (f32x4){0.f, 0.f, 0.f, 0.f};
;     f32x2 s0[8], s1[8];
;     MD_GLDS_A(0, 0); MD_B_ISSUE(s0, 0); MD_B_ISSUE(s1, 1);
;     MD_B_WAIT(s0, 8); MD_B_WRITE(s0, 0); __builtin_amdgcn_sched_barrier(0); MD_B_ISSUE(s0, 2);
;     asm volatile("s_waitcnt vmcnt(16)" ::: "memory");
;     asm volatile("s_waitcnt lgkmcnt(0)" ::: "memory"); __builtin_amdgcn_s_barrier(); asm volatile("" ::: "memory");
; #pragma unroll 1
;     for (int t = 0; t < NT; t += 2) {
;         if (t + 2 < NT) MD_B_WAIT(s1, 8); else MD_B_WAIT(s1, 0);
;         MD_B_WRITE(s1, 1); __builtin_amdgcn_sched_barrier(0); MD_GLDS_A(1, t + 1); __builtin_amdgcn_sched_barrier(0);
;         if (t + 3 < NT) MD_B_ISSUE(s1, t + 3);
;         MD_COMPUTE(0);
;         MD_END(t + 3 >= NT);
;         if (t + 2 < NT) { MD_B_WAIT(s0, 8); MD_B_WRITE(s0, 0); __builtin_amdgcn_sched_barrier(0); MD_GLDS_A(0, t + 2); __builtin_amdgcn_sched_barrier(0); }
;         if (t + 4 < NT) MD_B_ISSUE(s0, t + 4);
;         MD_COMPUTE(1);
;         MD_END(t + 4 >= NT);
	s_mov_b32 s49, s46
	s_mov_b32 s46, s47
	s_mov_b32 s47, s48
	s_mov_b32 s48, s49
	s_add_i32 s50, s50, 1
	v_cvt_pk_bf16_f32 v172, v186, v188
	v_cvt_pk_bf16_f32 v173, v190, v192
	v_cvt_pk_bf16_f32 v174, v194, v196
	v_cvt_pk_bf16_f32 v175, v198, v200
	v_cvt_pk_bf16_f32 v176, v187, v189
	v_cvt_pk_bf16_f32 v177, v191, v193
	v_cvt_pk_bf16_f32 v178, v195, v197
	v_cvt_pk_bf16_f32 v179, v199, v201
	ds_write_b128 v95, v[172:175] offset:0
	ds_write_b128 v95, v[176:179] offset:128
	v_add_u32_e32 v91, s46, v135
	v_add_u32_e32 v93, s46, v137
	ds_read_b128 v[238:241], v139 offset:19456
	ds_read_b128 v[242:245], v139 offset:21504
	ds_read_b128 v[246:249], v139 offset:23552
	ds_read_b128 v[250:253], v139 offset:25600
	ds_read_b128 v[218:221], v91 offset:0
	ds_read_b128 v[222:225], v91 offset:2048
	ds_read_b128 v[226:229], v91 offset:4096
	ds_read_b128 v[230:233], v91 offset:6144
	ds_read_b128 v[234:237], v91 offset:8192
	s_add_i32 s49, s48, s74
	s_add_i32 s52, s52, 1
	s_and_b32 s54, s52, 7
	s_cmp_eq_u32 s54, 0
	s_cselect_b32 s54, s53, s32
	s_cselect_b32 s55, -1, 0
	s_add_u32 s30, s30, s54
	s_addc_u32 s31, s31, s55
	s_waitcnt lgkmcnt(0)
	v_mfma_f32_16x16x32_bf16 v[78:81], v[238:241], v[218:221], v[78:81]
	v_mfma_f32_16x16x32_bf16 v[74:77], v[242:245], v[218:221], v[74:77]
	v_mfma_f32_16x16x32_bf16 v[70:73], v[246:249], v[218:221], v[70:73]
	v_mfma_f32_16x16x32_bf16 v[66:69], v[250:253], v[218:221], v[66:69]
	ds_read_b128 v[218:221], v93 offset:0
	ds_read_b128 v[142:145], v141 offset:19456
	s_mov_b32 m0, s49
	s_nop 0
	global_load_lds_dwordx4 v88, s[30:31]
	v_mfma_f32_16x16x32_bf16 v[62:65], v[238:241], v[222:225], v[62:65]
	v_mfma_f32_16x16x32_bf16 v[58:61], v[242:245], v[222:225], v[58:61]
	v_mfma_f32_16x16x32_bf16 v[54:57], v[246:249], v[222:225], v[54:57]
	v_mfma_f32_16x16x32_bf16 v[50:53], v[250:253], v[222:225], v[50:53]
	ds_read_b128 v[222:225], v93 offset:2048
	ds_read_b128 v[146:149], v141 offset:21504
	s_add_i32 m0, s49, 0x2000
	s_nop 0
	global_load_lds_dwordx4 v90, s[30:31]
	v_mfma_f32_16x16x32_bf16 v[46:49], v[238:241], v[226:229], v[46:49]
	v_mfma_f32_16x16x32_bf16 v[42:45], v[242:245], v[226:229], v[42:45]
	v_mfma_f32_16x16x32_bf16 v[38:41], v[246:249], v[226:229], v[38:41]
	v_mfma_f32_16x16x32_bf16 v[34:37], v[250:253], v[226:229], v[34:37]
	ds_read_b128 v[226:229], v93 offset:4096
	ds_read_b128 v[156:159], v141 offset:23552
	s_add_i32 m0, s49, 0x4000
	s_nop 0
	global_load_lds_dwordx4 v92, s[30:31]
	v_mfma_f32_16x16x32_bf16 v[18:21], v[238:241], v[230:233], v[18:21]
	v_mfma_f32_16x16x32_bf16 v[22:25], v[242:245], v[230:233], v[22:25]
	v_mfma_f32_16x16x32_bf16 v[26:29], v[246:249], v[230:233], v[26:29]
	v_mfma_f32_16x16x32_bf16 v[30:33], v[250:253], v[230:233], v[30:33]
	ds_read_b128 v[230:233], v93 offset:6144
	ds_read_b128 v[160:163], v141 offset:25600
	s_add_i32 m0, s49, 0x6000
	s_nop 0
	global_load_lds_dwordx4 v94, s[30:31]
	v_mfma_f32_16x16x32_bf16 v[2:5], v[238:241], v[234:237], v[2:5]
	v_mfma_f32_16x16x32_bf16 v[6:9], v[242:245], v[234:237], v[6:9]
	v_mfma_f32_16x16x32_bf16 v[10:13], v[246:249], v[234:237], v[10:13]
	v_mfma_f32_16x16x32_bf16 v[14:17], v[250:253], v[234:237], v[14:17]
	ds_read_b128 v[234:237], v93 offset:8192
	s_add_i32 m0, s49, 0x8000
	s_nop 0
	global_load_lds_dwordx4 v96, s[30:31]
	s_waitcnt lgkmcnt(0)
	v_mfma_f32_16x16x32_bf16 v[78:81], v[142:145], v[218:221], v[78:81]
	v_mfma_f32_16x16x32_bf16 v[74:77], v[146:149], v[218:221], v[74:77]
	v_mfma_f32_16x16x32_bf16 v[70:73], v[156:159], v[218:221], v[70:73]
	v_mfma_f32_16x16x32_bf16 v[66:69], v[160:163], v[218:221], v[66:69]
	s_add_i32 s51, s51, 1
	s_and_b32 s54, s51, 7
	s_cmp_eq_u32 s54, 0
	s_cselect_b32 s44, s34, s35
	s_cselect_b32 s45, -1, 0
	v_lshl_add_u64 v[132:133], v[132:133], 0, s[44:45]
	global_load_dwordx2 v[186:187], v[132:133], off
	v_lshl_add_u64 v[180:181], v[132:133], 0, s[24:25]
	global_load_dwordx2 v[188:189], v[180:181], off
	v_mfma_f32_16x16x32_bf16 v[62:65], v[142:145], v[222:225], v[62:65]
	v_mfma_f32_16x16x32_bf16 v[58:61], v[146:149], v[222:225], v[58:61]
	v_mfma_f32_16x16x32_bf16 v[54:57], v[156:159], v[222:225], v[54:57]
	v_mfma_f32_16x16x32_bf16 v[50:53], v[160:163], v[222:225], v[50:53]
	v_lshl_add_u64 v[180:181], v[132:133], 0, s[26:27]
	global_load_dwordx2 v[190:191], v[180:181], off
	v_lshl_add_u64 v[180:181], v[132:133], 0, s[28:29]
	global_load_dwordx2 v[192:193], v[180:181], off
	v_mfma_f32_16x16x32_bf16 v[46:49], v[142:145], v[226:229], v[46:49]
	v_mfma_f32_16x16x32_bf16 v[42:45], v[146:149], v[226:229], v[42:45]
	v_mfma_f32_16x16x32_bf16 v[38:41], v[156:159], v[226:229], v[38:41]
	v_mfma_f32_16x16x32_bf16 v[34:37], v[160:163], v[226:229], v[34:37]
	v_lshl_add_u64 v[180:181], v[132:133], 0, s[36:37]
	global_load_dwordx2 v[194:195], v[180:181], off
	v_lshl_add_u64 v[180:181], v[132:133], 0, s[38:39]
	global_load_dwordx2 v[196:197], v[180:181], off
	v_mfma_f32_16x16x32_bf16 v[18:21], v[142:145], v[230:233], v[18:21]
	v_mfma_f32_16x16x32_bf16 v[22:25], v[146:149], v[230:233], v[22:25]
	v_mfma_f32_16x16x32_bf16 v[26:29], v[156:159], v[230:233], v[26:29]
	v_mfma_f32_16x16x32_bf16 v[30:33], v[160:163], v[230:233], v[30:33]
	v_lshl_add_u64 v[180:181], v[132:133], 0, s[40:41]
	global_load_dwordx2 v[198:199], v[180:181], off
	v_lshl_add_u64 v[180:181], v[132:133], 0, s[42:43]
	global_load_dwordx2 v[200:201], v[180:181], off
	v_mfma_f32_16x16x32_bf16 v[2:5], v[142:145], v[234:237], v[2:5]
	v_mfma_f32_16x16x32_bf16 v[6:9], v[146:149], v[234:237], v[6:9]
	v_mfma_f32_16x16x32_bf16 v[10:13], v[156:159], v[234:237], v[10:13]
	v_mfma_f32_16x16x32_bf16 v[14:17], v[160:163], v[234:237], v[14:17]
	s_waitcnt vmcnt(21)
	s_waitcnt lgkmcnt(0)
	s_barrier
; #define MD_GLDS_A(buf, tau) do { _Pragma("unroll") for (int i = 0; i < 5; ++i) if (amask & (1u << i)) \
;         __builtin_amdgcn_global_load_lds((const unsigned*)((const char*)HIDp + aoff[i] + (size_t)((tau) & 7) * 128), (PG8_LAS unsigned*)(MD_SA(buf) + wid * 1024 + i * 8192), 16, 0, 0); } while (0)
; #define MD_B_ISSUE(sb, tau) do { const char* kb_ = Bb + (size_t)((tau) >> 3) * 512 + (size_t)((tau) & 7) * (64 * (size_t)RB); _Pragma("unroll") for (int j = 0; j < 8; ++j) { const char* p_ = kb_ + (size_t)j * RB; \
;         asm volatile("global_load_dwordx2 %0, %1, off" : "=&v"(sb[j]) : "v"(p_) : "memory"); } } while (0)
; #define MD_B_WAIT(sb, N) asm volatile("s_waitcnt vmcnt(%8)" : "+v"(sb[0]), "+v"(sb[1]), "+v"(sb[2]), "+v"(sb[3]), "+v"(sb[4]), "+v"(sb[5]), "+v"(sb[6]), "+v"(sb[7]) : "n"(N) : "memory")
; __device__ __forceinline__ void moe_down_stream(PG8_LAS unsigned char* lds, int e, int cb0, int slot0, int nv, const bf16_t* HIDp, const float* Wd, bf16_t* Y, const float* slot_w, const int* slot_dst) {
;     ...
;     f32x4 acc[DNM][4];
; #pragma unroll
;     for (int m = 0; m < DNM; ++m)
; #pragma unroll
;         for (int n = 0; n < 4; ++n) acc[m][n] = (f32x4){0.f, 0.f, 0.f, 0.f};
;     f32x2 s0[8], s1[8];
;     MD_GLDS_A(0, 0); MD_B_ISSUE(s0, 0); MD_B_ISSUE(s1, 1);
;     MD_B_WAIT(s0, 8); MD_B_WRITE(s0, 0); __builtin_amdgcn_sched_barrier(0); MD_B_ISSUE(s0, 2);
;     asm volatile("s_waitcnt vmcnt(16)" ::: "memory");
;     asm volatile("s_waitcnt lgkmcnt(0)" ::: "memory"); __builtin_amdgcn_s_barrier(); asm volatile("" ::: "memory");
; #pragma unroll 1
;     for (int t = 0; t < NT; t += 2) {
;         if (t + 2 < NT) MD_B_WAIT(s1, 8); else MD_B_WAIT(s1, 0);
;         MD_B_WRITE(s1, 1); __builtin_amdgcn_sched_barrier(0); MD_GLDS_A(1, t + 1); __builtin_amdgcn_sched_barrier(0);
;         if (t + 3 < NT) MD_B_ISSUE(s1, t + 3);
;         MD_COMPUTE(0);
;         MD_END(t + 3 >= NT);
;         if (t + 2 < NT) { MD_B_WAIT(s0, 8); MD_B_WRITE(s0, 0); __builtin_amdgcn_sched_barrier(0); MD_GLDS_A(0, t + 2); __builtin_amdgcn_sched_barrier(0); }
;         if (t + 4 < NT) MD_B_ISSUE(s0, t + 4);
;         MD_COMPUTE(1);
;         MD_END(t + 4 >= NT);
	s_mov_b32 s49, s46
	s_mov_b32 s46, s47
	s_mov_b32 s47, s48
	s_mov_b32 s48, s49
	s_add_i32 s50, s50, 1
	v_cvt_pk_bf16_f32 v172, v202, v204
	v_cvt_pk_bf16_f32 v173, v206, v208
	v_cvt_pk_bf16_f32 v174, v210, v212
	v_cvt_pk_bf16_f32 v175, v214, v216
	v_cvt_pk_bf16_f32 v176, v203, v205
	v_cvt_pk_bf16_f32 v177, v207, v209
	v_cvt_pk_bf16_f32 v178, v211, v213
	v_cvt_pk_bf16_f32 v179, v215, v217
	ds_write_b128 v95, v[172:175] offset:19456
	ds_write_b128 v95, v[176:179] offset:19584
	v_add_u32_e32 v91, s46, v135
	v_add_u32_e32 v93, s46, v137
	ds_read_b128 v[238:241], v139 offset:0
	ds_read_b128 v[242:245], v139 offset:2048
	ds_read_b128 v[246:249], v139 offset:4096
	ds_read_b128 v[250:253], v139 offset:6144
	ds_read_b128 v[218:221], v91 offset:0
	ds_read_b128 v[222:225], v91 offset:2048
	ds_read_b128 v[226:229], v91 offset:4096
	ds_read_b128 v[230:233], v91 offset:6144
	ds_read_b128 v[234:237], v91 offset:8192
	s_add_i32 s49, s48, s74
	s_add_i32 s52, s52, 1
	s_and_b32 s54, s52, 7
	s_cmp_eq_u32 s54, 0
	s_cselect_b32 s54, s53, s32
	s_cselect_b32 s55, -1, 0
	s_add_u32 s30, s30, s54
	s_addc_u32 s31, s31, s55
	s_waitcnt lgkmcnt(0)
	v_mfma_f32_16x16x32_bf16 v[78:81], v[238:241], v[218:221], v[78:81]
	v_mfma_f32_16x16x32_bf16 v[74:77], v[242:245], v[218:221], v[74:77]
	v_mfma_f32_16x16x32_bf16 v[70:73], v[246:249], v[218:221], v[70:73]
	v_mfma_f32_16x16x32_bf16 v[66:69], v[250:253], v[218:221], v[66:69]
	ds_read_b128 v[218:221], v93 offset:0
	ds_read_b128 v[142:145], v141 offset:0
	s_mov_b32 m0, s49
	s_nop 0
	global_load_lds_dwordx4 v88, s[30:31]
	v_mfma_f32_16x16x32_bf16 v[62:65], v[238:241], v[222:225], v[62:65]
	v_mfma_f32_16x16x32_bf16 v[58:61], v[242:245], v[222:225], v[58:61]
	v_mfma_f32_16x16x32_bf16 v[54:57], v[246:249], v[222:225], v[54:57]
	v_mfma_f32_16x16x32_bf16 v[50:53], v[250:253], v[222:225], v[50:53]
	ds_read_b128 v[222:225], v93 offset:2048
	ds_read_b128 v[146:149], v141 offset:2048
	s_add_i32 m0, s49, 0x2000
	s_nop 0
	global_load_lds_dwordx4 v90, s[30:31]
	v_mfma_f32_16x16x32_bf16 v[46:49], v[238:241], v[226:229], v[46:49]
	v_mfma_f32_16x16x32_bf16 v[42:45], v[242:245], v[226:229], v[42:45]
	v_mfma_f32_16x16x32_bf16 v[38:41], v[246:249], v[226:229], v[38:41]
	v_mfma_f32_16x16x32_bf16 v[34:37], v[250:253], v[226:229], v[34:37]
	ds_read_b128 v[226:229], v93 offset:4096
	ds_read_b128 v[156:159], v141 offset:4096
	s_add_i32 m0, s49, 0x4000
	s_nop 0
	global_load_lds_dwordx4 v92, s[30:31]
	v_mfma_f32_16x16x32_bf16 v[18:21], v[238:241], v[230:233], v[18:21]
	v_mfma_f32_16x16x32_bf16 v[22:25], v[242:245], v[230:233], v[22:25]
	v_mfma_f32_16x16x32_bf16 v[26:29], v[246:249], v[230:233], v[26:29]
	v_mfma_f32_16x16x32_bf16 v[30:33], v[250:253], v[230:233], v[30:33]
	ds_read_b128 v[230:233], v93 offset:6144
	ds_read_b128 v[160:163], v141 offset:6144
	s_add_i32 m0, s49, 0x6000
	s_nop 0
	global_load_lds_dwordx4 v94, s[30:31]
	v_mfma_f32_16x16x32_bf16 v[2:5], v[238:241], v[234:237], v[2:5]
	v_mfma_f32_16x16x32_bf16 v[6:9], v[242:245], v[234:237], v[6:9]
	v_mfma_f32_16x16x32_bf16 v[10:13], v[246:249], v[234:237], v[10:13]
	v_mfma_f32_16x16x32_bf16 v[14:17], v[250:253], v[234:237], v[14:17]
	ds_read_b128 v[234:237], v93 offset:8192
	s_add_i32 m0, s49, 0x8000
	s_nop 0
	global_load_lds_dwordx4 v96, s[30:31]
	s_waitcnt lgkmcnt(0)
	v_mfma_f32_16x16x32_bf16 v[78:81], v[142:145], v[218:221], v[78:81]
	v_mfma_f32_16x16x32_bf16 v[74:77], v[146:149], v[218:221], v[74:77]
	v_mfma_f32_16x16x32_bf16 v[70:73], v[156:159], v[218:221], v[70:73]
	v_mfma_f32_16x16x32_bf16 v[66:69], v[160:163], v[218:221], v[66:69]
	s_add_i32 s51, s51, 1
	s_and_b32 s54, s51, 7
	s_cmp_eq_u32 s54, 0
	s_cselect_b32 s44, s34, s35
	s_cselect_b32 s45, -1, 0
	v_lshl_add_u64 v[132:133], v[132:133], 0, s[44:45]
	global_load_dwordx2 v[202:203], v[132:133], off
	v_lshl_add_u64 v[180:181], v[132:133], 0, s[24:25]
	global_load_dwordx2 v[204:205], v[180:181], off
	v_mfma_f32_16x16x32_bf16 v[62:65], v[142:145], v[222:225], v[62:65]
	v_mfma_f32_16x16x32_bf16 v[58:61], v[146:149], v[222:225], v[58:61]
	v_mfma_f32_16x16x32_bf16 v[54:57], v[156:159], v[222:225], v[54:57]
	v_mfma_f32_16x16x32_bf16 v[50:53], v[160:163], v[222:225], v[50:53]
	v_lshl_add_u64 v[180:181], v[132:133], 0, s[26:27]
	global_load_dwordx2 v[206:207], v[180:181], off
	v_lshl_add_u64 v[180:181], v[132:133], 0, s[28:29]
	global_load_dwordx2 v[208:209], v[180:181], off
	v_mfma_f32_16x16x32_bf16 v[46:49], v[142:145], v[226:229], v[46:49]
	v_mfma_f32_16x16x32_bf16 v[42:45], v[146:149], v[226:229], v[42:45]
	v_mfma_f32_16x16x32_bf16 v[38:41], v[156:159], v[226:229], v[38:41]
	v_mfma_f32_16x16x32_bf16 v[34:37], v[160:163], v[226:229], v[34:37]
	v_lshl_add_u64 v[180:181], v[132:133], 0, s[36:37]
	global_load_dwordx2 v[210:211], v[180:181], off
	v_lshl_add_u64 v[180:181], v[132:133], 0, s[38:39]
	global_load_dwordx2 v[212:213], v[180:181], off
	v_mfma_f32_16x16x32_bf16 v[18:21], v[142:145], v[230:233], v[18:21]
	v_mfma_f32_16x16x32_bf16 v[22:25], v[146:149], v[230:233], v[22:25]
	v_mfma_f32_16x16x32_bf16 v[26:29], v[156:159], v[230:233], v[26:29]
	v_mfma_f32_16x16x32_bf16 v[30:33], v[160:163], v[230:233], v[30:33]
	v_lshl_add_u64 v[180:181], v[132:133], 0, s[40:41]
	global_load_dwordx2 v[214:215], v[180:181], off
	v_lshl_add_u64 v[180:181], v[132:133], 0, s[42:43]
	global_load_dwordx2 v[216:217], v[180:181], off
	v_mfma_f32_16x16x32_bf16 v[2:5], v[142:145], v[234:237], v[2:5]
	v_mfma_f32_16x16x32_bf16 v[6:9], v[146:149], v[234:237], v[6:9]
	v_mfma_f32_16x16x32_bf16 v[10:13], v[156:159], v[234:237], v[10:13]
	v_mfma_f32_16x16x32_bf16 v[14:17], v[160:163], v[234:237], v[14:17]
	s_waitcnt vmcnt(21)
	s_waitcnt lgkmcnt(0)
	s_barrier
; #define MD_GLDS_A(buf, tau) do { _Pragma("unroll") for (int i = 0; i < 5; ++i) if (amask & (1u << i)) \
;         __builtin_amdgcn_global_load_lds((const unsigned*)((const char*)HIDp + aoff[i] + (size_t)((tau) & 7) * 128), (PG8_LAS unsigned*)(MD_SA(buf) + wid * 1024 + i * 8192), 16, 0, 0); } while (0)
; #define MD_B_ISSUE(sb, tau) do { const char* kb_ = Bb + (size_t)((tau) >> 3) * 512 + (size_t)((tau) & 7) * (64 * (size_t)RB); _Pragma("unroll") for (int j = 0; j < 8; ++j) { const char* p_ = kb_ + (size_t)j * RB; \
;         asm volatile("global_load_dwordx2 %0, %1, off" : "=&v"(sb[j]) : "v"(p_) : "memory"); } } while (0)
; #define MD_B_WAIT(sb, N) asm volatile("s_waitcnt vmcnt(%8)" : "+v"(sb[0]), "+v"(sb[1]), "+v"(sb[2]), "+v"(sb[3]), "+v"(sb[4]), "+v"(sb[5]), "+v"(sb[6]), "+v"(sb[7]) : "n"(N) : "memory")
; __device__ __forceinline__ void moe_down_stream(PG8_LAS unsigned char* lds, int e, int cb0, int slot0, int nv, const bf16_t* HIDp, const float* Wd, bf16_t* Y, const float* slot_w, const int* slot_dst) {
;     ...
;     f32x4 acc[DNM][4];
; #pragma unroll
;     for (int m = 0; m < DNM; ++m)
; #pragma unroll
;         for (int n = 0; n < 4; ++n) acc[m][n] = (f32x4){0.f, 0.f, 0.f, 0.f};
;     f32x2 s0[8], s1[8];
;     MD_GLDS_A(0, 0); MD_B_ISSUE(s0, 0); MD_B_ISSUE(s1, 1);
;     MD_B_WAIT(s0, 8); MD_B_WRITE(s0, 0); __builtin_amdgcn_sched_barrier(0); MD_B_ISSUE(s0, 2);
;     asm volatile("s_waitcnt vmcnt(16)" ::: "memory");
;     asm volatile("s_waitcnt lgkmcnt(0)" ::: "memory"); __builtin_amdgcn_s_barrier(); asm volatile("" ::: "memory");
; #pragma unroll 1
;     for (int t = 0; t < NT; t += 2) {
;         if (t + 2 < NT) MD_B_WAIT(s1, 8); else MD_B_WAIT(s1, 0);
;         MD_B_WRITE(s1, 1); __builtin_amdgcn_sched_barrier(0); MD_GLDS_A(1, t + 1); __builtin_amdgcn_sched_barrier(0);
;         if (t + 3 < NT) MD_B_ISSUE(s1, t + 3);
;         MD_COMPUTE(0);
;         MD_END(t + 3 >= NT);
;         if (t + 2 < NT) { MD_B_WAIT(s0, 8); MD_B_WRITE(s0, 0); __builtin_amdgcn_sched_barrier(0); MD_GLDS_A(0, t + 2); __builtin_amdgcn_sched_barrier(0); }
;         if (t + 4 < NT) MD_B_ISSUE(s0, t + 4);
;         MD_COMPUTE(1);
;         MD_END(t + 4 >= NT);
	s_mov_b32 s49, s46
	s_mov_b32 s46, s47
	s_mov_b32 s47, s48
	s_mov_b32 s48, s49
	s_add_i32 s50, s50, 1
	v_cvt_pk_bf16_f32 v172, v98, v100
	v_cvt_pk_bf16_f32 v173, v102, v104
	v_cvt_pk_bf16_f32 v174, v106, v108
	v_cvt_pk_bf16_f32 v175, v110, v112
	v_cvt_pk_bf16_f32 v176, v99, v101
	v_cvt_pk_bf16_f32 v177, v103, v105
	v_cvt_pk_bf16_f32 v178, v107, v109
	v_cvt_pk_bf16_f32 v179, v111, v113
	ds_write_b128 v95, v[172:175] offset:0
	ds_write_b128 v95, v[176:179] offset:128
	v_add_u32_e32 v91, s46, v135
	v_add_u32_e32 v93, s46, v137
	ds_read_b128 v[238:241], v139 offset:19456
	ds_read_b128 v[242:245], v139 offset:21504
	ds_read_b128 v[246:249], v139 offset:23552
	ds_read_b128 v[250:253], v139 offset:25600
	ds_read_b128 v[218:221], v91 offset:0
	ds_read_b128 v[222:225], v91 offset:2048
	ds_read_b128 v[226:229], v91 offset:4096
	ds_read_b128 v[230:233], v91 offset:6144
	ds_read_b128 v[234:237], v91 offset:8192
	s_add_i32 s49, s48, s74
	s_add_i32 s52, s52, 1
	s_and_b32 s54, s52, 7
	s_cmp_eq_u32 s54, 0
	s_cselect_b32 s54, s53, s32
	s_cselect_b32 s55, -1, 0
	s_add_u32 s30, s30, s54
	s_addc_u32 s31, s31, s55
	s_waitcnt lgkmcnt(0)
	v_mfma_f32_16x16x32_bf16 v[78:81], v[238:241], v[218:221], v[78:81]
	v_mfma_f32_16x16x32_bf16 v[74:77], v[242:245], v[218:221], v[74:77]
	v_mfma_f32_16x16x32_bf16 v[70:73], v[246:249], v[218:221], v[70:73]
	v_mfma_f32_16x16x32_bf16 v[66:69], v[250:253], v[218:221], v[66:69]
	ds_read_b128 v[218:221], v93 offset:0
	ds_read_b128 v[142:145], v141 offset:19456
	s_mov_b32 m0, s49
	s_nop 0
	global_load_lds_dwordx4 v88, s[30:31]
	v_mfma_f32_16x16x32_bf16 v[62:65], v[238:241], v[222:225], v[62:65]
	v_mfma_f32_16x16x32_bf16 v[58:61], v[242:245], v[222:225], v[58:61]
	v_mfma_f32_16x16x32_bf16 v[54:57], v[246:249], v[222:225], v[54:57]
	v_mfma_f32_16x16x32_bf16 v[50:53], v[250:253], v[222:225], v[50:53]
	ds_read_b128 v[222:225], v93 offset:2048
	ds_read_b128 v[146:149], v141 offset:21504
	s_add_i32 m0, s49, 0x2000
	s_nop 0
	global_load_lds_dwordx4 v90, s[30:31]
	v_mfma_f32_16x16x32_bf16 v[46:49], v[238:241], v[226:229], v[46:49]
	v_mfma_f32_16x16x32_bf16 v[42:45], v[242:245], v[226:229], v[42:45]
	v_mfma_f32_16x16x32_bf16 v[38:41], v[246:249], v[226:229], v[38:41]
	v_mfma_f32_16x16x32_bf16 v[34:37], v[250:253], v[226:229], v[34:37]
	ds_read_b128 v[226:229], v93 offset:4096
	ds_read_b128 v[156:159], v141 offset:23552
	s_add_i32 m0, s49, 0x4000
	s_nop 0
	global_load_lds_dwordx4 v92, s[30:31]
	v_mfma_f32_16x16x32_bf16 v[18:21], v[238:241], v[230:233], v[18:21]
	v_mfma_f32_16x16x32_bf16 v[22:25], v[242:245], v[230:233], v[22:25]
	v_mfma_f32_16x16x32_bf16 v[26:29], v[246:249], v[230:233], v[26:29]
	v_mfma_f32_16x16x32_bf16 v[30:33], v[250:253], v[230:233], v[30:33]
	ds_read_b128 v[230:233], v93 offset:6144
	ds_read_b128 v[160:163], v141 offset:25600
	s_add_i32 m0, s49, 0x6000
	s_nop 0
	global_load_lds_dwordx4 v94, s[30:31]
	v_mfma_f32_16x16x32_bf16 v[2:5], v[238:241], v[234:237], v[2:5]
	v_mfma_f32_16x16x32_bf16 v[6:9], v[242:245], v[234:237], v[6:9]
	v_mfma_f32_16x16x32_bf16 v[10:13], v[246:249], v[234:237], v[10:13]
	v_mfma_f32_16x16x32_bf16 v[14:17], v[250:253], v[234:237], v[14:17]
	ds_read_b128 v[234:237], v93 offset:8192
	s_add_i32 m0, s49, 0x8000
	s_nop 0
	global_load_lds_dwordx4 v96, s[30:31]
	s_waitcnt lgkmcnt(0)
	v_mfma_f32_16x16x32_bf16 v[78:81], v[142:145], v[218:221], v[78:81]
	v_mfma_f32_16x16x32_bf16 v[74:77], v[146:149], v[218:221], v[74:77]
	v_mfma_f32_16x16x32_bf16 v[70:73], v[156:159], v[218:221], v[70:73]
	v_mfma_f32_16x16x32_bf16 v[66:69], v[160:163], v[218:221], v[66:69]
	s_add_i32 s51, s51, 1
	s_and_b32 s54, s51, 7
	s_cmp_eq_u32 s54, 0
	s_cselect_b32 s44, s34, s35
	s_cselect_b32 s45, -1, 0
	v_lshl_add_u64 v[132:133], v[132:133], 0, s[44:45]
	global_load_dwordx2 v[98:99], v[132:133], off
	v_lshl_add_u64 v[180:181], v[132:133], 0, s[24:25]
	global_load_dwordx2 v[100:101], v[180:181], off
	v_mfma_f32_16x16x32_bf16 v[62:65], v[142:145], v[222:225], v[62:65]
	v_mfma_f32_16x16x32_bf16 v[58:61], v[146:149], v[222:225], v[58:61]
	v_mfma_f32_16x16x32_bf16 v[54:57], v[156:159], v[222:225], v[54:57]
	v_mfma_f32_16x16x32_bf16 v[50:53], v[160:163], v[222:225], v[50:53]
	v_lshl_add_u64 v[180:181], v[132:133], 0, s[26:27]
	global_load_dwordx2 v[102:103], v[180:181], off
	v_lshl_add_u64 v[180:181], v[132:133], 0, s[28:29]
	global_load_dwordx2 v[104:105], v[180:181], off
	v_mfma_f32_16x16x32_bf16 v[46:49], v[142:145], v[226:229], v[46:49]
	v_mfma_f32_16x16x32_bf16 v[42:45], v[146:149], v[226:229], v[42:45]
	v_mfma_f32_16x16x32_bf16 v[38:41], v[156:159], v[226:229], v[38:41]
	v_mfma_f32_16x16x32_bf16 v[34:37], v[160:163], v[226:229], v[34:37]
	v_lshl_add_u64 v[180:181], v[132:133], 0, s[36:37]
	global_load_dwordx2 v[106:107], v[180:181], off
	v_lshl_add_u64 v[180:181], v[132:133], 0, s[38:39]
	global_load_dwordx2 v[108:109], v[180:181], off
	v_mfma_f32_16x16x32_bf16 v[18:21], v[142:145], v[230:233], v[18:21]
	v_mfma_f32_16x16x32_bf16 v[22:25], v[146:149], v[230:233], v[22:25]
	v_mfma_f32_16x16x32_bf16 v[26:29], v[156:159], v[230:233], v[26:29]
	v_mfma_f32_16x16x32_bf16 v[30:33], v[160:163], v[230:233], v[30:33]
	v_lshl_add_u64 v[180:181], v[132:133], 0, s[40:41]
	global_load_dwordx2 v[110:111], v[180:181], off
	v_lshl_add_u64 v[180:181], v[132:133], 0, s[42:43]
	global_load_dwordx2 v[112:113], v[180:181], off
	v_mfma_f32_16x16x32_bf16 v[2:5], v[142:145], v[234:237], v[2:5]
	v_mfma_f32_16x16x32_bf16 v[6:9], v[146:149], v[234:237], v[6:9]
	v_mfma_f32_16x16x32_bf16 v[10:13], v[156:159], v[234:237], v[10:13]
	v_mfma_f32_16x16x32_bf16 v[14:17], v[160:163], v[234:237], v[14:17]
	s_waitcnt vmcnt(21)
	s_waitcnt lgkmcnt(0)
	s_barrier
; #define PG8_LAS __attribute__((address_space(3)))
; __device__ __forceinline__ unsigned cvtpk(float lo, float hi) { f32x2 v = {lo, hi}; bf16x2_t b = __builtin_convertvector(v, bf16x2_t); return __builtin_bit_cast(unsigned, b); }
; __device__ __forceinline__ void moe_down_stream(PG8_LAS unsigned char* lds, int e, int cb0, int slot0, int nv, const bf16_t* HIDp, const float* Wd, bf16_t* Y, const float* slot_w, const int* slot_dst) {
;     ...
;         if (((t + 1) & 7) == 7) {
;             const int cb = cb0 + ((t + 1) >> 3);
; #pragma unroll
;             for (int m = 0; m < DNM; ++m) {
;                 const float w_ = lw[4 * (16 * m + fr) + wr];
; #pragma unroll
;                 for (int p = 0; p < 2; ++p) { const f32x4 v0 = acc[m][2 * p] * w_, v1 = acc[m][2 * p + 1] * w_; u32x4 w; w.x = cvtpk(v0[0], v0[1]); w.y = cvtpk(v0[2], v0[3]); w.z = cvtpk(v1[0], v1[1]); w.w = cvtpk(v1[2], v1[3]);
;                     *(PG8_LAS u32x4*)(stg + fr * 128 + (((4 * p + fq) ^ (fr & 7)) * 16)) = w; }
; #pragma unroll
;                 for (int hh = 0; hh < 2; ++hh) { const int r = (lane >> 3) + 8 * hh, cc = lane & 7; const u32x4 d = *(const PG8_LAS u32x4*)(stg + r * 128 + ((cc ^ (r & 7)) * 16)); const int dst_ = ldst[4 * (16 * m + r) + wr];
;                     if (dst_ >= 0) *(u32x4*)(Y + (size_t)dst_ * D + 128 * cb + 64 * wc + 8 * cc) = d; }
; #pragma unroll
;                 for (int n = 0; n < 4; ++n) acc[m][n] = (f32x4){0.f, 0.f, 0.f, 0.f}; } }
	s_mov_b32 s49, s46
	s_mov_b32 s46, s47
	s_mov_b32 s47, s48
	s_mov_b32 s48, s49
	s_add_i32 s50, s50, 1
	s_and_b32 s54, s50, 7
	s_cmp_lg_u32 s54, 0
	s_cbranch_scc1 .Lmd_noepi_X
	s_add_i32 s54, s48, s74
	v_add_u32_e32 v164, s54, v84
	v_add_u32_e32 v165, s54, v85
	ds_read_b32 v150, v82 offset:0
	ds_read_b32 v151, v83 offset:0
	ds_read_b32 v166, v83 offset:128
	s_waitcnt lgkmcnt(2)
	v_mul_f32_e32 v78, v150, v78
	v_mul_f32_e32 v79, v150, v79
	v_mul_f32_e32 v80, v150, v80
	v_mul_f32_e32 v81, v150, v81
	v_mul_f32_e32 v74, v150, v74
	v_mul_f32_e32 v75, v150, v75
	v_mul_f32_e32 v76, v150, v76
	v_mul_f32_e32 v77, v150, v77
	v_cvt_pk_bf16_f32 v182, v78, v79
	v_cvt_pk_bf16_f32 v183, v80, v81
	v_cvt_pk_bf16_f32 v184, v74, v75
	v_cvt_pk_bf16_f32 v185, v76, v77
	ds_write_b128 v164, v[182:185]
	v_mul_f32_e32 v70, v150, v70
	v_mul_f32_e32 v71, v150, v71
	v_mul_f32_e32 v72, v150, v72
	v_mul_f32_e32 v73, v150, v73
	v_mul_f32_e32 v66, v150, v66
	v_mul_f32_e32 v67, v150, v67
	v_mul_f32_e32 v68, v150, v68
	v_mul_f32_e32 v69, v150, v69
	v_cvt_pk_bf16_f32 v182, v70, v71
	v_cvt_pk_bf16_f32 v183, v72, v73
	v_cvt_pk_bf16_f32 v184, v66, v67
	v_cvt_pk_bf16_f32 v185, v68, v69
	v_xor_b32_e32 v167, 64, v164
	ds_write_b128 v167, v[182:185]
	v_mov_b32_e32 v78, 0
	v_mov_b32_e32 v74, 0
	v_mov_b32_e32 v70, 0
	v_mov_b32_e32 v66, 0
	v_mov_b32_e32 v79, 0
	v_mov_b32_e32 v75, 0
	v_mov_b32_e32 v71, 0
	v_mov_b32_e32 v67, 0
	v_mov_b32_e32 v80, 0
	v_mov_b32_e32 v76, 0
	v_mov_b32_e32 v72, 0
	v_mov_b32_e32 v68, 0
	v_mov_b32_e32 v81, 0
	v_mov_b32_e32 v77, 0
	v_mov_b32_e32 v73, 0
	v_mov_b32_e32 v69, 0
	ds_read_b128 v[182:185], v165 offset:0
	v_cmp_lt_i32_e32 vcc, -1, v151
	v_lshlrev_b32_e32 v148, 13, v151
	v_mov_b32_e32 v149, 0
	v_lshl_add_u64 v[148:149], v[148:149], 0, v[86:87]
	v_cndmask_b32_e32 v148, v168, v148, vcc
	v_cndmask_b32_e32 v149, v169, v149, vcc
	s_waitcnt lgkmcnt(0)
	global_store_dwordx4 v[148:149], v[182:185], off nt
	ds_read_b128 v[182:185], v165 offset:8192
	v_cmp_lt_i32_e32 vcc, -1, v166
	v_lshlrev_b32_e32 v148, 13, v166
	v_mov_b32_e32 v149, 0
	v_lshl_add_u64 v[148:149], v[148:149], 0, v[86:87]
	v_cndmask_b32_e32 v148, v168, v148, vcc
	v_cndmask_b32_e32 v149, v169, v149, vcc
	s_waitcnt lgkmcnt(0)
	global_store_dwordx4 v[148:149], v[182:185], off nt
	ds_read_b32 v150, v82 offset:256
	ds_read_b32 v151, v83 offset:256
	ds_read_b32 v166, v83 offset:384
	s_waitcnt lgkmcnt(2)
	v_mul_f32_e32 v62, v150, v62
	v_mul_f32_e32 v63, v150, v63
	v_mul_f32_e32 v64, v150, v64
	v_mul_f32_e32 v65, v150, v65
	v_mul_f32_e32 v58, v150, v58
	v_mul_f32_e32 v59, v150, v59
	v_mul_f32_e32 v60, v150, v60
	v_mul_f32_e32 v61, v150, v61
	v_cvt_pk_bf16_f32 v182, v62, v63
	v_cvt_pk_bf16_f32 v183, v64, v65
	v_cvt_pk_bf16_f32 v184, v58, v59
	v_cvt_pk_bf16_f32 v185, v60, v61
	ds_write_b128 v164, v[182:185]
	v_mul_f32_e32 v54, v150, v54
	v_mul_f32_e32 v55, v150, v55
	v_mul_f32_e32 v56, v150, v56
	v_mul_f32_e32 v57, v150, v57
	v_mul_f32_e32 v50, v150, v50
	v_mul_f32_e32 v51, v150, v51
	v_mul_f32_e32 v52, v150, v52
	v_mul_f32_e32 v53, v150, v53
	v_cvt_pk_bf16_f32 v182, v54, v55
	v_cvt_pk_bf16_f32 v183, v56, v57
	v_cvt_pk_bf16_f32 v184, v50, v51
	v_cvt_pk_bf16_f32 v185, v52, v53
	v_xor_b32_e32 v167, 64, v164
	ds_write_b128 v167, v[182:185]
	v_mov_b32_e32 v62, 0
	v_mov_b32_e32 v58, 0
	v_mov_b32_e32 v54, 0
	v_mov_b32_e32 v50, 0
	v_mov_b32_e32 v63, 0
	v_mov_b32_e32 v59, 0
	v_mov_b32_e32 v55, 0
	v_mov_b32_e32 v51, 0
	v_mov_b32_e32 v64, 0
	v_mov_b32_e32 v60, 0
	v_mov_b32_e32 v56, 0
	v_mov_b32_e32 v52, 0
	v_mov_b32_e32 v65, 0
	v_mov_b32_e32 v61, 0
	v_mov_b32_e32 v57, 0
	v_mov_b32_e32 v53, 0
	ds_read_b128 v[182:185], v165 offset:0
	v_cmp_lt_i32_e32 vcc, -1, v151
	v_lshlrev_b32_e32 v148, 13, v151
	v_mov_b32_e32 v149, 0
	v_lshl_add_u64 v[148:149], v[148:149], 0, v[86:87]
	v_cndmask_b32_e32 v148, v168, v148, vcc
	v_cndmask_b32_e32 v149, v169, v149, vcc
	s_waitcnt lgkmcnt(0)
	global_store_dwordx4 v[148:149], v[182:185], off nt
	ds_read_b128 v[182:185], v165 offset:8192
	v_cmp_lt_i32_e32 vcc, -1, v166
	v_lshlrev_b32_e32 v148, 13, v166
	v_mov_b32_e32 v149, 0
	v_lshl_add_u64 v[148:149], v[148:149], 0, v[86:87]
	v_cndmask_b32_e32 v148, v168, v148, vcc
	v_cndmask_b32_e32 v149, v169, v149, vcc
	s_waitcnt lgkmcnt(0)
	global_store_dwordx4 v[148:149], v[182:185], off nt
	ds_read_b32 v150, v82 offset:512
	ds_read_b32 v151, v83 offset:512
	ds_read_b32 v166, v83 offset:640
	s_waitcnt lgkmcnt(2)
	v_mul_f32_e32 v46, v150, v46
	v_mul_f32_e32 v47, v150, v47
	v_mul_f32_e32 v48, v150, v48
	v_mul_f32_e32 v49, v150, v49
	v_mul_f32_e32 v42, v150, v42
	v_mul_f32_e32 v43, v150, v43
	v_mul_f32_e32 v44, v150, v44
	v_mul_f32_e32 v45, v150, v45
	v_cvt_pk_bf16_f32 v182, v46, v47
	v_cvt_pk_bf16_f32 v183, v48, v49
	v_cvt_pk_bf16_f32 v184, v42, v43
	v_cvt_pk_bf16_f32 v185, v44, v45
	ds_write_b128 v164, v[182:185]
	v_mul_f32_e32 v38, v150, v38
	v_mul_f32_e32 v39, v150, v39
	v_mul_f32_e32 v40, v150, v40
	v_mul_f32_e32 v41, v150, v41
	v_mul_f32_e32 v34, v150, v34
	v_mul_f32_e32 v35, v150, v35
	v_mul_f32_e32 v36, v150, v36
	v_mul_f32_e32 v37, v150, v37
	v_cvt_pk_bf16_f32 v182, v38, v39
	v_cvt_pk_bf16_f32 v183, v40, v41
	v_cvt_pk_bf16_f32 v184, v34, v35
	v_cvt_pk_bf16_f32 v185, v36, v37
	v_xor_b32_e32 v167, 64, v164
	ds_write_b128 v167, v[182:185]
	v_mov_b32_e32 v46, 0
	v_mov_b32_e32 v42, 0
	v_mov_b32_e32 v38, 0
	v_mov_b32_e32 v34, 0
	v_mov_b32_e32 v47, 0
	v_mov_b32_e32 v43, 0
	v_mov_b32_e32 v39, 0
	v_mov_b32_e32 v35, 0
	v_mov_b32_e32 v48, 0
	v_mov_b32_e32 v44, 0
	v_mov_b32_e32 v40, 0
	v_mov_b32_e32 v36, 0
	v_mov_b32_e32 v49, 0
	v_mov_b32_e32 v45, 0
	v_mov_b32_e32 v41, 0
	v_mov_b32_e32 v37, 0
	ds_read_b128 v[182:185], v165 offset:0
	v_cmp_lt_i32_e32 vcc, -1, v151
	v_lshlrev_b32_e32 v148, 13, v151
	v_mov_b32_e32 v149, 0
	v_lshl_add_u64 v[148:149], v[148:149], 0, v[86:87]
	v_cndmask_b32_e32 v148, v168, v148, vcc
	v_cndmask_b32_e32 v149, v169, v149, vcc
	s_waitcnt lgkmcnt(0)
; #define PG8_LAS __attribute__((address_space(3)))
; __device__ __forceinline__ unsigned cvtpk(float lo, float hi) { f32x2 v = {lo, hi}; bf16x2_t b = __builtin_convertvector(v, bf16x2_t); return __builtin_bit_cast(unsigned, b); }
; __device__ __forceinline__ void moe_down_stream(PG8_LAS unsigned char* lds, int e, int cb0, int slot0, int nv, const bf16_t* HIDp, const float* Wd, bf16_t* Y, const float* slot_w, const int* slot_dst) {
;     ...
;         if (((t + 1) & 7) == 7) {
;             const int cb = cb0 + ((t + 1) >> 3);
; #pragma unroll
;             for (int m = 0; m < DNM; ++m) {
;                 const float w_ = lw[4 * (16 * m + fr) + wr];
; #pragma unroll
;                 for (int p = 0; p < 2; ++p) { const f32x4 v0 = acc[m][2 * p] * w_, v1 = acc[m][2 * p + 1] * w_; u32x4 w; w.x = cvtpk(v0[0], v0[1]); w.y = cvtpk(v0[2], v0[3]); w.z = cvtpk(v1[0], v1[1]); w.w = cvtpk(v1[2], v1[3]);
;                     *(PG8_LAS u32x4*)(stg + fr * 128 + (((4 * p + fq) ^ (fr & 7)) * 16)) = w; }
; #pragma unroll
;                 for (int hh = 0; hh < 2; ++hh) { const int r = (lane >> 3) + 8 * hh, cc = lane & 7; const u32x4 d = *(const PG8_LAS u32x4*)(stg + r * 128 + ((cc ^ (r & 7)) * 16)); const int dst_ = ldst[4 * (16 * m + r) + wr];
;                     if (dst_ >= 0) *(u32x4*)(Y + (size_t)dst_ * D + 128 * cb + 64 * wc + 8 * cc) = d; }
; #pragma unroll
;                 for (int n = 0; n < 4; ++n) acc[m][n] = (f32x4){0.f, 0.f, 0.f, 0.f}; } }
	global_store_dwordx4 v[148:149], v[182:185], off nt
	ds_read_b128 v[182:185], v165 offset:8192
	v_cmp_lt_i32_e32 vcc, -1, v166
	v_lshlrev_b32_e32 v148, 13, v166
	v_mov_b32_e32 v149, 0
	v_lshl_add_u64 v[148:149], v[148:149], 0, v[86:87]
	v_cndmask_b32_e32 v148, v168, v148, vcc
	v_cndmask_b32_e32 v149, v169, v149, vcc
	s_waitcnt lgkmcnt(0)
	global_store_dwordx4 v[148:149], v[182:185], off nt
	ds_read_b32 v150, v82 offset:768
	ds_read_b32 v151, v83 offset:768
	ds_read_b32 v166, v83 offset:896
	s_waitcnt lgkmcnt(2)
	v_mul_f32_e32 v18, v150, v18
	v_mul_f32_e32 v19, v150, v19
	v_mul_f32_e32 v20, v150, v20
	v_mul_f32_e32 v21, v150, v21
	v_mul_f32_e32 v22, v150, v22
	v_mul_f32_e32 v23, v150, v23
	v_mul_f32_e32 v24, v150, v24
	v_mul_f32_e32 v25, v150, v25
	v_cvt_pk_bf16_f32 v182, v18, v19
	v_cvt_pk_bf16_f32 v183, v20, v21
	v_cvt_pk_bf16_f32 v184, v22, v23
	v_cvt_pk_bf16_f32 v185, v24, v25
	ds_write_b128 v164, v[182:185]
	v_mul_f32_e32 v26, v150, v26
	v_mul_f32_e32 v27, v150, v27
	v_mul_f32_e32 v28, v150, v28
	v_mul_f32_e32 v29, v150, v29
	v_mul_f32_e32 v30, v150, v30
	v_mul_f32_e32 v31, v150, v31
	v_mul_f32_e32 v32, v150, v32
	v_mul_f32_e32 v33, v150, v33
	v_cvt_pk_bf16_f32 v182, v26, v27
	v_cvt_pk_bf16_f32 v183, v28, v29
	v_cvt_pk_bf16_f32 v184, v30, v31
	v_cvt_pk_bf16_f32 v185, v32, v33
	v_xor_b32_e32 v167, 64, v164
	ds_write_b128 v167, v[182:185]
	v_mov_b32_e32 v18, 0
	v_mov_b32_e32 v22, 0
	v_mov_b32_e32 v26, 0
	v_mov_b32_e32 v30, 0
	v_mov_b32_e32 v19, 0
	v_mov_b32_e32 v23, 0
	v_mov_b32_e32 v27, 0
	v_mov_b32_e32 v31, 0
	v_mov_b32_e32 v20, 0
	v_mov_b32_e32 v24, 0
	v_mov_b32_e32 v28, 0
	v_mov_b32_e32 v32, 0
	v_mov_b32_e32 v21, 0
	v_mov_b32_e32 v25, 0
	v_mov_b32_e32 v29, 0
	v_mov_b32_e32 v33, 0
	ds_read_b128 v[182:185], v165 offset:0
	v_cmp_lt_i32_e32 vcc, -1, v151
	v_lshlrev_b32_e32 v148, 13, v151
	v_mov_b32_e32 v149, 0
	v_lshl_add_u64 v[148:149], v[148:149], 0, v[86:87]
	v_cndmask_b32_e32 v148, v168, v148, vcc
	v_cndmask_b32_e32 v149, v169, v149, vcc
	s_waitcnt lgkmcnt(0)
	global_store_dwordx4 v[148:149], v[182:185], off nt
	ds_read_b128 v[182:185], v165 offset:8192
	v_cmp_lt_i32_e32 vcc, -1, v166
	v_lshlrev_b32_e32 v148, 13, v166
	v_mov_b32_e32 v149, 0
	v_lshl_add_u64 v[148:149], v[148:149], 0, v[86:87]
	v_cndmask_b32_e32 v148, v168, v148, vcc
	v_cndmask_b32_e32 v149, v169, v149, vcc
	s_waitcnt lgkmcnt(0)
	global_store_dwordx4 v[148:149], v[182:185], off nt
	ds_read_b32 v150, v82 offset:1024
	ds_read_b32 v151, v83 offset:1024
	ds_read_b32 v166, v83 offset:1152
	s_waitcnt lgkmcnt(2)
	v_mul_f32_e32 v2, v150, v2
	v_mul_f32_e32 v3, v150, v3
	v_mul_f32_e32 v4, v150, v4
	v_mul_f32_e32 v5, v150, v5
	v_mul_f32_e32 v6, v150, v6
	v_mul_f32_e32 v7, v150, v7
	v_mul_f32_e32 v8, v150, v8
	v_mul_f32_e32 v9, v150, v9
	v_cvt_pk_bf16_f32 v182, v2, v3
	v_cvt_pk_bf16_f32 v183, v4, v5
	v_cvt_pk_bf16_f32 v184, v6, v7
	v_cvt_pk_bf16_f32 v185, v8, v9
	ds_write_b128 v164, v[182:185]
	v_mul_f32_e32 v10, v150, v10
	v_mul_f32_e32 v11, v150, v11
	v_mul_f32_e32 v12, v150, v12
	v_mul_f32_e32 v13, v150, v13
	v_mul_f32_e32 v14, v150, v14
	v_mul_f32_e32 v15, v150, v15
	v_mul_f32_e32 v16, v150, v16
	v_mul_f32_e32 v17, v150, v17
	v_cvt_pk_bf16_f32 v182, v10, v11
	v_cvt_pk_bf16_f32 v183, v12, v13
	v_cvt_pk_bf16_f32 v184, v14, v15
	v_cvt_pk_bf16_f32 v185, v16, v17
	v_xor_b32_e32 v167, 64, v164
	ds_write_b128 v167, v[182:185]
	v_mov_b32_e32 v2, 0
	v_mov_b32_e32 v6, 0
	v_mov_b32_e32 v10, 0
	v_mov_b32_e32 v14, 0
	v_mov_b32_e32 v3, 0
	v_mov_b32_e32 v7, 0
	v_mov_b32_e32 v11, 0
	v_mov_b32_e32 v15, 0
	v_mov_b32_e32 v4, 0
	v_mov_b32_e32 v8, 0
	v_mov_b32_e32 v12, 0
	v_mov_b32_e32 v16, 0
	v_mov_b32_e32 v5, 0
	v_mov_b32_e32 v9, 0
	v_mov_b32_e32 v13, 0
	v_mov_b32_e32 v17, 0
	ds_read_b128 v[182:185], v165 offset:0
	v_cmp_lt_i32_e32 vcc, -1, v151
	v_lshlrev_b32_e32 v148, 13, v151
	v_mov_b32_e32 v149, 0
	v_lshl_add_u64 v[148:149], v[148:149], 0, v[86:87]
	v_cndmask_b32_e32 v148, v168, v148, vcc
	v_cndmask_b32_e32 v149, v169, v149, vcc
	s_waitcnt lgkmcnt(0)
	global_store_dwordx4 v[148:149], v[182:185], off nt
	ds_read_b128 v[182:185], v165 offset:8192
	v_cmp_lt_i32_e32 vcc, -1, v166
	v_lshlrev_b32_e32 v148, 13, v166
	v_mov_b32_e32 v149, 0
	v_lshl_add_u64 v[148:149], v[148:149], 0, v[86:87]
	v_cndmask_b32_e32 v148, v168, v148, vcc
	v_cndmask_b32_e32 v149, v169, v149, vcc
	s_waitcnt lgkmcnt(0)
	global_store_dwordx4 v[148:149], v[182:185], off nt
	v_add_co_u32_e32 v86, vcc, 0x400, v86
	s_nop 1
	v_addc_co_u32_e32 v87, vcc, 0, v87, vcc
	s_waitcnt lgkmcnt(0)
; #define MD_GLDS_A(buf, tau) do { _Pragma("unroll") for (int i = 0; i < 5; ++i) if (amask & (1u << i)) \
;         __builtin_amdgcn_global_load_lds((const unsigned*)((const char*)HIDp + aoff[i] + (size_t)((tau) & 7) * 128), (PG8_LAS unsigned*)(MD_SA(buf) + wid * 1024 + i * 8192), 16, 0, 0); } while (0)
; #define MD_B_ISSUE(sb, tau) do { const char* kb_ = Bb + (size_t)((tau) >> 3) * 512 + (size_t)((tau) & 7) * (64 * (size_t)RB); _Pragma("unroll") for (int j = 0; j < 8; ++j) { const char* p_ = kb_ + (size_t)j * RB; \
;         asm volatile("global_load_dwordx2 %0, %1, off" : "=&v"(sb[j]) : "v"(p_) : "memory"); } } while (0)
; #define MD_B_WAIT(sb, N) asm volatile("s_waitcnt vmcnt(%8)" : "+v"(sb[0]), "+v"(sb[1]), "+v"(sb[2]), "+v"(sb[3]), "+v"(sb[4]), "+v"(sb[5]), "+v"(sb[6]), "+v"(sb[7]) : "n"(N) : "memory")
; #define MD_END(last) do { if (last) asm volatile("s_waitcnt vmcnt(0)" ::: "memory"); else asm volatile("s_waitcnt vmcnt(8)" ::: "memory"); \
;         asm volatile("s_waitcnt lgkmcnt(0)" ::: "memory"); __builtin_amdgcn_s_barrier(); asm volatile("" ::: "memory"); } while (0)
; __device__ __forceinline__ void moe_down_stream(PG8_LAS unsigned char* lds, int e, int cb0, int slot0, int nv, const bf16_t* HIDp, const float* Wd, bf16_t* Y, const float* slot_w, const int* slot_dst) {
;     ...
;     for (int t = 0; t < NT; t += 2) {
;         if (t + 2 < NT) MD_B_WAIT(s1, 8); else MD_B_WAIT(s1, 0);
;         MD_B_WRITE(s1, 1); __builtin_amdgcn_sched_barrier(0); MD_GLDS_A(1, t + 1); __builtin_amdgcn_sched_barrier(0);
;         if (t + 3 < NT) MD_B_ISSUE(s1, t + 3);
;         MD_COMPUTE(0);
;         MD_END(t + 3 >= NT);
;         if (t + 2 < NT) { MD_B_WAIT(s0, 8); MD_B_WRITE(s0, 0); __builtin_amdgcn_sched_barrier(0); MD_GLDS_A(0, t + 2); __builtin_amdgcn_sched_barrier(0); }
;         if (t + 4 < NT) MD_B_ISSUE(s0, t + 4);
;         MD_COMPUTE(1);
;         MD_END(t + 4 >= NT);
.Lmd_noepi_X:
	s_sub_u32 s56, s56, 1
	s_cmp_lg_u32 s56, 0
	s_cbranch_scc1 .Lmd_loop_X
	v_cvt_pk_bf16_f32 v172, v114, v116
	v_cvt_pk_bf16_f32 v173, v118, v120
	v_cvt_pk_bf16_f32 v174, v122, v124
	v_cvt_pk_bf16_f32 v175, v126, v128
	v_cvt_pk_bf16_f32 v176, v115, v117
	v_cvt_pk_bf16_f32 v177, v119, v121
	v_cvt_pk_bf16_f32 v178, v123, v125
	v_cvt_pk_bf16_f32 v179, v127, v129
	ds_write_b128 v95, v[172:175] offset:19456
	ds_write_b128 v95, v[176:179] offset:19584
	v_add_u32_e32 v91, s46, v135
	v_add_u32_e32 v93, s46, v137
	ds_read_b128 v[238:241], v139 offset:0
	ds_read_b128 v[242:245], v139 offset:2048
	ds_read_b128 v[246:249], v139 offset:4096
	ds_read_b128 v[250:253], v139 offset:6144
	ds_read_b128 v[218:221], v91 offset:0
	ds_read_b128 v[222:225], v91 offset:2048
	ds_read_b128 v[226:229], v91 offset:4096
	ds_read_b128 v[230:233], v91 offset:6144
	ds_read_b128 v[234:237], v91 offset:8192
	s_add_i32 s49, s48, s74
	s_add_i32 s52, s52, 1
	s_and_b32 s54, s52, 7
	s_cmp_eq_u32 s54, 0
	s_cselect_b32 s54, s53, s32
	s_cselect_b32 s55, -1, 0
	s_add_u32 s30, s30, s54
	s_addc_u32 s31, s31, s55
	s_waitcnt lgkmcnt(0)
	v_mfma_f32_16x16x32_bf16 v[78:81], v[238:241], v[218:221], v[78:81]
	v_mfma_f32_16x16x32_bf16 v[74:77], v[242:245], v[218:221], v[74:77]
	v_mfma_f32_16x16x32_bf16 v[70:73], v[246:249], v[218:221], v[70:73]
	v_mfma_f32_16x16x32_bf16 v[66:69], v[250:253], v[218:221], v[66:69]
	ds_read_b128 v[218:221], v93 offset:0
	ds_read_b128 v[142:145], v141 offset:0
	s_mov_b32 m0, s49
	s_nop 0
	global_load_lds_dwordx4 v88, s[30:31]
	v_mfma_f32_16x16x32_bf16 v[62:65], v[238:241], v[222:225], v[62:65]
	v_mfma_f32_16x16x32_bf16 v[58:61], v[242:245], v[222:225], v[58:61]
	v_mfma_f32_16x16x32_bf16 v[54:57], v[246:249], v[222:225], v[54:57]
	v_mfma_f32_16x16x32_bf16 v[50:53], v[250:253], v[222:225], v[50:53]
	ds_read_b128 v[222:225], v93 offset:2048
	ds_read_b128 v[146:149], v141 offset:2048
	s_add_i32 m0, s49, 0x2000
	s_nop 0
	global_load_lds_dwordx4 v90, s[30:31]
	v_mfma_f32_16x16x32_bf16 v[46:49], v[238:241], v[226:229], v[46:49]
	v_mfma_f32_16x16x32_bf16 v[42:45], v[242:245], v[226:229], v[42:45]
	v_mfma_f32_16x16x32_bf16 v[38:41], v[246:249], v[226:229], v[38:41]
	v_mfma_f32_16x16x32_bf16 v[34:37], v[250:253], v[226:229], v[34:37]
	ds_read_b128 v[226:229], v93 offset:4096
	ds_read_b128 v[156:159], v141 offset:4096
	s_add_i32 m0, s49, 0x4000
	s_nop 0
	global_load_lds_dwordx4 v92, s[30:31]
	v_mfma_f32_16x16x32_bf16 v[18:21], v[238:241], v[230:233], v[18:21]
	v_mfma_f32_16x16x32_bf16 v[22:25], v[242:245], v[230:233], v[22:25]
	v_mfma_f32_16x16x32_bf16 v[26:29], v[246:249], v[230:233], v[26:29]
	v_mfma_f32_16x16x32_bf16 v[30:33], v[250:253], v[230:233], v[30:33]
	ds_read_b128 v[230:233], v93 offset:6144
	ds_read_b128 v[160:163], v141 offset:6144
	s_add_i32 m0, s49, 0x6000
	s_nop 0
	global_load_lds_dwordx4 v94, s[30:31]
	v_mfma_f32_16x16x32_bf16 v[2:5], v[238:241], v[234:237], v[2:5]
	v_mfma_f32_16x16x32_bf16 v[6:9], v[242:245], v[234:237], v[6:9]
	v_mfma_f32_16x16x32_bf16 v[10:13], v[246:249], v[234:237], v[10:13]
	v_mfma_f32_16x16x32_bf16 v[14:17], v[250:253], v[234:237], v[14:17]
	ds_read_b128 v[234:237], v93 offset:8192
	s_add_i32 m0, s49, 0x8000
	s_nop 0
	global_load_lds_dwordx4 v96, s[30:31]
	s_waitcnt lgkmcnt(0)
	v_mfma_f32_16x16x32_bf16 v[78:81], v[142:145], v[218:221], v[78:81]
	v_mfma_f32_16x16x32_bf16 v[74:77], v[146:149], v[218:221], v[74:77]
	v_mfma_f32_16x16x32_bf16 v[70:73], v[156:159], v[218:221], v[70:73]
	v_mfma_f32_16x16x32_bf16 v[66:69], v[160:163], v[218:221], v[66:69]
	s_add_i32 s51, s51, 1
	s_and_b32 s54, s51, 7
	s_cmp_eq_u32 s54, 0
	s_cselect_b32 s44, s34, s35
	s_cselect_b32 s45, -1, 0
	v_lshl_add_u64 v[132:133], v[132:133], 0, s[44:45]
	global_load_dwordx2 v[114:115], v[132:133], off
	v_lshl_add_u64 v[180:181], v[132:133], 0, s[24:25]
	global_load_dwordx2 v[116:117], v[180:181], off
	v_mfma_f32_16x16x32_bf16 v[62:65], v[142:145], v[222:225], v[62:65]
	v_mfma_f32_16x16x32_bf16 v[58:61], v[146:149], v[222:225], v[58:61]
	v_mfma_f32_16x16x32_bf16 v[54:57], v[156:159], v[222:225], v[54:57]
	v_mfma_f32_16x16x32_bf16 v[50:53], v[160:163], v[222:225], v[50:53]
	v_lshl_add_u64 v[180:181], v[132:133], 0, s[26:27]
	global_load_dwordx2 v[118:119], v[180:181], off
	v_lshl_add_u64 v[180:181], v[132:133], 0, s[28:29]
	global_load_dwordx2 v[120:121], v[180:181], off
	v_mfma_f32_16x16x32_bf16 v[46:49], v[142:145], v[226:229], v[46:49]
	v_mfma_f32_16x16x32_bf16 v[42:45], v[146:149], v[226:229], v[42:45]
	v_mfma_f32_16x16x32_bf16 v[38:41], v[156:159], v[226:229], v[38:41]
	v_mfma_f32_16x16x32_bf16 v[34:37], v[160:163], v[226:229], v[34:37]
	v_lshl_add_u64 v[180:181], v[132:133], 0, s[36:37]
	global_load_dwordx2 v[122:123], v[180:181], off
	v_lshl_add_u64 v[180:181], v[132:133], 0, s[38:39]
	global_load_dwordx2 v[124:125], v[180:181], off
	v_mfma_f32_16x16x32_bf16 v[18:21], v[142:145], v[230:233], v[18:21]
	v_mfma_f32_16x16x32_bf16 v[22:25], v[146:149], v[230:233], v[22:25]
	v_mfma_f32_16x16x32_bf16 v[26:29], v[156:159], v[230:233], v[26:29]
	v_mfma_f32_16x16x32_bf16 v[30:33], v[160:163], v[230:233], v[30:33]
	v_lshl_add_u64 v[180:181], v[132:133], 0, s[40:41]
	global_load_dwordx2 v[126:127], v[180:181], off
	v_lshl_add_u64 v[180:181], v[132:133], 0, s[42:43]
	global_load_dwordx2 v[128:129], v[180:181], off
	v_mfma_f32_16x16x32_bf16 v[2:5], v[142:145], v[234:237], v[2:5]
	v_mfma_f32_16x16x32_bf16 v[6:9], v[146:149], v[234:237], v[6:9]
	v_mfma_f32_16x16x32_bf16 v[10:13], v[156:159], v[234:237], v[10:13]
	v_mfma_f32_16x16x32_bf16 v[14:17], v[160:163], v[234:237], v[14:17]
	s_waitcnt vmcnt(21)
	s_waitcnt lgkmcnt(0)
	s_barrier
; #define MD_GLDS_A(buf, tau) do { _Pragma("unroll") for (int i = 0; i < 5; ++i) if (amask & (1u << i)) \
;         __builtin_amdgcn_global_load_lds((const unsigned*)((const char*)HIDp + aoff[i] + (size_t)((tau) & 7) * 128), (PG8_LAS unsigned*)(MD_SA(buf) + wid * 1024 + i * 8192), 16, 0, 0); } while (0)
; #define MD_B_ISSUE(sb, tau) do { const char* kb_ = Bb + (size_t)((tau) >> 3) * 512 + (size_t)((tau) & 7) * (64 * (size_t)RB); _Pragma("unroll") for (int j = 0; j < 8; ++j) { const char* p_ = kb_ + (size_t)j * RB; \
;         asm volatile("global_load_dwordx2 %0, %1, off" : "=&v"(sb[j]) : "v"(p_) : "memory"); } } while (0)
; #define MD_B_WAIT(sb, N) asm volatile("s_waitcnt vmcnt(%8)" : "+v"(sb[0]), "+v"(sb[1]), "+v"(sb[2]), "+v"(sb[3]), "+v"(sb[4]), "+v"(sb[5]), "+v"(sb[6]), "+v"(sb[7]) : "n"(N) : "memory")
; __device__ __forceinline__ void moe_down_stream(PG8_LAS unsigned char* lds, int e, int cb0, int slot0, int nv, const bf16_t* HIDp, const float* Wd, bf16_t* Y, const float* slot_w, const int* slot_dst) {
;     ...
;     f32x4 acc[DNM][4];
; #pragma unroll
;     for (int m = 0; m < DNM; ++m)
; #pragma unroll
;         for (int n = 0; n < 4; ++n) acc[m][n] = (f32x4){0.f, 0.f, 0.f, 0.f};
;     f32x2 s0[8], s1[8];
;     MD_GLDS_A(0, 0); MD_B_ISSUE(s0, 0); MD_B_ISSUE(s1, 1);
;     MD_B_WAIT(s0, 8); MD_B_WRITE(s0, 0); __builtin_amdgcn_sched_barrier(0); MD_B_ISSUE(s0, 2);
;     asm volatile("s_waitcnt vmcnt(16)" ::: "memory");
;     asm volatile("s_waitcnt lgkmcnt(0)" ::: "memory"); __builtin_amdgcn_s_barrier(); asm volatile("" ::: "memory");
; #pragma unroll 1
;     for (int t = 0; t < NT; t += 2) {
;         if (t + 2 < NT) MD_B_WAIT(s1, 8); else MD_B_WAIT(s1, 0);
;         MD_B_WRITE(s1, 1); __builtin_amdgcn_sched_barrier(0); MD_GLDS_A(1, t + 1); __builtin_amdgcn_sched_barrier(0);
;         if (t + 3 < NT) MD_B_ISSUE(s1, t + 3);
;         MD_COMPUTE(0);
;         MD_END(t + 3 >= NT);
;         if (t + 2 < NT) { MD_B_WAIT(s0, 8); MD_B_WRITE(s0, 0); __builtin_amdgcn_sched_barrier(0); MD_GLDS_A(0, t + 2); __builtin_amdgcn_sched_barrier(0); }
;         if (t + 4 < NT) MD_B_ISSUE(s0, t + 4);
;         MD_COMPUTE(1);
;         MD_END(t + 4 >= NT);
	s_mov_b32 s49, s46
	s_mov_b32 s46, s47
	s_mov_b32 s47, s48
	s_mov_b32 s48, s49
	s_add_i32 s50, s50, 1
	v_cvt_pk_bf16_f32 v172, v186, v188
	v_cvt_pk_bf16_f32 v173, v190, v192
	v_cvt_pk_bf16_f32 v174, v194, v196
	v_cvt_pk_bf16_f32 v175, v198, v200
	v_cvt_pk_bf16_f32 v176, v187, v189
	v_cvt_pk_bf16_f32 v177, v191, v193
	v_cvt_pk_bf16_f32 v178, v195, v197
	v_cvt_pk_bf16_f32 v179, v199, v201
	ds_write_b128 v95, v[172:175] offset:0
	ds_write_b128 v95, v[176:179] offset:128
	v_add_u32_e32 v91, s46, v135
	v_add_u32_e32 v93, s46, v137
	ds_read_b128 v[238:241], v139 offset:19456
	ds_read_b128 v[242:245], v139 offset:21504
	ds_read_b128 v[246:249], v139 offset:23552
	ds_read_b128 v[250:253], v139 offset:25600
	ds_read_b128 v[218:221], v91 offset:0
	ds_read_b128 v[222:225], v91 offset:2048
	ds_read_b128 v[226:229], v91 offset:4096
	ds_read_b128 v[230:233], v91 offset:6144
	ds_read_b128 v[234:237], v91 offset:8192
	s_add_i32 s49, s48, s74
	s_add_i32 s52, s52, 1
	s_and_b32 s54, s52, 7
	s_cmp_eq_u32 s54, 0
	s_cselect_b32 s54, s53, s32
	s_cselect_b32 s55, -1, 0
	s_add_u32 s30, s30, s54
	s_addc_u32 s31, s31, s55
	s_waitcnt lgkmcnt(0)
	v_mfma_f32_16x16x32_bf16 v[78:81], v[238:241], v[218:221], v[78:81]
	v_mfma_f32_16x16x32_bf16 v[74:77], v[242:245], v[218:221], v[74:77]
	v_mfma_f32_16x16x32_bf16 v[70:73], v[246:249], v[218:221], v[70:73]
	v_mfma_f32_16x16x32_bf16 v[66:69], v[250:253], v[218:221], v[66:69]
	ds_read_b128 v[218:221], v93 offset:0
	ds_read_b128 v[142:145], v141 offset:19456
	s_mov_b32 m0, s49
	s_nop 0
	global_load_lds_dwordx4 v88, s[30:31]
	v_mfma_f32_16x16x32_bf16 v[62:65], v[238:241], v[222:225], v[62:65]
	v_mfma_f32_16x16x32_bf16 v[58:61], v[242:245], v[222:225], v[58:61]
	v_mfma_f32_16x16x32_bf16 v[54:57], v[246:249], v[222:225], v[54:57]
	v_mfma_f32_16x16x32_bf16 v[50:53], v[250:253], v[222:225], v[50:53]
	ds_read_b128 v[222:225], v93 offset:2048
	ds_read_b128 v[146:149], v141 offset:21504
	s_add_i32 m0, s49, 0x2000
	s_nop 0
	global_load_lds_dwordx4 v90, s[30:31]
	v_mfma_f32_16x16x32_bf16 v[46:49], v[238:241], v[226:229], v[46:49]
	v_mfma_f32_16x16x32_bf16 v[42:45], v[242:245], v[226:229], v[42:45]
	v_mfma_f32_16x16x32_bf16 v[38:41], v[246:249], v[226:229], v[38:41]
	v_mfma_f32_16x16x32_bf16 v[34:37], v[250:253], v[226:229], v[34:37]
	ds_read_b128 v[226:229], v93 offset:4096
	ds_read_b128 v[156:159], v141 offset:23552
	s_add_i32 m0, s49, 0x4000
	s_nop 0
	global_load_lds_dwordx4 v92, s[30:31]
	v_mfma_f32_16x16x32_bf16 v[18:21], v[238:241], v[230:233], v[18:21]
	v_mfma_f32_16x16x32_bf16 v[22:25], v[242:245], v[230:233], v[22:25]
	v_mfma_f32_16x16x32_bf16 v[26:29], v[246:249], v[230:233], v[26:29]
	v_mfma_f32_16x16x32_bf16 v[30:33], v[250:253], v[230:233], v[30:33]
	ds_read_b128 v[230:233], v93 offset:6144
	ds_read_b128 v[160:163], v141 offset:25600
	s_add_i32 m0, s49, 0x6000
	s_nop 0
	global_load_lds_dwordx4 v94, s[30:31]
	v_mfma_f32_16x16x32_bf16 v[2:5], v[238:241], v[234:237], v[2:5]
	v_mfma_f32_16x16x32_bf16 v[6:9], v[242:245], v[234:237], v[6:9]
	v_mfma_f32_16x16x32_bf16 v[10:13], v[246:249], v[234:237], v[10:13]
	v_mfma_f32_16x16x32_bf16 v[14:17], v[250:253], v[234:237], v[14:17]
	ds_read_b128 v[234:237], v93 offset:8192
	s_add_i32 m0, s49, 0x8000
	s_nop 0
	global_load_lds_dwordx4 v96, s[30:31]
	s_waitcnt lgkmcnt(0)
	v_mfma_f32_16x16x32_bf16 v[78:81], v[142:145], v[218:221], v[78:81]
	v_mfma_f32_16x16x32_bf16 v[74:77], v[146:149], v[218:221], v[74:77]
	v_mfma_f32_16x16x32_bf16 v[70:73], v[156:159], v[218:221], v[70:73]
	v_mfma_f32_16x16x32_bf16 v[66:69], v[160:163], v[218:221], v[66:69]
	s_add_i32 s51, s51, 1
	s_and_b32 s54, s51, 7
	s_cmp_eq_u32 s54, 0
	s_cselect_b32 s44, s34, s35
	s_cselect_b32 s45, -1, 0
	v_lshl_add_u64 v[132:133], v[132:133], 0, s[44:45]
	global_load_dwordx2 v[186:187], v[132:133], off
	v_lshl_add_u64 v[180:181], v[132:133], 0, s[24:25]
	global_load_dwordx2 v[188:189], v[180:181], off
	v_mfma_f32_16x16x32_bf16 v[62:65], v[142:145], v[222:225], v[62:65]
	v_mfma_f32_16x16x32_bf16 v[58:61], v[146:149], v[222:225], v[58:61]
	v_mfma_f32_16x16x32_bf16 v[54:57], v[156:159], v[222:225], v[54:57]
	v_mfma_f32_16x16x32_bf16 v[50:53], v[160:163], v[222:225], v[50:53]
	v_lshl_add_u64 v[180:181], v[132:133], 0, s[26:27]
	global_load_dwordx2 v[190:191], v[180:181], off
	v_lshl_add_u64 v[180:181], v[132:133], 0, s[28:29]
	global_load_dwordx2 v[192:193], v[180:181], off
	v_mfma_f32_16x16x32_bf16 v[46:49], v[142:145], v[226:229], v[46:49]
	v_mfma_f32_16x16x32_bf16 v[42:45], v[146:149], v[226:229], v[42:45]
	v_mfma_f32_16x16x32_bf16 v[38:41], v[156:159], v[226:229], v[38:41]
	v_mfma_f32_16x16x32_bf16 v[34:37], v[160:163], v[226:229], v[34:37]
	v_lshl_add_u64 v[180:181], v[132:133], 0, s[36:37]
	global_load_dwordx2 v[194:195], v[180:181], off
	v_lshl_add_u64 v[180:181], v[132:133], 0, s[38:39]
	global_load_dwordx2 v[196:197], v[180:181], off
	v_mfma_f32_16x16x32_bf16 v[18:21], v[142:145], v[230:233], v[18:21]
	v_mfma_f32_16x16x32_bf16 v[22:25], v[146:149], v[230:233], v[22:25]
	v_mfma_f32_16x16x32_bf16 v[26:29], v[156:159], v[230:233], v[26:29]
	v_mfma_f32_16x16x32_bf16 v[30:33], v[160:163], v[230:233], v[30:33]
	v_lshl_add_u64 v[180:181], v[132:133], 0, s[40:41]
	global_load_dwordx2 v[198:199], v[180:181], off
	v_lshl_add_u64 v[180:181], v[132:133], 0, s[42:43]
	global_load_dwordx2 v[200:201], v[180:181], off
	v_mfma_f32_16x16x32_bf16 v[2:5], v[142:145], v[234:237], v[2:5]
	v_mfma_f32_16x16x32_bf16 v[6:9], v[146:149], v[234:237], v[6:9]
	v_mfma_f32_16x16x32_bf16 v[10:13], v[156:159], v[234:237], v[10:13]
	v_mfma_f32_16x16x32_bf16 v[14:17], v[160:163], v[234:237], v[14:17]
	s_waitcnt vmcnt(21)
	s_waitcnt lgkmcnt(0)
	s_barrier
; #define MD_GLDS_A(buf, tau) do { _Pragma("unroll") for (int i = 0; i < 5; ++i) if (amask & (1u << i)) \
;         __builtin_amdgcn_global_load_lds((const unsigned*)((const char*)HIDp + aoff[i] + (size_t)((tau) & 7) * 128), (PG8_LAS unsigned*)(MD_SA(buf) + wid * 1024 + i * 8192), 16, 0, 0); } while (0)
; #define MD_B_ISSUE(sb, tau) do { const char* kb_ = Bb + (size_t)((tau) >> 3) * 512 + (size_t)((tau) & 7) * (64 * (size_t)RB); _Pragma("unroll") for (int j = 0; j < 8; ++j) { const char* p_ = kb_ + (size_t)j * RB; \
;         asm volatile("global_load_dwordx2 %0, %1, off" : "=&v"(sb[j]) : "v"(p_) : "memory"); } } while (0)
; #define MD_B_WAIT(sb, N) asm volatile("s_waitcnt vmcnt(%8)" : "+v"(sb[0]), "+v"(sb[1]), "+v"(sb[2]), "+v"(sb[3]), "+v"(sb[4]), "+v"(sb[5]), "+v"(sb[6]), "+v"(sb[7]) : "n"(N) : "memory")
; __device__ __forceinline__ void moe_down_stream(PG8_LAS unsigned char* lds, int e, int cb0, int slot0, int nv, const bf16_t* HIDp, const float* Wd, bf16_t* Y, const float* slot_w, const int* slot_dst) {
;     ...
;     f32x4 acc[DNM][4];
; #pragma unroll
;     for (int m = 0; m < DNM; ++m)
; #pragma unroll
;         for (int n = 0; n < 4; ++n) acc[m][n] = (f32x4){0.f, 0.f, 0.f, 0.f};
;     f32x2 s0[8], s1[8];
;     MD_GLDS_A(0, 0); MD_B_ISSUE(s0, 0); MD_B_ISSUE(s1, 1);
;     MD_B_WAIT(s0, 8); MD_B_WRITE(s0, 0); __builtin_amdgcn_sched_barrier(0); MD_B_ISSUE(s0, 2);
;     asm volatile("s_waitcnt vmcnt(16)" ::: "memory");
;     asm volatile("s_waitcnt lgkmcnt(0)" ::: "memory"); __builtin_amdgcn_s_barrier(); asm volatile("" ::: "memory");
; #pragma unroll 1
;     for (int t = 0; t < NT; t += 2) {
;         if (t + 2 < NT) MD_B_WAIT(s1, 8); else MD_B_WAIT(s1, 0);
;         MD_B_WRITE(s1, 1); __builtin_amdgcn_sched_barrier(0); MD_GLDS_A(1, t + 1); __builtin_amdgcn_sched_barrier(0);
;         if (t + 3 < NT) MD_B_ISSUE(s1, t + 3);
;         MD_COMPUTE(0);
;         MD_END(t + 3 >= NT);
;         if (t + 2 < NT) { MD_B_WAIT(s0, 8); MD_B_WRITE(s0, 0); __builtin_amdgcn_sched_barrier(0); MD_GLDS_A(0, t + 2); __builtin_amdgcn_sched_barrier(0); }
;         if (t + 4 < NT) MD_B_ISSUE(s0, t + 4);
;         MD_COMPUTE(1);
;         MD_END(t + 4 >= NT);
	s_mov_b32 s49, s46
	s_mov_b32 s46, s47
	s_mov_b32 s47, s48
	s_mov_b32 s48, s49
	s_add_i32 s50, s50, 1
	v_cvt_pk_bf16_f32 v172, v202, v204
	v_cvt_pk_bf16_f32 v173, v206, v208
	v_cvt_pk_bf16_f32 v174, v210, v212
	v_cvt_pk_bf16_f32 v175, v214, v216
	v_cvt_pk_bf16_f32 v176, v203, v205
	v_cvt_pk_bf16_f32 v177, v207, v209
	v_cvt_pk_bf16_f32 v178, v211, v213
	v_cvt_pk_bf16_f32 v179, v215, v217
	ds_write_b128 v95, v[172:175] offset:19456
	ds_write_b128 v95, v[176:179] offset:19584
	v_add_u32_e32 v91, s46, v135
	v_add_u32_e32 v93, s46, v137
	ds_read_b128 v[238:241], v139 offset:0
	ds_read_b128 v[242:245], v139 offset:2048
	ds_read_b128 v[246:249], v139 offset:4096
	ds_read_b128 v[250:253], v139 offset:6144
	ds_read_b128 v[218:221], v91 offset:0
	ds_read_b128 v[222:225], v91 offset:2048
	ds_read_b128 v[226:229], v91 offset:4096
	ds_read_b128 v[230:233], v91 offset:6144
	ds_read_b128 v[234:237], v91 offset:8192
	s_add_i32 s49, s48, s74
	s_add_i32 s52, s52, 1
	s_and_b32 s54, s52, 7
	s_cmp_eq_u32 s54, 0
	s_cselect_b32 s54, s53, s32
	s_cselect_b32 s55, -1, 0
	s_add_u32 s30, s30, s54
	s_addc_u32 s31, s31, s55
	s_waitcnt lgkmcnt(0)
	v_mfma_f32_16x16x32_bf16 v[78:81], v[238:241], v[218:221], v[78:81]
	v_mfma_f32_16x16x32_bf16 v[74:77], v[242:245], v[218:221], v[74:77]
	v_mfma_f32_16x16x32_bf16 v[70:73], v[246:249], v[218:221], v[70:73]
	v_mfma_f32_16x16x32_bf16 v[66:69], v[250:253], v[218:221], v[66:69]
	ds_read_b128 v[218:221], v93 offset:0
	ds_read_b128 v[142:145], v141 offset:0
	s_mov_b32 m0, s49
	s_nop 0
	global_load_lds_dwordx4 v88, s[30:31]
	v_mfma_f32_16x16x32_bf16 v[62:65], v[238:241], v[222:225], v[62:65]
	v_mfma_f32_16x16x32_bf16 v[58:61], v[242:245], v[222:225], v[58:61]
	v_mfma_f32_16x16x32_bf16 v[54:57], v[246:249], v[222:225], v[54:57]
	v_mfma_f32_16x16x32_bf16 v[50:53], v[250:253], v[222:225], v[50:53]
	ds_read_b128 v[222:225], v93 offset:2048
	ds_read_b128 v[146:149], v141 offset:2048
	s_add_i32 m0, s49, 0x2000
	s_nop 0
	global_load_lds_dwordx4 v90, s[30:31]
	v_mfma_f32_16x16x32_bf16 v[46:49], v[238:241], v[226:229], v[46:49]
	v_mfma_f32_16x16x32_bf16 v[42:45], v[242:245], v[226:229], v[42:45]
	v_mfma_f32_16x16x32_bf16 v[38:41], v[246:249], v[226:229], v[38:41]
	v_mfma_f32_16x16x32_bf16 v[34:37], v[250:253], v[226:229], v[34:37]
	ds_read_b128 v[226:229], v93 offset:4096
	ds_read_b128 v[156:159], v141 offset:4096
	s_add_i32 m0, s49, 0x4000
	s_nop 0
	global_load_lds_dwordx4 v92, s[30:31]
	v_mfma_f32_16x16x32_bf16 v[18:21], v[238:241], v[230:233], v[18:21]
	v_mfma_f32_16x16x32_bf16 v[22:25], v[242:245], v[230:233], v[22:25]
	v_mfma_f32_16x16x32_bf16 v[26:29], v[246:249], v[230:233], v[26:29]
	v_mfma_f32_16x16x32_bf16 v[30:33], v[250:253], v[230:233], v[30:33]
	ds_read_b128 v[230:233], v93 offset:6144
	ds_read_b128 v[160:163], v141 offset:6144
	s_add_i32 m0, s49, 0x6000
	s_nop 0
	global_load_lds_dwordx4 v94, s[30:31]
	v_mfma_f32_16x16x32_bf16 v[2:5], v[238:241], v[234:237], v[2:5]
	v_mfma_f32_16x16x32_bf16 v[6:9], v[242:245], v[234:237], v[6:9]
	v_mfma_f32_16x16x32_bf16 v[10:13], v[246:249], v[234:237], v[10:13]
	v_mfma_f32_16x16x32_bf16 v[14:17], v[250:253], v[234:237], v[14:17]
	ds_read_b128 v[234:237], v93 offset:8192
	s_add_i32 m0, s49, 0x8000
	s_nop 0
	global_load_lds_dwordx4 v96, s[30:31]
	s_waitcnt lgkmcnt(0)
	v_mfma_f32_16x16x32_bf16 v[78:81], v[142:145], v[218:221], v[78:81]
	v_mfma_f32_16x16x32_bf16 v[74:77], v[146:149], v[218:221], v[74:77]
	v_mfma_f32_16x16x32_bf16 v[70:73], v[156:159], v[218:221], v[70:73]
	v_mfma_f32_16x16x32_bf16 v[66:69], v[160:163], v[218:221], v[66:69]
	s_add_i32 s51, s51, 1
	s_and_b32 s54, s51, 7
	s_cmp_eq_u32 s54, 0
	s_cselect_b32 s44, s34, s35
	s_cselect_b32 s45, -1, 0
	v_lshl_add_u64 v[132:133], v[132:133], 0, s[44:45]
	global_load_dwordx2 v[202:203], v[132:133], off
	v_lshl_add_u64 v[180:181], v[132:133], 0, s[24:25]
	global_load_dwordx2 v[204:205], v[180:181], off
	v_mfma_f32_16x16x32_bf16 v[62:65], v[142:145], v[222:225], v[62:65]
	v_mfma_f32_16x16x32_bf16 v[58:61], v[146:149], v[222:225], v[58:61]
	v_mfma_f32_16x16x32_bf16 v[54:57], v[156:159], v[222:225], v[54:57]
	v_mfma_f32_16x16x32_bf16 v[50:53], v[160:163], v[222:225], v[50:53]
	v_lshl_add_u64 v[180:181], v[132:133], 0, s[26:27]
	global_load_dwordx2 v[206:207], v[180:181], off
	v_lshl_add_u64 v[180:181], v[132:133], 0, s[28:29]
	global_load_dwordx2 v[208:209], v[180:181], off
	v_mfma_f32_16x16x32_bf16 v[46:49], v[142:145], v[226:229], v[46:49]
	v_mfma_f32_16x16x32_bf16 v[42:45], v[146:149], v[226:229], v[42:45]
	v_mfma_f32_16x16x32_bf16 v[38:41], v[156:159], v[226:229], v[38:41]
	v_mfma_f32_16x16x32_bf16 v[34:37], v[160:163], v[226:229], v[34:37]
	v_lshl_add_u64 v[180:181], v[132:133], 0, s[36:37]
	global_load_dwordx2 v[210:211], v[180:181], off
	v_lshl_add_u64 v[180:181], v[132:133], 0, s[38:39]
	global_load_dwordx2 v[212:213], v[180:181], off
	v_mfma_f32_16x16x32_bf16 v[18:21], v[142:145], v[230:233], v[18:21]
	v_mfma_f32_16x16x32_bf16 v[22:25], v[146:149], v[230:233], v[22:25]
	v_mfma_f32_16x16x32_bf16 v[26:29], v[156:159], v[230:233], v[26:29]
	v_mfma_f32_16x16x32_bf16 v[30:33], v[160:163], v[230:233], v[30:33]
	v_lshl_add_u64 v[180:181], v[132:133], 0, s[40:41]
	global_load_dwordx2 v[214:215], v[180:181], off
	v_lshl_add_u64 v[180:181], v[132:133], 0, s[42:43]
	global_load_dwordx2 v[216:217], v[180:181], off
	v_mfma_f32_16x16x32_bf16 v[2:5], v[142:145], v[234:237], v[2:5]
	v_mfma_f32_16x16x32_bf16 v[6:9], v[146:149], v[234:237], v[6:9]
	v_mfma_f32_16x16x32_bf16 v[10:13], v[156:159], v[234:237], v[10:13]
	v_mfma_f32_16x16x32_bf16 v[14:17], v[160:163], v[234:237], v[14:17]
	s_waitcnt vmcnt(21)
	s_waitcnt lgkmcnt(0)
	s_barrier
; #define MD_GLDS_A(buf, tau) do { _Pragma("unroll") for (int i = 0; i < 5; ++i) if (amask & (1u << i)) \
;         __builtin_amdgcn_global_load_lds((const unsigned*)((const char*)HIDp + aoff[i] + (size_t)((tau) & 7) * 128), (PG8_LAS unsigned*)(MD_SA(buf) + wid * 1024 + i * 8192), 16, 0, 0); } while (0)
; #define MD_B_ISSUE(sb, tau) do { const char* kb_ = Bb + (size_t)((tau) >> 3) * 512 + (size_t)((tau) & 7) * (64 * (size_t)RB); _Pragma("unroll") for (int j = 0; j < 8; ++j) { const char* p_ = kb_ + (size_t)j * RB; \
;         asm volatile("global_load_dwordx2 %0, %1, off" : "=&v"(sb[j]) : "v"(p_) : "memory"); } } while (0)
; #define MD_B_WAIT(sb, N) asm volatile("s_waitcnt vmcnt(%8)" : "+v"(sb[0]), "+v"(sb[1]), "+v"(sb[2]), "+v"(sb[3]), "+v"(sb[4]), "+v"(sb[5]), "+v"(sb[6]), "+v"(sb[7]) : "n"(N) : "memory")
; __device__ __forceinline__ void moe_down_stream(PG8_LAS unsigned char* lds, int e, int cb0, int slot0, int nv, const bf16_t* HIDp, const float* Wd, bf16_t* Y, const float* slot_w, const int* slot_dst) {
;     ...
;     f32x4 acc[DNM][4];
; #pragma unroll
;     for (int m = 0; m < DNM; ++m)
; #pragma unroll
;         for (int n = 0; n < 4; ++n) acc[m][n] = (f32x4){0.f, 0.f, 0.f, 0.f};
;     f32x2 s0[8], s1[8];
;     MD_GLDS_A(0, 0); MD_B_ISSUE(s0, 0); MD_B_ISSUE(s1, 1);
;     MD_B_WAIT(s0, 8); MD_B_WRITE(s0, 0); __builtin_amdgcn_sched_barrier(0); MD_B_ISSUE(s0, 2);
;     asm volatile("s_waitcnt vmcnt(16)" ::: "memory");
;     asm volatile("s_waitcnt lgkmcnt(0)" ::: "memory"); __builtin_amdgcn_s_barrier(); asm volatile("" ::: "memory");
; #pragma unroll 1
;     for (int t = 0; t < NT; t += 2) {
;         if (t + 2 < NT) MD_B_WAIT(s1, 8); else MD_B_WAIT(s1, 0);
;         MD_B_WRITE(s1, 1); __builtin_amdgcn_sched_barrier(0); MD_GLDS_A(1, t + 1); __builtin_amdgcn_sched_barrier(0);
;         if (t + 3 < NT) MD_B_ISSUE(s1, t + 3);
;         MD_COMPUTE(0);
;         MD_END(t + 3 >= NT);
;         if (t + 2 < NT) { MD_B_WAIT(s0, 8); MD_B_WRITE(s0, 0); __builtin_amdgcn_sched_barrier(0); MD_GLDS_A(0, t + 2); __builtin_amdgcn_sched_barrier(0); }
;         if (t + 4 < NT) MD_B_ISSUE(s0, t + 4);
;         MD_COMPUTE(1);
;         MD_END(t + 4 >= NT);
	s_mov_b32 s49, s46
	s_mov_b32 s46, s47
	s_mov_b32 s47, s48
	s_mov_b32 s48, s49
	s_add_i32 s50, s50, 1
	v_cvt_pk_bf16_f32 v172, v98, v100
	v_cvt_pk_bf16_f32 v173, v102, v104
	v_cvt_pk_bf16_f32 v174, v106, v108
	v_cvt_pk_bf16_f32 v175, v110, v112
	v_cvt_pk_bf16_f32 v176, v99, v101
	v_cvt_pk_bf16_f32 v177, v103, v105
	v_cvt_pk_bf16_f32 v178, v107, v109
	v_cvt_pk_bf16_f32 v179, v111, v113
	ds_write_b128 v95, v[172:175] offset:0
	ds_write_b128 v95, v[176:179] offset:128
	v_add_u32_e32 v91, s46, v135
	v_add_u32_e32 v93, s46, v137
	ds_read_b128 v[238:241], v139 offset:19456
	ds_read_b128 v[242:245], v139 offset:21504
	ds_read_b128 v[246:249], v139 offset:23552
	ds_read_b128 v[250:253], v139 offset:25600
	ds_read_b128 v[218:221], v91 offset:0
	ds_read_b128 v[222:225], v91 offset:2048
	ds_read_b128 v[226:229], v91 offset:4096
	ds_read_b128 v[230:233], v91 offset:6144
	ds_read_b128 v[234:237], v91 offset:8192
	s_add_i32 s49, s48, s74
	s_add_i32 s52, s52, 1
	s_and_b32 s54, s52, 7
	s_cmp_eq_u32 s54, 0
	s_cselect_b32 s54, s53, s32
	s_cselect_b32 s55, -1, 0
	s_add_u32 s30, s30, s54
	s_addc_u32 s31, s31, s55
	s_waitcnt lgkmcnt(0)
	v_mfma_f32_16x16x32_bf16 v[78:81], v[238:241], v[218:221], v[78:81]
	v_mfma_f32_16x16x32_bf16 v[74:77], v[242:245], v[218:221], v[74:77]
	v_mfma_f32_16x16x32_bf16 v[70:73], v[246:249], v[218:221], v[70:73]
	v_mfma_f32_16x16x32_bf16 v[66:69], v[250:253], v[218:221], v[66:69]
	ds_read_b128 v[218:221], v93 offset:0
	ds_read_b128 v[142:145], v141 offset:19456
	s_mov_b32 m0, s49
	s_nop 0
	global_load_lds_dwordx4 v88, s[30:31]
	v_mfma_f32_16x16x32_bf16 v[62:65], v[238:241], v[222:225], v[62:65]
	v_mfma_f32_16x16x32_bf16 v[58:61], v[242:245], v[222:225], v[58:61]
	v_mfma_f32_16x16x32_bf16 v[54:57], v[246:249], v[222:225], v[54:57]
	v_mfma_f32_16x16x32_bf16 v[50:53], v[250:253], v[222:225], v[50:53]
	ds_read_b128 v[222:225], v93 offset:2048
	ds_read_b128 v[146:149], v141 offset:21504
	s_add_i32 m0, s49, 0x2000
	s_nop 0
	global_load_lds_dwordx4 v90, s[30:31]
	v_mfma_f32_16x16x32_bf16 v[46:49], v[238:241], v[226:229], v[46:49]
	v_mfma_f32_16x16x32_bf16 v[42:45], v[242:245], v[226:229], v[42:45]
	v_mfma_f32_16x16x32_bf16 v[38:41], v[246:249], v[226:229], v[38:41]
	v_mfma_f32_16x16x32_bf16 v[34:37], v[250:253], v[226:229], v[34:37]
	ds_read_b128 v[226:229], v93 offset:4096
	ds_read_b128 v[156:159], v141 offset:23552
	s_add_i32 m0, s49, 0x4000
	s_nop 0
	global_load_lds_dwordx4 v92, s[30:31]
	v_mfma_f32_16x16x32_bf16 v[18:21], v[238:241], v[230:233], v[18:21]
	v_mfma_f32_16x16x32_bf16 v[22:25], v[242:245], v[230:233], v[22:25]
	v_mfma_f32_16x16x32_bf16 v[26:29], v[246:249], v[230:233], v[26:29]
	v_mfma_f32_16x16x32_bf16 v[30:33], v[250:253], v[230:233], v[30:33]
	ds_read_b128 v[230:233], v93 offset:6144
	ds_read_b128 v[160:163], v141 offset:25600
	s_add_i32 m0, s49, 0x6000
	s_nop 0
	global_load_lds_dwordx4 v94, s[30:31]
	v_mfma_f32_16x16x32_bf16 v[2:5], v[238:241], v[234:237], v[2:5]
	v_mfma_f32_16x16x32_bf16 v[6:9], v[242:245], v[234:237], v[6:9]
	v_mfma_f32_16x16x32_bf16 v[10:13], v[246:249], v[234:237], v[10:13]
	v_mfma_f32_16x16x32_bf16 v[14:17], v[250:253], v[234:237], v[14:17]
	ds_read_b128 v[234:237], v93 offset:8192
	s_add_i32 m0, s49, 0x8000
	s_nop 0
	global_load_lds_dwordx4 v96, s[30:31]
	s_waitcnt lgkmcnt(0)
	v_mfma_f32_16x16x32_bf16 v[78:81], v[142:145], v[218:221], v[78:81]
	v_mfma_f32_16x16x32_bf16 v[74:77], v[146:149], v[218:221], v[74:77]
	v_mfma_f32_16x16x32_bf16 v[70:73], v[156:159], v[218:221], v[70:73]
	v_mfma_f32_16x16x32_bf16 v[66:69], v[160:163], v[218:221], v[66:69]
	v_mfma_f32_16x16x32_bf16 v[62:65], v[142:145], v[222:225], v[62:65]
	v_mfma_f32_16x16x32_bf16 v[58:61], v[146:149], v[222:225], v[58:61]
	v_mfma_f32_16x16x32_bf16 v[54:57], v[156:159], v[222:225], v[54:57]
	v_mfma_f32_16x16x32_bf16 v[50:53], v[160:163], v[222:225], v[50:53]
	v_mfma_f32_16x16x32_bf16 v[46:49], v[142:145], v[226:229], v[46:49]
	v_mfma_f32_16x16x32_bf16 v[42:45], v[146:149], v[226:229], v[42:45]
	v_mfma_f32_16x16x32_bf16 v[38:41], v[156:159], v[226:229], v[38:41]
	v_mfma_f32_16x16x32_bf16 v[34:37], v[160:163], v[226:229], v[34:37]
	v_mfma_f32_16x16x32_bf16 v[18:21], v[142:145], v[230:233], v[18:21]
	v_mfma_f32_16x16x32_bf16 v[22:25], v[146:149], v[230:233], v[22:25]
	v_mfma_f32_16x16x32_bf16 v[26:29], v[156:159], v[230:233], v[26:29]
	v_mfma_f32_16x16x32_bf16 v[30:33], v[160:163], v[230:233], v[30:33]
	v_mfma_f32_16x16x32_bf16 v[2:5], v[142:145], v[234:237], v[2:5]
	v_mfma_f32_16x16x32_bf16 v[6:9], v[146:149], v[234:237], v[6:9]
	v_mfma_f32_16x16x32_bf16 v[10:13], v[156:159], v[234:237], v[10:13]
	v_mfma_f32_16x16x32_bf16 v[14:17], v[160:163], v[234:237], v[14:17]
	s_waitcnt vmcnt(13)
	s_waitcnt lgkmcnt(0)
	s_barrier
; #define MD_GLDS_A(buf, tau) do { _Pragma("unroll") for (int i = 0; i < 5; ++i) if (amask & (1u << i)) \
;         __builtin_amdgcn_global_load_lds((const unsigned*)((const char*)HIDp + aoff[i] + (size_t)((tau) & 7) * 128), (PG8_LAS unsigned*)(MD_SA(buf) + wid * 1024 + i * 8192), 16, 0, 0); } while (0)
; #define MD_B_ISSUE(sb, tau) do { const char* kb_ = Bb + (size_t)((tau) >> 3) * 512 + (size_t)((tau) & 7) * (64 * (size_t)RB); _Pragma("unroll") for (int j = 0; j < 8; ++j) { const char* p_ = kb_ + (size_t)j * RB; \
;         asm volatile("global_load_dwordx2 %0, %1, off" : "=&v"(sb[j]) : "v"(p_) : "memory"); } } while (0)
; #define MD_B_WAIT(sb, N) asm volatile("s_waitcnt vmcnt(%8)" : "+v"(sb[0]), "+v"(sb[1]), "+v"(sb[2]), "+v"(sb[3]), "+v"(sb[4]), "+v"(sb[5]), "+v"(sb[6]), "+v"(sb[7]) : "n"(N) : "memory")
; __device__ __forceinline__ void moe_down_stream(PG8_LAS unsigned char* lds, int e, int cb0, int slot0, int nv, const bf16_t* HIDp, const float* Wd, bf16_t* Y, const float* slot_w, const int* slot_dst) {
;     ...
;     f32x4 acc[DNM][4];
; #pragma unroll
;     for (int m = 0; m < DNM; ++m)
; #pragma unroll
;         for (int n = 0; n < 4; ++n) acc[m][n] = (f32x4){0.f, 0.f, 0.f, 0.f};
;     f32x2 s0[8], s1[8];
;     MD_GLDS_A(0, 0); MD_B_ISSUE(s0, 0); MD_B_ISSUE(s1, 1);
;     MD_B_WAIT(s0, 8); MD_B_WRITE(s0, 0); __builtin_amdgcn_sched_barrier(0); MD_B_ISSUE(s0, 2);
;     asm volatile("s_waitcnt vmcnt(16)" ::: "memory");
;     asm volatile("s_waitcnt lgkmcnt(0)" ::: "memory"); __builtin_amdgcn_s_barrier(); asm volatile("" ::: "memory");
; #pragma unroll 1
;     for (int t = 0; t < NT; t += 2) {
;         if (t + 2 < NT) MD_B_WAIT(s1, 8); else MD_B_WAIT(s1, 0);
;         MD_B_WRITE(s1, 1); __builtin_amdgcn_sched_barrier(0); MD_GLDS_A(1, t + 1); __builtin_amdgcn_sched_barrier(0);
;         if (t + 3 < NT) MD_B_ISSUE(s1, t + 3);
;         MD_COMPUTE(0);
;         MD_END(t + 3 >= NT);
;         if (t + 2 < NT) { MD_B_WAIT(s0, 8); MD_B_WRITE(s0, 0); __builtin_amdgcn_sched_barrier(0); MD_GLDS_A(0, t + 2); __builtin_amdgcn_sched_barrier(0); }
;         if (t + 4 < NT) MD_B_ISSUE(s0, t + 4);
;         MD_COMPUTE(1);
;         MD_END(t + 4 >= NT);
	s_mov_b32 s49, s46
	s_mov_b32 s46, s47
	s_mov_b32 s47, s48
	s_mov_b32 s48, s49
	s_add_i32 s50, s50, 1
	v_cvt_pk_bf16_f32 v172, v114, v116
	v_cvt_pk_bf16_f32 v173, v118, v120
	v_cvt_pk_bf16_f32 v174, v122, v124
	v_cvt_pk_bf16_f32 v175, v126, v128
	v_cvt_pk_bf16_f32 v176, v115, v117
	v_cvt_pk_bf16_f32 v177, v119, v121
	v_cvt_pk_bf16_f32 v178, v123, v125
	v_cvt_pk_bf16_f32 v179, v127, v129
	ds_write_b128 v95, v[172:175] offset:19456
	ds_write_b128 v95, v[176:179] offset:19584
	v_add_u32_e32 v91, s46, v135
	v_add_u32_e32 v93, s46, v137
	ds_read_b128 v[238:241], v139 offset:0
	ds_read_b128 v[242:245], v139 offset:2048
	ds_read_b128 v[246:249], v139 offset:4096
	ds_read_b128 v[250:253], v139 offset:6144
	ds_read_b128 v[218:221], v91 offset:0
	ds_read_b128 v[222:225], v91 offset:2048
	ds_read_b128 v[226:229], v91 offset:4096
	ds_read_b128 v[230:233], v91 offset:6144
	ds_read_b128 v[234:237], v91 offset:8192
	s_add_i32 s49, s48, s74
	s_add_i32 s52, s52, 1
	s_and_b32 s54, s52, 7
	s_cmp_eq_u32 s54, 0
	s_cselect_b32 s54, s53, s32
	s_cselect_b32 s55, -1, 0
	s_add_u32 s30, s30, s54
	s_addc_u32 s31, s31, s55
	s_waitcnt lgkmcnt(0)
	v_mfma_f32_16x16x32_bf16 v[78:81], v[238:241], v[218:221], v[78:81]
	v_mfma_f32_16x16x32_bf16 v[74:77], v[242:245], v[218:221], v[74:77]
	v_mfma_f32_16x16x32_bf16 v[70:73], v[246:249], v[218:221], v[70:73]
	v_mfma_f32_16x16x32_bf16 v[66:69], v[250:253], v[218:221], v[66:69]
	ds_read_b128 v[218:221], v93 offset:0
	ds_read_b128 v[142:145], v141 offset:0
	s_mov_b32 m0, s49
	s_nop 0
	global_load_lds_dwordx4 v88, s[30:31]
	v_mfma_f32_16x16x32_bf16 v[62:65], v[238:241], v[222:225], v[62:65]
	v_mfma_f32_16x16x32_bf16 v[58:61], v[242:245], v[222:225], v[58:61]
	v_mfma_f32_16x16x32_bf16 v[54:57], v[246:249], v[222:225], v[54:57]
	v_mfma_f32_16x16x32_bf16 v[50:53], v[250:253], v[222:225], v[50:53]
	ds_read_b128 v[222:225], v93 offset:2048
	ds_read_b128 v[146:149], v141 offset:2048
	s_add_i32 m0, s49, 0x2000
	s_nop 0
	global_load_lds_dwordx4 v90, s[30:31]
	v_mfma_f32_16x16x32_bf16 v[46:49], v[238:241], v[226:229], v[46:49]
	v_mfma_f32_16x16x32_bf16 v[42:45], v[242:245], v[226:229], v[42:45]
	v_mfma_f32_16x16x32_bf16 v[38:41], v[246:249], v[226:229], v[38:41]
	v_mfma_f32_16x16x32_bf16 v[34:37], v[250:253], v[226:229], v[34:37]
	ds_read_b128 v[226:229], v93 offset:4096
	ds_read_b128 v[156:159], v141 offset:4096
	s_add_i32 m0, s49, 0x4000
	s_nop 0
	global_load_lds_dwordx4 v92, s[30:31]
	v_mfma_f32_16x16x32_bf16 v[18:21], v[238:241], v[230:233], v[18:21]
	v_mfma_f32_16x16x32_bf16 v[22:25], v[242:245], v[230:233], v[22:25]
	v_mfma_f32_16x16x32_bf16 v[26:29], v[246:249], v[230:233], v[26:29]
	v_mfma_f32_16x16x32_bf16 v[30:33], v[250:253], v[230:233], v[30:33]
	ds_read_b128 v[230:233], v93 offset:6144
	ds_read_b128 v[160:163], v141 offset:6144
	s_add_i32 m0, s49, 0x6000
	s_nop 0
	global_load_lds_dwordx4 v94, s[30:31]
	v_mfma_f32_16x16x32_bf16 v[2:5], v[238:241], v[234:237], v[2:5]
	v_mfma_f32_16x16x32_bf16 v[6:9], v[242:245], v[234:237], v[6:9]
	v_mfma_f32_16x16x32_bf16 v[10:13], v[246:249], v[234:237], v[10:13]
	v_mfma_f32_16x16x32_bf16 v[14:17], v[250:253], v[234:237], v[14:17]
	ds_read_b128 v[234:237], v93 offset:8192
	s_add_i32 m0, s49, 0x8000
	s_nop 0
	global_load_lds_dwordx4 v96, s[30:31]
	s_waitcnt lgkmcnt(0)
	v_mfma_f32_16x16x32_bf16 v[78:81], v[142:145], v[218:221], v[78:81]
	v_mfma_f32_16x16x32_bf16 v[74:77], v[146:149], v[218:221], v[74:77]
	v_mfma_f32_16x16x32_bf16 v[70:73], v[156:159], v[218:221], v[70:73]
	v_mfma_f32_16x16x32_bf16 v[66:69], v[160:163], v[218:221], v[66:69]
	v_mfma_f32_16x16x32_bf16 v[62:65], v[142:145], v[222:225], v[62:65]
	v_mfma_f32_16x16x32_bf16 v[58:61], v[146:149], v[222:225], v[58:61]
	v_mfma_f32_16x16x32_bf16 v[54:57], v[156:159], v[222:225], v[54:57]
	v_mfma_f32_16x16x32_bf16 v[50:53], v[160:163], v[222:225], v[50:53]
	v_mfma_f32_16x16x32_bf16 v[46:49], v[142:145], v[226:229], v[46:49]
	v_mfma_f32_16x16x32_bf16 v[42:45], v[146:149], v[226:229], v[42:45]
	v_mfma_f32_16x16x32_bf16 v[38:41], v[156:159], v[226:229], v[38:41]
	v_mfma_f32_16x16x32_bf16 v[34:37], v[160:163], v[226:229], v[34:37]
	v_mfma_f32_16x16x32_bf16 v[18:21], v[142:145], v[230:233], v[18:21]
	v_mfma_f32_16x16x32_bf16 v[22:25], v[146:149], v[230:233], v[22:25]
	v_mfma_f32_16x16x32_bf16 v[26:29], v[156:159], v[230:233], v[26:29]
	v_mfma_f32_16x16x32_bf16 v[30:33], v[160:163], v[230:233], v[30:33]
	v_mfma_f32_16x16x32_bf16 v[2:5], v[142:145], v[234:237], v[2:5]
	v_mfma_f32_16x16x32_bf16 v[6:9], v[146:149], v[234:237], v[6:9]
	v_mfma_f32_16x16x32_bf16 v[10:13], v[156:159], v[234:237], v[10:13]
	v_mfma_f32_16x16x32_bf16 v[14:17], v[160:163], v[234:237], v[14:17]
	s_waitcnt vmcnt(5)
	s_waitcnt lgkmcnt(0)
	s_barrier
; #define MD_GLDS_A(buf, tau) do { _Pragma("unroll") for (int i = 0; i < 5; ++i) if (amask & (1u << i)) \
;         __builtin_amdgcn_global_load_lds((const unsigned*)((const char*)HIDp + aoff[i] + (size_t)((tau) & 7) * 128), (PG8_LAS unsigned*)(MD_SA(buf) + wid * 1024 + i * 8192), 16, 0, 0); } while (0)
; #define MD_B_ISSUE(sb, tau) do { const char* kb_ = Bb + (size_t)((tau) >> 3) * 512 + (size_t)((tau) & 7) * (64 * (size_t)RB); _Pragma("unroll") for (int j = 0; j < 8; ++j) { const char* p_ = kb_ + (size_t)j * RB; \
;         asm volatile("global_load_dwordx2 %0, %1, off" : "=&v"(sb[j]) : "v"(p_) : "memory"); } } while (0)
; #define MD_B_WAIT(sb, N) asm volatile("s_waitcnt vmcnt(%8)" : "+v"(sb[0]), "+v"(sb[1]), "+v"(sb[2]), "+v"(sb[3]), "+v"(sb[4]), "+v"(sb[5]), "+v"(sb[6]), "+v"(sb[7]) : "n"(N) : "memory")
; __device__ __forceinline__ void moe_down_stream(PG8_LAS unsigned char* lds, int e, int cb0, int slot0, int nv, const bf16_t* HIDp, const float* Wd, bf16_t* Y, const float* slot_w, const int* slot_dst) {
;     ...
;     f32x4 acc[DNM][4];
; #pragma unroll
;     for (int m = 0; m < DNM; ++m)
; #pragma unroll
;         for (int n = 0; n < 4; ++n) acc[m][n] = (f32x4){0.f, 0.f, 0.f, 0.f};
;     f32x2 s0[8], s1[8];
;     MD_GLDS_A(0, 0); MD_B_ISSUE(s0, 0); MD_B_ISSUE(s1, 1);
;     MD_B_WAIT(s0, 8); MD_B_WRITE(s0, 0); __builtin_amdgcn_sched_barrier(0); MD_B_ISSUE(s0, 2);
;     asm volatile("s_waitcnt vmcnt(16)" ::: "memory");
;     asm volatile("s_waitcnt lgkmcnt(0)" ::: "memory"); __builtin_amdgcn_s_barrier(); asm volatile("" ::: "memory");
; #pragma unroll 1
;     for (int t = 0; t < NT; t += 2) {
;         if (t + 2 < NT) MD_B_WAIT(s1, 8); else MD_B_WAIT(s1, 0);
;         MD_B_WRITE(s1, 1); __builtin_amdgcn_sched_barrier(0); MD_GLDS_A(1, t + 1); __builtin_amdgcn_sched_barrier(0);
;         if (t + 3 < NT) MD_B_ISSUE(s1, t + 3);
;         MD_COMPUTE(0);
;         MD_END(t + 3 >= NT);
;         if (t + 2 < NT) { MD_B_WAIT(s0, 8); MD_B_WRITE(s0, 0); __builtin_amdgcn_sched_barrier(0); MD_GLDS_A(0, t + 2); __builtin_amdgcn_sched_barrier(0); }
;         if (t + 4 < NT) MD_B_ISSUE(s0, t + 4);
;         MD_COMPUTE(1);
;         MD_END(t + 4 >= NT);
	s_mov_b32 s49, s46
	s_mov_b32 s46, s47
	s_mov_b32 s47, s48
	s_mov_b32 s48, s49
	s_add_i32 s50, s50, 1
	v_cvt_pk_bf16_f32 v172, v186, v188
	v_cvt_pk_bf16_f32 v173, v190, v192
	v_cvt_pk_bf16_f32 v174, v194, v196
	v_cvt_pk_bf16_f32 v175, v198, v200
	v_cvt_pk_bf16_f32 v176, v187, v189
	v_cvt_pk_bf16_f32 v177, v191, v193
	v_cvt_pk_bf16_f32 v178, v195, v197
	v_cvt_pk_bf16_f32 v179, v199, v201
	ds_write_b128 v95, v[172:175] offset:0
	ds_write_b128 v95, v[176:179] offset:128
	v_add_u32_e32 v91, s46, v135
	v_add_u32_e32 v93, s46, v137
	ds_read_b128 v[238:241], v139 offset:19456
	ds_read_b128 v[242:245], v139 offset:21504
	ds_read_b128 v[246:249], v139 offset:23552
	ds_read_b128 v[250:253], v139 offset:25600
	ds_read_b128 v[218:221], v91 offset:0
	ds_read_b128 v[222:225], v91 offset:2048
	ds_read_b128 v[226:229], v91 offset:4096
	ds_read_b128 v[230:233], v91 offset:6144
	ds_read_b128 v[234:237], v91 offset:8192
	s_add_i32 s49, s48, s74
	s_add_i32 s52, s52, 1
	s_and_b32 s54, s52, 7
	s_cmp_eq_u32 s54, 0
	s_cselect_b32 s54, s53, s32
	s_cselect_b32 s55, -1, 0
	s_add_u32 s30, s30, s54
	s_addc_u32 s31, s31, s55
	s_waitcnt lgkmcnt(0)
	v_mfma_f32_16x16x32_bf16 v[78:81], v[238:241], v[218:221], v[78:81]
	v_mfma_f32_16x16x32_bf16 v[74:77], v[242:245], v[218:221], v[74:77]
	v_mfma_f32_16x16x32_bf16 v[70:73], v[246:249], v[218:221], v[70:73]
	v_mfma_f32_16x16x32_bf16 v[66:69], v[250:253], v[218:221], v[66:69]
	ds_read_b128 v[218:221], v93 offset:0
	ds_read_b128 v[142:145], v141 offset:19456
	s_mov_b32 m0, s49
	s_nop 0
	global_load_lds_dwordx4 v88, s[30:31]
	v_mfma_f32_16x16x32_bf16 v[62:65], v[238:241], v[222:225], v[62:65]
	v_mfma_f32_16x16x32_bf16 v[58:61], v[242:245], v[222:225], v[58:61]
	v_mfma_f32_16x16x32_bf16 v[54:57], v[246:249], v[222:225], v[54:57]
	v_mfma_f32_16x16x32_bf16 v[50:53], v[250:253], v[222:225], v[50:53]
	ds_read_b128 v[222:225], v93 offset:2048
	ds_read_b128 v[146:149], v141 offset:21504
	s_add_i32 m0, s49, 0x2000
	s_nop 0
	global_load_lds_dwordx4 v90, s[30:31]
	v_mfma_f32_16x16x32_bf16 v[46:49], v[238:241], v[226:229], v[46:49]
	v_mfma_f32_16x16x32_bf16 v[42:45], v[242:245], v[226:229], v[42:45]
	v_mfma_f32_16x16x32_bf16 v[38:41], v[246:249], v[226:229], v[38:41]
	v_mfma_f32_16x16x32_bf16 v[34:37], v[250:253], v[226:229], v[34:37]
	ds_read_b128 v[226:229], v93 offset:4096
	ds_read_b128 v[156:159], v141 offset:23552
	s_add_i32 m0, s49, 0x4000
	s_nop 0
	global_load_lds_dwordx4 v92, s[30:31]
	v_mfma_f32_16x16x32_bf16 v[18:21], v[238:241], v[230:233], v[18:21]
	v_mfma_f32_16x16x32_bf16 v[22:25], v[242:245], v[230:233], v[22:25]
	v_mfma_f32_16x16x32_bf16 v[26:29], v[246:249], v[230:233], v[26:29]
	v_mfma_f32_16x16x32_bf16 v[30:33], v[250:253], v[230:233], v[30:33]
	ds_read_b128 v[230:233], v93 offset:6144
	ds_read_b128 v[160:163], v141 offset:25600
	s_add_i32 m0, s49, 0x6000
	s_nop 0
	global_load_lds_dwordx4 v94, s[30:31]
	v_mfma_f32_16x16x32_bf16 v[2:5], v[238:241], v[234:237], v[2:5]
	v_mfma_f32_16x16x32_bf16 v[6:9], v[242:245], v[234:237], v[6:9]
	v_mfma_f32_16x16x32_bf16 v[10:13], v[246:249], v[234:237], v[10:13]
	v_mfma_f32_16x16x32_bf16 v[14:17], v[250:253], v[234:237], v[14:17]
	ds_read_b128 v[234:237], v93 offset:8192
	s_add_i32 m0, s49, 0x8000
	s_nop 0
	global_load_lds_dwordx4 v96, s[30:31]
	s_waitcnt lgkmcnt(0)
	v_mfma_f32_16x16x32_bf16 v[78:81], v[142:145], v[218:221], v[78:81]
	v_mfma_f32_16x16x32_bf16 v[74:77], v[146:149], v[218:221], v[74:77]
	v_mfma_f32_16x16x32_bf16 v[70:73], v[156:159], v[218:221], v[70:73]
	v_mfma_f32_16x16x32_bf16 v[66:69], v[160:163], v[218:221], v[66:69]
	v_mfma_f32_16x16x32_bf16 v[62:65], v[142:145], v[222:225], v[62:65]
	v_mfma_f32_16x16x32_bf16 v[58:61], v[146:149], v[222:225], v[58:61]
	v_mfma_f32_16x16x32_bf16 v[54:57], v[156:159], v[222:225], v[54:57]
	v_mfma_f32_16x16x32_bf16 v[50:53], v[160:163], v[222:225], v[50:53]
	v_mfma_f32_16x16x32_bf16 v[46:49], v[142:145], v[226:229], v[46:49]
	v_mfma_f32_16x16x32_bf16 v[42:45], v[146:149], v[226:229], v[42:45]
	v_mfma_f32_16x16x32_bf16 v[38:41], v[156:159], v[226:229], v[38:41]
	v_mfma_f32_16x16x32_bf16 v[34:37], v[160:163], v[226:229], v[34:37]
	v_mfma_f32_16x16x32_bf16 v[18:21], v[142:145], v[230:233], v[18:21]
	v_mfma_f32_16x16x32_bf16 v[22:25], v[146:149], v[230:233], v[22:25]
	v_mfma_f32_16x16x32_bf16 v[26:29], v[156:159], v[230:233], v[26:29]
	v_mfma_f32_16x16x32_bf16 v[30:33], v[160:163], v[230:233], v[30:33]
	v_mfma_f32_16x16x32_bf16 v[2:5], v[142:145], v[234:237], v[2:5]
	v_mfma_f32_16x16x32_bf16 v[6:9], v[146:149], v[234:237], v[6:9]
	v_mfma_f32_16x16x32_bf16 v[10:13], v[156:159], v[234:237], v[10:13]
	v_mfma_f32_16x16x32_bf16 v[14:17], v[160:163], v[234:237], v[14:17]
	s_waitcnt vmcnt(5)
	s_waitcnt lgkmcnt(0)
	s_barrier
; #define MD_GLDS_A(buf, tau) do { _Pragma("unroll") for (int i = 0; i < 5; ++i) if (amask & (1u << i)) \
;         __builtin_amdgcn_global_load_lds((const unsigned*)((const char*)HIDp + aoff[i] + (size_t)((tau) & 7) * 128), (PG8_LAS unsigned*)(MD_SA(buf) + wid * 1024 + i * 8192), 16, 0, 0); } while (0)
; #define MD_B_ISSUE(sb, tau) do { const char* kb_ = Bb + (size_t)((tau) >> 3) * 512 + (size_t)((tau) & 7) * (64 * (size_t)RB); _Pragma("unroll") for (int j = 0; j < 8; ++j) { const char* p_ = kb_ + (size_t)j * RB; \
;         asm volatile("global_load_dwordx2 %0, %1, off" : "=&v"(sb[j]) : "v"(p_) : "memory"); } } while (0)
; #define MD_B_WAIT(sb, N) asm volatile("s_waitcnt vmcnt(%8)" : "+v"(sb[0]), "+v"(sb[1]), "+v"(sb[2]), "+v"(sb[3]), "+v"(sb[4]), "+v"(sb[5]), "+v"(sb[6]), "+v"(sb[7]) : "n"(N) : "memory")
; __device__ __forceinline__ void moe_down_stream(PG8_LAS unsigned char* lds, int e, int cb0, int slot0, int nv, const bf16_t* HIDp, const float* Wd, bf16_t* Y, const float* slot_w, const int* slot_dst) {
;     ...
;     f32x4 acc[DNM][4];
; #pragma unroll
;     for (int m = 0; m < DNM; ++m)
; #pragma unroll
;         for (int n = 0; n < 4; ++n) acc[m][n] = (f32x4){0.f, 0.f, 0.f, 0.f};
;     f32x2 s0[8], s1[8];
;     MD_GLDS_A(0, 0); MD_B_ISSUE(s0, 0); MD_B_ISSUE(s1, 1);
;     MD_B_WAIT(s0, 8); MD_B_WRITE(s0, 0); __builtin_amdgcn_sched_barrier(0); MD_B_ISSUE(s0, 2);
;     asm volatile("s_waitcnt vmcnt(16)" ::: "memory");
;     asm volatile("s_waitcnt lgkmcnt(0)" ::: "memory"); __builtin_amdgcn_s_barrier(); asm volatile("" ::: "memory");
; #pragma unroll 1
;     for (int t = 0; t < NT; t += 2) {
;         if (t + 2 < NT) MD_B_WAIT(s1, 8); else MD_B_WAIT(s1, 0);
;         MD_B_WRITE(s1, 1); __builtin_amdgcn_sched_barrier(0); MD_GLDS_A(1, t + 1); __builtin_amdgcn_sched_barrier(0);
;         if (t + 3 < NT) MD_B_ISSUE(s1, t + 3);
;         MD_COMPUTE(0);
;         MD_END(t + 3 >= NT);
;         if (t + 2 < NT) { MD_B_WAIT(s0, 8); MD_B_WRITE(s0, 0); __builtin_amdgcn_sched_barrier(0); MD_GLDS_A(0, t + 2); __builtin_amdgcn_sched_barrier(0); }
;         if (t + 4 < NT) MD_B_ISSUE(s0, t + 4);
;         MD_COMPUTE(1);
;         MD_END(t + 4 >= NT);
	s_mov_b32 s49, s46
	s_mov_b32 s46, s47
	s_mov_b32 s47, s48
	s_mov_b32 s48, s49
	s_add_i32 s50, s50, 1
	v_cvt_pk_bf16_f32 v172, v202, v204
	v_cvt_pk_bf16_f32 v173, v206, v208
	v_cvt_pk_bf16_f32 v174, v210, v212
	v_cvt_pk_bf16_f32 v175, v214, v216
	v_cvt_pk_bf16_f32 v176, v203, v205
	v_cvt_pk_bf16_f32 v177, v207, v209
	v_cvt_pk_bf16_f32 v178, v211, v213
	v_cvt_pk_bf16_f32 v179, v215, v217
	ds_write_b128 v95, v[172:175] offset:19456
	ds_write_b128 v95, v[176:179] offset:19584
	v_add_u32_e32 v91, s46, v135
	v_add_u32_e32 v93, s46, v137
	ds_read_b128 v[238:241], v139 offset:0
	ds_read_b128 v[242:245], v139 offset:2048
	ds_read_b128 v[246:249], v139 offset:4096
	ds_read_b128 v[250:253], v139 offset:6144
	ds_read_b128 v[218:221], v91 offset:0
	ds_read_b128 v[222:225], v91 offset:2048
	ds_read_b128 v[226:229], v91 offset:4096
	ds_read_b128 v[230:233], v91 offset:6144
	ds_read_b128 v[234:237], v91 offset:8192
	s_waitcnt lgkmcnt(0)
	v_mfma_f32_16x16x32_bf16 v[78:81], v[238:241], v[218:221], v[78:81]
	v_mfma_f32_16x16x32_bf16 v[74:77], v[242:245], v[218:221], v[74:77]
	v_mfma_f32_16x16x32_bf16 v[70:73], v[246:249], v[218:221], v[70:73]
	v_mfma_f32_16x16x32_bf16 v[66:69], v[250:253], v[218:221], v[66:69]
	ds_read_b128 v[218:221], v93 offset:0
	ds_read_b128 v[142:145], v141 offset:0
	v_mfma_f32_16x16x32_bf16 v[62:65], v[238:241], v[222:225], v[62:65]
	v_mfma_f32_16x16x32_bf16 v[58:61], v[242:245], v[222:225], v[58:61]
	v_mfma_f32_16x16x32_bf16 v[54:57], v[246:249], v[222:225], v[54:57]
	v_mfma_f32_16x16x32_bf16 v[50:53], v[250:253], v[222:225], v[50:53]
	ds_read_b128 v[222:225], v93 offset:2048
	ds_read_b128 v[146:149], v141 offset:2048
	v_mfma_f32_16x16x32_bf16 v[46:49], v[238:241], v[226:229], v[46:49]
	v_mfma_f32_16x16x32_bf16 v[42:45], v[242:245], v[226:229], v[42:45]
	v_mfma_f32_16x16x32_bf16 v[38:41], v[246:249], v[226:229], v[38:41]
	v_mfma_f32_16x16x32_bf16 v[34:37], v[250:253], v[226:229], v[34:37]
	ds_read_b128 v[226:229], v93 offset:4096
	ds_read_b128 v[156:159], v141 offset:4096
	v_mfma_f32_16x16x32_bf16 v[18:21], v[238:241], v[230:233], v[18:21]
	v_mfma_f32_16x16x32_bf16 v[22:25], v[242:245], v[230:233], v[22:25]
	v_mfma_f32_16x16x32_bf16 v[26:29], v[246:249], v[230:233], v[26:29]
	v_mfma_f32_16x16x32_bf16 v[30:33], v[250:253], v[230:233], v[30:33]
	ds_read_b128 v[230:233], v93 offset:6144
	ds_read_b128 v[160:163], v141 offset:6144
	v_mfma_f32_16x16x32_bf16 v[2:5], v[238:241], v[234:237], v[2:5]
	v_mfma_f32_16x16x32_bf16 v[6:9], v[242:245], v[234:237], v[6:9]
	v_mfma_f32_16x16x32_bf16 v[10:13], v[246:249], v[234:237], v[10:13]
	v_mfma_f32_16x16x32_bf16 v[14:17], v[250:253], v[234:237], v[14:17]
	ds_read_b128 v[234:237], v93 offset:8192
	s_waitcnt lgkmcnt(0)
	v_mfma_f32_16x16x32_bf16 v[78:81], v[142:145], v[218:221], v[78:81]
	v_mfma_f32_16x16x32_bf16 v[74:77], v[146:149], v[218:221], v[74:77]
	v_mfma_f32_16x16x32_bf16 v[70:73], v[156:159], v[218:221], v[70:73]
	v_mfma_f32_16x16x32_bf16 v[66:69], v[160:163], v[218:221], v[66:69]
	v_mfma_f32_16x16x32_bf16 v[62:65], v[142:145], v[222:225], v[62:65]
	v_mfma_f32_16x16x32_bf16 v[58:61], v[146:149], v[222:225], v[58:61]
	v_mfma_f32_16x16x32_bf16 v[54:57], v[156:159], v[222:225], v[54:57]
	v_mfma_f32_16x16x32_bf16 v[50:53], v[160:163], v[222:225], v[50:53]
	v_mfma_f32_16x16x32_bf16 v[46:49], v[142:145], v[226:229], v[46:49]
	v_mfma_f32_16x16x32_bf16 v[42:45], v[146:149], v[226:229], v[42:45]
	v_mfma_f32_16x16x32_bf16 v[38:41], v[156:159], v[226:229], v[38:41]
	v_mfma_f32_16x16x32_bf16 v[34:37], v[160:163], v[226:229], v[34:37]
	v_mfma_f32_16x16x32_bf16 v[18:21], v[142:145], v[230:233], v[18:21]
	v_mfma_f32_16x16x32_bf16 v[22:25], v[146:149], v[230:233], v[22:25]
	v_mfma_f32_16x16x32_bf16 v[26:29], v[156:159], v[230:233], v[26:29]
	v_mfma_f32_16x16x32_bf16 v[30:33], v[160:163], v[230:233], v[30:33]
	v_mfma_f32_16x16x32_bf16 v[2:5], v[142:145], v[234:237], v[2:5]
	v_mfma_f32_16x16x32_bf16 v[6:9], v[146:149], v[234:237], v[6:9]
	v_mfma_f32_16x16x32_bf16 v[10:13], v[156:159], v[234:237], v[10:13]
	v_mfma_f32_16x16x32_bf16 v[14:17], v[160:163], v[234:237], v[14:17]
	s_waitcnt vmcnt(0)
	s_waitcnt lgkmcnt(0)
	s_barrier
	s_mov_b32 s49, s46
	s_mov_b32 s46, s47
	s_mov_b32 s47, s48
	s_mov_b32 s48, s49
	s_add_i32 s50, s50, 1
	v_add_u32_e32 v91, s46, v135
	v_add_u32_e32 v93, s46, v137
	ds_read_b128 v[238:241], v139 offset:19456
	ds_read_b128 v[242:245], v139 offset:21504
	ds_read_b128 v[246:249], v139 offset:23552
	ds_read_b128 v[250:253], v139 offset:25600
	ds_read_b128 v[218:221], v91 offset:0
	ds_read_b128 v[222:225], v91 offset:2048
	ds_read_b128 v[226:229], v91 offset:4096
	ds_read_b128 v[230:233], v91 offset:6144
	ds_read_b128 v[234:237], v91 offset:8192
	s_waitcnt lgkmcnt(0)
	v_mfma_f32_16x16x32_bf16 v[78:81], v[238:241], v[218:221], v[78:81]
	v_mfma_f32_16x16x32_bf16 v[74:77], v[242:245], v[218:221], v[74:77]
	v_mfma_f32_16x16x32_bf16 v[70:73], v[246:249], v[218:221], v[70:73]
	v_mfma_f32_16x16x32_bf16 v[66:69], v[250:253], v[218:221], v[66:69]
	ds_read_b128 v[218:221], v93 offset:0
	ds_read_b128 v[142:145], v141 offset:19456
	v_mfma_f32_16x16x32_bf16 v[62:65], v[238:241], v[222:225], v[62:65]
	v_mfma_f32_16x16x32_bf16 v[58:61], v[242:245], v[222:225], v[58:61]
	v_mfma_f32_16x16x32_bf16 v[54:57], v[246:249], v[222:225], v[54:57]
	v_mfma_f32_16x16x32_bf16 v[50:53], v[250:253], v[222:225], v[50:53]
	ds_read_b128 v[222:225], v93 offset:2048
	ds_read_b128 v[146:149], v141 offset:21504
	v_mfma_f32_16x16x32_bf16 v[46:49], v[238:241], v[226:229], v[46:49]
	v_mfma_f32_16x16x32_bf16 v[42:45], v[242:245], v[226:229], v[42:45]
	v_mfma_f32_16x16x32_bf16 v[38:41], v[246:249], v[226:229], v[38:41]
	v_mfma_f32_16x16x32_bf16 v[34:37], v[250:253], v[226:229], v[34:37]
	ds_read_b128 v[226:229], v93 offset:4096
	ds_read_b128 v[156:159], v141 offset:23552
	v_mfma_f32_16x16x32_bf16 v[18:21], v[238:241], v[230:233], v[18:21]
	v_mfma_f32_16x16x32_bf16 v[22:25], v[242:245], v[230:233], v[22:25]
	v_mfma_f32_16x16x32_bf16 v[26:29], v[246:249], v[230:233], v[26:29]
	v_mfma_f32_16x16x32_bf16 v[30:33], v[250:253], v[230:233], v[30:33]
	ds_read_b128 v[230:233], v93 offset:6144
	ds_read_b128 v[160:163], v141 offset:25600
	v_mfma_f32_16x16x32_bf16 v[2:5], v[238:241], v[234:237], v[2:5]
	v_mfma_f32_16x16x32_bf16 v[6:9], v[242:245], v[234:237], v[6:9]
	v_mfma_f32_16x16x32_bf16 v[10:13], v[246:249], v[234:237], v[10:13]
	v_mfma_f32_16x16x32_bf16 v[14:17], v[250:253], v[234:237], v[14:17]
	ds_read_b128 v[234:237], v93 offset:8192
	s_waitcnt lgkmcnt(0)
; #define PG8_LAS __attribute__((address_space(3)))
; __device__ __forceinline__ unsigned cvtpk(float lo, float hi) { f32x2 v = {lo, hi}; bf16x2_t b = __builtin_convertvector(v, bf16x2_t); return __builtin_bit_cast(unsigned, b); }
; __device__ __forceinline__ void moe_down_stream(PG8_LAS unsigned char* lds, int e, int cb0, int slot0, int nv, const bf16_t* HIDp, const float* Wd, bf16_t* Y, const float* slot_w, const int* slot_dst) {
;     ...
;         if (((t + 1) & 7) == 7) {
;             const int cb = cb0 + ((t + 1) >> 3);
; #pragma unroll
;             for (int m = 0; m < DNM; ++m) {
;                 const float w_ = lw[4 * (16 * m + fr) + wr];
; #pragma unroll
;                 for (int p = 0; p < 2; ++p) { const f32x4 v0 = acc[m][2 * p] * w_, v1 = acc[m][2 * p + 1] * w_; u32x4 w; w.x = cvtpk(v0[0], v0[1]); w.y = cvtpk(v0[2], v0[3]); w.z = cvtpk(v1[0], v1[1]); w.w = cvtpk(v1[2], v1[3]);
;                     *(PG8_LAS u32x4*)(stg + fr * 128 + (((4 * p + fq) ^ (fr & 7)) * 16)) = w; }
; #pragma unroll
;                 for (int hh = 0; hh < 2; ++hh) { const int r = (lane >> 3) + 8 * hh, cc = lane & 7; const u32x4 d = *(const PG8_LAS u32x4*)(stg + r * 128 + ((cc ^ (r & 7)) * 16)); const int dst_ = ldst[4 * (16 * m + r) + wr];
;                     if (dst_ >= 0) *(u32x4*)(Y + (size_t)dst_ * D + 128 * cb + 64 * wc + 8 * cc) = d; }
; #pragma unroll
;                 for (int n = 0; n < 4; ++n) acc[m][n] = (f32x4){0.f, 0.f, 0.f, 0.f}; } }
	v_mfma_f32_16x16x32_bf16 v[78:81], v[142:145], v[218:221], v[78:81]
	v_mfma_f32_16x16x32_bf16 v[74:77], v[146:149], v[218:221], v[74:77]
	v_mfma_f32_16x16x32_bf16 v[70:73], v[156:159], v[218:221], v[70:73]
	v_mfma_f32_16x16x32_bf16 v[66:69], v[160:163], v[218:221], v[66:69]
	v_mfma_f32_16x16x32_bf16 v[62:65], v[142:145], v[222:225], v[62:65]
	v_mfma_f32_16x16x32_bf16 v[58:61], v[146:149], v[222:225], v[58:61]
	v_mfma_f32_16x16x32_bf16 v[54:57], v[156:159], v[222:225], v[54:57]
	v_mfma_f32_16x16x32_bf16 v[50:53], v[160:163], v[222:225], v[50:53]
	v_mfma_f32_16x16x32_bf16 v[46:49], v[142:145], v[226:229], v[46:49]
	v_mfma_f32_16x16x32_bf16 v[42:45], v[146:149], v[226:229], v[42:45]
	v_mfma_f32_16x16x32_bf16 v[38:41], v[156:159], v[226:229], v[38:41]
	v_mfma_f32_16x16x32_bf16 v[34:37], v[160:163], v[226:229], v[34:37]
	v_mfma_f32_16x16x32_bf16 v[18:21], v[142:145], v[230:233], v[18:21]
	v_mfma_f32_16x16x32_bf16 v[22:25], v[146:149], v[230:233], v[22:25]
	v_mfma_f32_16x16x32_bf16 v[26:29], v[156:159], v[230:233], v[26:29]
	v_mfma_f32_16x16x32_bf16 v[30:33], v[160:163], v[230:233], v[30:33]
	v_mfma_f32_16x16x32_bf16 v[2:5], v[142:145], v[234:237], v[2:5]
	v_mfma_f32_16x16x32_bf16 v[6:9], v[146:149], v[234:237], v[6:9]
	v_mfma_f32_16x16x32_bf16 v[10:13], v[156:159], v[234:237], v[10:13]
	v_mfma_f32_16x16x32_bf16 v[14:17], v[160:163], v[234:237], v[14:17]
	s_waitcnt lgkmcnt(0)
	s_barrier
	s_mov_b32 s49, s46
	s_mov_b32 s46, s47
	s_mov_b32 s47, s48
	s_mov_b32 s48, s49
	s_add_i32 s50, s50, 1
	s_add_i32 s54, s48, s74
	v_add_u32_e32 v164, s54, v84
	v_add_u32_e32 v165, s54, v85
	ds_read_b32 v150, v82 offset:0
	ds_read_b32 v151, v83 offset:0
	ds_read_b32 v166, v83 offset:128
	s_waitcnt lgkmcnt(2)
	v_mul_f32_e32 v78, v150, v78
	v_mul_f32_e32 v79, v150, v79
	v_mul_f32_e32 v80, v150, v80
	v_mul_f32_e32 v81, v150, v81
	v_mul_f32_e32 v74, v150, v74
	v_mul_f32_e32 v75, v150, v75
	v_mul_f32_e32 v76, v150, v76
	v_mul_f32_e32 v77, v150, v77
	v_cvt_pk_bf16_f32 v182, v78, v79
	v_cvt_pk_bf16_f32 v183, v80, v81
	v_cvt_pk_bf16_f32 v184, v74, v75
	v_cvt_pk_bf16_f32 v185, v76, v77
	ds_write_b128 v164, v[182:185]
	v_mul_f32_e32 v70, v150, v70
	v_mul_f32_e32 v71, v150, v71
	v_mul_f32_e32 v72, v150, v72
	v_mul_f32_e32 v73, v150, v73
	v_mul_f32_e32 v66, v150, v66
	v_mul_f32_e32 v67, v150, v67
	v_mul_f32_e32 v68, v150, v68
	v_mul_f32_e32 v69, v150, v69
	v_cvt_pk_bf16_f32 v182, v70, v71
	v_cvt_pk_bf16_f32 v183, v72, v73
	v_cvt_pk_bf16_f32 v184, v66, v67
	v_cvt_pk_bf16_f32 v185, v68, v69
	v_xor_b32_e32 v167, 64, v164
	ds_write_b128 v167, v[182:185]
	v_mov_b32_e32 v78, 0
	v_mov_b32_e32 v74, 0
	v_mov_b32_e32 v70, 0
	v_mov_b32_e32 v66, 0
	v_mov_b32_e32 v79, 0
	v_mov_b32_e32 v75, 0
	v_mov_b32_e32 v71, 0
	v_mov_b32_e32 v67, 0
	v_mov_b32_e32 v80, 0
	v_mov_b32_e32 v76, 0
	v_mov_b32_e32 v72, 0
	v_mov_b32_e32 v68, 0
	v_mov_b32_e32 v81, 0
	v_mov_b32_e32 v77, 0
	v_mov_b32_e32 v73, 0
	v_mov_b32_e32 v69, 0
	ds_read_b128 v[182:185], v165 offset:0
	v_cmp_lt_i32_e32 vcc, -1, v151
	v_lshlrev_b32_e32 v148, 13, v151
	v_mov_b32_e32 v149, 0
	v_lshl_add_u64 v[148:149], v[148:149], 0, v[86:87]
	v_cndmask_b32_e32 v148, v168, v148, vcc
	v_cndmask_b32_e32 v149, v169, v149, vcc
	s_waitcnt lgkmcnt(0)
	global_store_dwordx4 v[148:149], v[182:185], off nt
	ds_read_b128 v[182:185], v165 offset:8192
	v_cmp_lt_i32_e32 vcc, -1, v166
	v_lshlrev_b32_e32 v148, 13, v166
	v_mov_b32_e32 v149, 0
	v_lshl_add_u64 v[148:149], v[148:149], 0, v[86:87]
	v_cndmask_b32_e32 v148, v168, v148, vcc
	v_cndmask_b32_e32 v149, v169, v149, vcc
	s_waitcnt lgkmcnt(0)
	global_store_dwordx4 v[148:149], v[182:185], off nt
	ds_read_b32 v150, v82 offset:256
	ds_read_b32 v151, v83 offset:256
	ds_read_b32 v166, v83 offset:384
	s_waitcnt lgkmcnt(2)
	v_mul_f32_e32 v62, v150, v62
	v_mul_f32_e32 v63, v150, v63
	v_mul_f32_e32 v64, v150, v64
	v_mul_f32_e32 v65, v150, v65
	v_mul_f32_e32 v58, v150, v58
	v_mul_f32_e32 v59, v150, v59
	v_mul_f32_e32 v60, v150, v60
	v_mul_f32_e32 v61, v150, v61
	v_cvt_pk_bf16_f32 v182, v62, v63
	v_cvt_pk_bf16_f32 v183, v64, v65
	v_cvt_pk_bf16_f32 v184, v58, v59
	v_cvt_pk_bf16_f32 v185, v60, v61
	ds_write_b128 v164, v[182:185]
	v_mul_f32_e32 v54, v150, v54
	v_mul_f32_e32 v55, v150, v55
	v_mul_f32_e32 v56, v150, v56
	v_mul_f32_e32 v57, v150, v57
	v_mul_f32_e32 v50, v150, v50
	v_mul_f32_e32 v51, v150, v51
	v_mul_f32_e32 v52, v150, v52
	v_mul_f32_e32 v53, v150, v53
	v_cvt_pk_bf16_f32 v182, v54, v55
	v_cvt_pk_bf16_f32 v183, v56, v57
	v_cvt_pk_bf16_f32 v184, v50, v51
	v_cvt_pk_bf16_f32 v185, v52, v53
	v_xor_b32_e32 v167, 64, v164
	ds_write_b128 v167, v[182:185]
	v_mov_b32_e32 v62, 0
	v_mov_b32_e32 v58, 0
	v_mov_b32_e32 v54, 0
	v_mov_b32_e32 v50, 0
	v_mov_b32_e32 v63, 0
	v_mov_b32_e32 v59, 0
	v_mov_b32_e32 v55, 0
	v_mov_b32_e32 v51, 0
	v_mov_b32_e32 v64, 0
	v_mov_b32_e32 v60, 0
	v_mov_b32_e32 v56, 0
	v_mov_b32_e32 v52, 0
	v_mov_b32_e32 v65, 0
	v_mov_b32_e32 v61, 0
	v_mov_b32_e32 v57, 0
	v_mov_b32_e32 v53, 0
	ds_read_b128 v[182:185], v165 offset:0
	v_cmp_lt_i32_e32 vcc, -1, v151
	v_lshlrev_b32_e32 v148, 13, v151
	v_mov_b32_e32 v149, 0
	v_lshl_add_u64 v[148:149], v[148:149], 0, v[86:87]
	v_cndmask_b32_e32 v148, v168, v148, vcc
	v_cndmask_b32_e32 v149, v169, v149, vcc
	s_waitcnt lgkmcnt(0)
	global_store_dwordx4 v[148:149], v[182:185], off nt
	ds_read_b128 v[182:185], v165 offset:8192
	v_cmp_lt_i32_e32 vcc, -1, v166
	v_lshlrev_b32_e32 v148, 13, v166
	v_mov_b32_e32 v149, 0
	v_lshl_add_u64 v[148:149], v[148:149], 0, v[86:87]
	v_cndmask_b32_e32 v148, v168, v148, vcc
	v_cndmask_b32_e32 v149, v169, v149, vcc
	s_waitcnt lgkmcnt(0)
	global_store_dwordx4 v[148:149], v[182:185], off nt
	ds_read_b32 v150, v82 offset:512
	ds_read_b32 v151, v83 offset:512
	ds_read_b32 v166, v83 offset:640
	s_waitcnt lgkmcnt(2)
; #define PG8_LAS __attribute__((address_space(3)))
; __device__ __forceinline__ unsigned cvtpk(float lo, float hi) { f32x2 v = {lo, hi}; bf16x2_t b = __builtin_convertvector(v, bf16x2_t); return __builtin_bit_cast(unsigned, b); }
; __device__ __forceinline__ void moe_down_stream(PG8_LAS unsigned char* lds, int e, int cb0, int slot0, int nv, const bf16_t* HIDp, const float* Wd, bf16_t* Y, const float* slot_w, const int* slot_dst) {
;     ...
;         if (((t + 1) & 7) == 7) {
;             const int cb = cb0 + ((t + 1) >> 3);
; #pragma unroll
;             for (int m = 0; m < DNM; ++m) {
;                 const float w_ = lw[4 * (16 * m + fr) + wr];
; #pragma unroll
;                 for (int p = 0; p < 2; ++p) { const f32x4 v0 = acc[m][2 * p] * w_, v1 = acc[m][2 * p + 1] * w_; u32x4 w; w.x = cvtpk(v0[0], v0[1]); w.y = cvtpk(v0[2], v0[3]); w.z = cvtpk(v1[0], v1[1]); w.w = cvtpk(v1[2], v1[3]);
;                     *(PG8_LAS u32x4*)(stg + fr * 128 + (((4 * p + fq) ^ (fr & 7)) * 16)) = w; }
; #pragma unroll
;                 for (int hh = 0; hh < 2; ++hh) { const int r = (lane >> 3) + 8 * hh, cc = lane & 7; const u32x4 d = *(const PG8_LAS u32x4*)(stg + r * 128 + ((cc ^ (r & 7)) * 16)); const int dst_ = ldst[4 * (16 * m + r) + wr];
;                     if (dst_ >= 0) *(u32x4*)(Y + (size_t)dst_ * D + 128 * cb + 64 * wc + 8 * cc) = d; }
; #pragma unroll
;                 for (int n = 0; n < 4; ++n) acc[m][n] = (f32x4){0.f, 0.f, 0.f, 0.f}; } }
	v_mul_f32_e32 v46, v150, v46
	v_mul_f32_e32 v47, v150, v47
	v_mul_f32_e32 v48, v150, v48
	v_mul_f32_e32 v49, v150, v49
	v_mul_f32_e32 v42, v150, v42
	v_mul_f32_e32 v43, v150, v43
	v_mul_f32_e32 v44, v150, v44
	v_mul_f32_e32 v45, v150, v45
	v_cvt_pk_bf16_f32 v182, v46, v47
	v_cvt_pk_bf16_f32 v183, v48, v49
	v_cvt_pk_bf16_f32 v184, v42, v43
	v_cvt_pk_bf16_f32 v185, v44, v45
	ds_write_b128 v164, v[182:185]
	v_mul_f32_e32 v38, v150, v38
	v_mul_f32_e32 v39, v150, v39
	v_mul_f32_e32 v40, v150, v40
	v_mul_f32_e32 v41, v150, v41
	v_mul_f32_e32 v34, v150, v34
	v_mul_f32_e32 v35, v150, v35
	v_mul_f32_e32 v36, v150, v36
	v_mul_f32_e32 v37, v150, v37
	v_cvt_pk_bf16_f32 v182, v38, v39
	v_cvt_pk_bf16_f32 v183, v40, v41
	v_cvt_pk_bf16_f32 v184, v34, v35
	v_cvt_pk_bf16_f32 v185, v36, v37
	v_xor_b32_e32 v167, 64, v164
	ds_write_b128 v167, v[182:185]
	v_mov_b32_e32 v46, 0
	v_mov_b32_e32 v42, 0
	v_mov_b32_e32 v38, 0
	v_mov_b32_e32 v34, 0
	v_mov_b32_e32 v47, 0
	v_mov_b32_e32 v43, 0
	v_mov_b32_e32 v39, 0
	v_mov_b32_e32 v35, 0
	v_mov_b32_e32 v48, 0
	v_mov_b32_e32 v44, 0
	v_mov_b32_e32 v40, 0
	v_mov_b32_e32 v36, 0
	v_mov_b32_e32 v49, 0
	v_mov_b32_e32 v45, 0
	v_mov_b32_e32 v41, 0
	v_mov_b32_e32 v37, 0
	ds_read_b128 v[182:185], v165 offset:0
	v_cmp_lt_i32_e32 vcc, -1, v151
	v_lshlrev_b32_e32 v148, 13, v151
	v_mov_b32_e32 v149, 0
	v_lshl_add_u64 v[148:149], v[148:149], 0, v[86:87]
	v_cndmask_b32_e32 v148, v168, v148, vcc
	v_cndmask_b32_e32 v149, v169, v149, vcc
	s_waitcnt lgkmcnt(0)
	global_store_dwordx4 v[148:149], v[182:185], off nt
	ds_read_b128 v[182:185], v165 offset:8192
	v_cmp_lt_i32_e32 vcc, -1, v166
	v_lshlrev_b32_e32 v148, 13, v166
	v_mov_b32_e32 v149, 0
	v_lshl_add_u64 v[148:149], v[148:149], 0, v[86:87]
	v_cndmask_b32_e32 v148, v168, v148, vcc
	v_cndmask_b32_e32 v149, v169, v149, vcc
	s_waitcnt lgkmcnt(0)
	global_store_dwordx4 v[148:149], v[182:185], off nt
	ds_read_b32 v150, v82 offset:768
	ds_read_b32 v151, v83 offset:768
	ds_read_b32 v166, v83 offset:896
	s_waitcnt lgkmcnt(2)
	v_mul_f32_e32 v18, v150, v18
	v_mul_f32_e32 v19, v150, v19
	v_mul_f32_e32 v20, v150, v20
	v_mul_f32_e32 v21, v150, v21
	v_mul_f32_e32 v22, v150, v22
	v_mul_f32_e32 v23, v150, v23
	v_mul_f32_e32 v24, v150, v24
	v_mul_f32_e32 v25, v150, v25
	v_cvt_pk_bf16_f32 v182, v18, v19
	v_cvt_pk_bf16_f32 v183, v20, v21
	v_cvt_pk_bf16_f32 v184, v22, v23
	v_cvt_pk_bf16_f32 v185, v24, v25
	ds_write_b128 v164, v[182:185]
	v_mul_f32_e32 v26, v150, v26
	v_mul_f32_e32 v27, v150, v27
	v_mul_f32_e32 v28, v150, v28
	v_mul_f32_e32 v29, v150, v29
	v_mul_f32_e32 v30, v150, v30
	v_mul_f32_e32 v31, v150, v31
	v_mul_f32_e32 v32, v150, v32
	v_mul_f32_e32 v33, v150, v33
	v_cvt_pk_bf16_f32 v182, v26, v27
	v_cvt_pk_bf16_f32 v183, v28, v29
	v_cvt_pk_bf16_f32 v184, v30, v31
	v_cvt_pk_bf16_f32 v185, v32, v33
	v_xor_b32_e32 v167, 64, v164
	ds_write_b128 v167, v[182:185]
	v_mov_b32_e32 v18, 0
	v_mov_b32_e32 v22, 0
	v_mov_b32_e32 v26, 0
	v_mov_b32_e32 v30, 0
	v_mov_b32_e32 v19, 0
	v_mov_b32_e32 v23, 0
	v_mov_b32_e32 v27, 0
	v_mov_b32_e32 v31, 0
	v_mov_b32_e32 v20, 0
	v_mov_b32_e32 v24, 0
	v_mov_b32_e32 v28, 0
	v_mov_b32_e32 v32, 0
	v_mov_b32_e32 v21, 0
	v_mov_b32_e32 v25, 0
	v_mov_b32_e32 v29, 0
	v_mov_b32_e32 v33, 0
	ds_read_b128 v[182:185], v165 offset:0
	v_cmp_lt_i32_e32 vcc, -1, v151
	v_lshlrev_b32_e32 v148, 13, v151
	v_mov_b32_e32 v149, 0
	v_lshl_add_u64 v[148:149], v[148:149], 0, v[86:87]
	v_cndmask_b32_e32 v148, v168, v148, vcc
	v_cndmask_b32_e32 v149, v169, v149, vcc
	s_waitcnt lgkmcnt(0)
	global_store_dwordx4 v[148:149], v[182:185], off nt
	ds_read_b128 v[182:185], v165 offset:8192
	v_cmp_lt_i32_e32 vcc, -1, v166
	v_lshlrev_b32_e32 v148, 13, v166
	v_mov_b32_e32 v149, 0
	v_lshl_add_u64 v[148:149], v[148:149], 0, v[86:87]
	v_cndmask_b32_e32 v148, v168, v148, vcc
	v_cndmask_b32_e32 v149, v169, v149, vcc
	s_waitcnt lgkmcnt(0)
	global_store_dwordx4 v[148:149], v[182:185], off nt
	ds_read_b32 v150, v82 offset:1024
	ds_read_b32 v151, v83 offset:1024
	ds_read_b32 v166, v83 offset:1152
	s_waitcnt lgkmcnt(2)
	v_mul_f32_e32 v2, v150, v2
	v_mul_f32_e32 v3, v150, v3
	v_mul_f32_e32 v4, v150, v4
	v_mul_f32_e32 v5, v150, v5
	v_mul_f32_e32 v6, v150, v6
	v_mul_f32_e32 v7, v150, v7
	v_mul_f32_e32 v8, v150, v8
	v_mul_f32_e32 v9, v150, v9
	v_cvt_pk_bf16_f32 v182, v2, v3
	v_cvt_pk_bf16_f32 v183, v4, v5
	v_cvt_pk_bf16_f32 v184, v6, v7
	v_cvt_pk_bf16_f32 v185, v8, v9
	ds_write_b128 v164, v[182:185]
	v_mul_f32_e32 v10, v150, v10
	v_mul_f32_e32 v11, v150, v11
	v_mul_f32_e32 v12, v150, v12
	v_mul_f32_e32 v13, v150, v13
	v_mul_f32_e32 v14, v150, v14
	v_mul_f32_e32 v15, v150, v15
	v_mul_f32_e32 v16, v150, v16
	v_mul_f32_e32 v17, v150, v17
	v_cvt_pk_bf16_f32 v182, v10, v11
	v_cvt_pk_bf16_f32 v183, v12, v13
	v_cvt_pk_bf16_f32 v184, v14, v15
	v_cvt_pk_bf16_f32 v185, v16, v17
	v_xor_b32_e32 v167, 64, v164
	ds_write_b128 v167, v[182:185]
	v_mov_b32_e32 v2, 0
	v_mov_b32_e32 v6, 0
	v_mov_b32_e32 v10, 0
	v_mov_b32_e32 v14, 0
	v_mov_b32_e32 v3, 0
	v_mov_b32_e32 v7, 0
	v_mov_b32_e32 v11, 0
	v_mov_b32_e32 v15, 0
	v_mov_b32_e32 v4, 0
	v_mov_b32_e32 v8, 0
	v_mov_b32_e32 v12, 0
	v_mov_b32_e32 v16, 0
	v_mov_b32_e32 v5, 0
	v_mov_b32_e32 v9, 0
	v_mov_b32_e32 v13, 0
	v_mov_b32_e32 v17, 0
	ds_read_b128 v[182:185], v165 offset:0
	v_cmp_lt_i32_e32 vcc, -1, v151
	v_lshlrev_b32_e32 v148, 13, v151
	v_mov_b32_e32 v149, 0
	v_lshl_add_u64 v[148:149], v[148:149], 0, v[86:87]
	v_cndmask_b32_e32 v148, v168, v148, vcc
	v_cndmask_b32_e32 v149, v169, v149, vcc
	s_waitcnt lgkmcnt(0)
	global_store_dwordx4 v[148:149], v[182:185], off nt
	ds_read_b128 v[182:185], v165 offset:8192
	v_cmp_lt_i32_e32 vcc, -1, v166
	v_lshlrev_b32_e32 v148, 13, v166
	v_mov_b32_e32 v149, 0
	v_lshl_add_u64 v[148:149], v[148:149], 0, v[86:87]
	v_cndmask_b32_e32 v148, v168, v148, vcc
	v_cndmask_b32_e32 v149, v169, v149, vcc
	s_waitcnt lgkmcnt(0)
	global_store_dwordx4 v[148:149], v[182:185], off nt
	v_add_co_u32_e32 v86, vcc, 0x400, v86
	s_nop 1
	v_addc_co_u32_e32 v87, vcc, 0, v87, vcc
	s_waitcnt lgkmcnt(0)
	s_branch .Lmd_done

; #define PG8_LAS __attribute__((address_space(3)))
; __device__ __forceinline__ unsigned cvtpk(float lo, float hi) { f32x2 v = {lo, hi}; bf16x2_t b = __builtin_convertvector(v, bf16x2_t); return __builtin_bit_cast(unsigned, b); }
; __device__ __forceinline__ void moe_down_stream(PG8_LAS unsigned char* lds, int e, int cb0, int slot0, int nv, const bf16_t* HIDp, const float* Wd, bf16_t* Y, const float* slot_w, const int* slot_dst) {
;     ...
;         if (((t + 1) & 7) == 7) {
;             const int cb = cb0 + ((t + 1) >> 3);
; #pragma unroll
;             for (int m = 0; m < DNM; ++m) {
;                 const float w_ = lw[4 * (16 * m + fr) + wr];
; #pragma unroll
;                 for (int p = 0; p < 2; ++p) { const f32x4 v0 = acc[m][2 * p] * w_, v1 = acc[m][2 * p + 1] * w_; u32x4 w; w.x = cvtpk(v0[0], v0[1]); w.y = cvtpk(v0[2], v0[3]); w.z = cvtpk(v1[0], v1[1]); w.w = cvtpk(v1[2], v1[3]);
;                     *(PG8_LAS u32x4*)(stg + fr * 128 + (((4 * p + fq) ^ (fr & 7)) * 16)) = w; }
; #pragma unroll
;                 for (int hh = 0; hh < 2; ++hh) { const int r = (lane >> 3) + 8 * hh, cc = lane & 7; const u32x4 d = *(const PG8_LAS u32x4*)(stg + r * 128 + ((cc ^ (r & 7)) * 16)); const int dst_ = ldst[4 * (16 * m + r) + wr];
;                     if (dst_ >= 0) *(u32x4*)(Y + (size_t)dst_ * D + 128 * cb + 64 * wc + 8 * cc) = d; }
; #pragma unroll
;                 for (int n = 0; n < 4; ++n) acc[m][n] = (f32x4){0.f, 0.f, 0.f, 0.f}; } }
.Lmd_loop_Y:
	v_mfma_f32_16x16x32_bf16 v[78:81], v[142:145], v[218:221], v[78:81]
	v_mfma_f32_16x16x32_bf16 v[74:77], v[146:149], v[218:221], v[74:77]
	v_mfma_f32_16x16x32_bf16 v[70:73], v[156:159], v[218:221], v[70:73]
	v_mfma_f32_16x16x32_bf16 v[66:69], v[160:163], v[218:221], v[66:69]
	v_mfma_f32_16x16x32_bf16 v[62:65], v[142:145], v[222:225], v[62:65]
	v_mfma_f32_16x16x32_bf16 v[58:61], v[146:149], v[222:225], v[58:61]
	v_mfma_f32_16x16x32_bf16 v[54:57], v[156:159], v[222:225], v[54:57]
	v_mfma_f32_16x16x32_bf16 v[50:53], v[160:163], v[222:225], v[50:53]
	v_mfma_f32_16x16x32_bf16 v[46:49], v[142:145], v[226:229], v[46:49]
	v_mfma_f32_16x16x32_bf16 v[42:45], v[146:149], v[226:229], v[42:45]
	v_mfma_f32_16x16x32_bf16 v[38:41], v[156:159], v[226:229], v[38:41]
	v_mfma_f32_16x16x32_bf16 v[34:37], v[160:163], v[226:229], v[34:37]
	v_mfma_f32_16x16x32_bf16 v[18:21], v[142:145], v[230:233], v[18:21]
	v_mfma_f32_16x16x32_bf16 v[22:25], v[146:149], v[230:233], v[22:25]
	v_mfma_f32_16x16x32_bf16 v[26:29], v[156:159], v[230:233], v[26:29]
	v_mfma_f32_16x16x32_bf16 v[30:33], v[160:163], v[230:233], v[30:33]
	v_mfma_f32_16x16x32_bf16 v[2:5], v[142:145], v[234:237], v[2:5]
	v_mfma_f32_16x16x32_bf16 v[6:9], v[146:149], v[234:237], v[6:9]
	v_mfma_f32_16x16x32_bf16 v[10:13], v[156:159], v[234:237], v[10:13]
	v_mfma_f32_16x16x32_bf16 v[14:17], v[160:163], v[234:237], v[14:17]
	s_and_b32 s54, s50, 7
	s_cmp_lg_u32 s54, 0
	s_cbranch_scc1 .Lmd_noepi_Y
	s_add_i32 s54, s48, s74
	v_add_u32_e32 v164, s54, v84
	v_add_u32_e32 v165, s54, v85
	ds_read_b32 v150, v82 offset:0
	ds_read_b32 v151, v83 offset:0
	ds_read_b32 v166, v83 offset:128
	s_waitcnt lgkmcnt(2)
	v_mul_f32_e32 v78, v150, v78
	v_mul_f32_e32 v79, v150, v79
	v_mul_f32_e32 v80, v150, v80
	v_mul_f32_e32 v81, v150, v81
	v_mul_f32_e32 v74, v150, v74
	v_mul_f32_e32 v75, v150, v75
	v_mul_f32_e32 v76, v150, v76
	v_mul_f32_e32 v77, v150, v77
	v_cvt_pk_bf16_f32 v182, v78, v79
	v_cvt_pk_bf16_f32 v183, v80, v81
	v_cvt_pk_bf16_f32 v184, v74, v75
	v_cvt_pk_bf16_f32 v185, v76, v77
	ds_write_b128 v164, v[182:185]
	v_mul_f32_e32 v70, v150, v70
	v_mul_f32_e32 v71, v150, v71
	v_mul_f32_e32 v72, v150, v72
	v_mul_f32_e32 v73, v150, v73
	v_mul_f32_e32 v66, v150, v66
	v_mul_f32_e32 v67, v150, v67
	v_mul_f32_e32 v68, v150, v68
	v_mul_f32_e32 v69, v150, v69
	v_cvt_pk_bf16_f32 v182, v70, v71
	v_cvt_pk_bf16_f32 v183, v72, v73
	v_cvt_pk_bf16_f32 v184, v66, v67
	v_cvt_pk_bf16_f32 v185, v68, v69
	v_xor_b32_e32 v167, 64, v164
	ds_write_b128 v167, v[182:185]
	v_mov_b32_e32 v78, 0
	v_mov_b32_e32 v74, 0
	v_mov_b32_e32 v70, 0
	v_mov_b32_e32 v66, 0
	v_mov_b32_e32 v79, 0
	v_mov_b32_e32 v75, 0
	v_mov_b32_e32 v71, 0
	v_mov_b32_e32 v67, 0
	v_mov_b32_e32 v80, 0
	v_mov_b32_e32 v76, 0
	v_mov_b32_e32 v72, 0
	v_mov_b32_e32 v68, 0
	v_mov_b32_e32 v81, 0
	v_mov_b32_e32 v77, 0
	v_mov_b32_e32 v73, 0
	v_mov_b32_e32 v69, 0
	ds_read_b128 v[182:185], v165 offset:0
	v_cmp_lt_i32_e32 vcc, -1, v151
	v_lshlrev_b32_e32 v148, 13, v151
	v_mov_b32_e32 v149, 0
	v_lshl_add_u64 v[148:149], v[148:149], 0, v[86:87]
	v_cndmask_b32_e32 v148, v168, v148, vcc
	v_cndmask_b32_e32 v149, v169, v149, vcc
	s_waitcnt lgkmcnt(0)
	global_store_dwordx4 v[148:149], v[182:185], off nt
	ds_read_b128 v[182:185], v165 offset:8192
	v_cmp_lt_i32_e32 vcc, -1, v166
	v_lshlrev_b32_e32 v148, 13, v166
	v_mov_b32_e32 v149, 0
	v_lshl_add_u64 v[148:149], v[148:149], 0, v[86:87]
	v_cndmask_b32_e32 v148, v168, v148, vcc
	v_cndmask_b32_e32 v149, v169, v149, vcc
	s_waitcnt lgkmcnt(0)
	global_store_dwordx4 v[148:149], v[182:185], off nt
	ds_read_b32 v150, v82 offset:256
	ds_read_b32 v151, v83 offset:256
	ds_read_b32 v166, v83 offset:384
	s_waitcnt lgkmcnt(2)
	v_mul_f32_e32 v62, v150, v62
	v_mul_f32_e32 v63, v150, v63
	v_mul_f32_e32 v64, v150, v64
	v_mul_f32_e32 v65, v150, v65
	v_mul_f32_e32 v58, v150, v58
	v_mul_f32_e32 v59, v150, v59
	v_mul_f32_e32 v60, v150, v60
	v_mul_f32_e32 v61, v150, v61
	v_cvt_pk_bf16_f32 v182, v62, v63
	v_cvt_pk_bf16_f32 v183, v64, v65
	v_cvt_pk_bf16_f32 v184, v58, v59
	v_cvt_pk_bf16_f32 v185, v60, v61
	ds_write_b128 v164, v[182:185]
	v_mul_f32_e32 v54, v150, v54
	v_mul_f32_e32 v55, v150, v55
	v_mul_f32_e32 v56, v150, v56
	v_mul_f32_e32 v57, v150, v57
	v_mul_f32_e32 v50, v150, v50
	v_mul_f32_e32 v51, v150, v51
	v_mul_f32_e32 v52, v150, v52
	v_mul_f32_e32 v53, v150, v53
	v_cvt_pk_bf16_f32 v182, v54, v55
	v_cvt_pk_bf16_f32 v183, v56, v57
	v_cvt_pk_bf16_f32 v184, v50, v51
	v_cvt_pk_bf16_f32 v185, v52, v53
	v_xor_b32_e32 v167, 64, v164
	ds_write_b128 v167, v[182:185]
	v_mov_b32_e32 v62, 0
	v_mov_b32_e32 v58, 0
	v_mov_b32_e32 v54, 0
	v_mov_b32_e32 v50, 0
	v_mov_b32_e32 v63, 0
	v_mov_b32_e32 v59, 0
	v_mov_b32_e32 v55, 0
	v_mov_b32_e32 v51, 0
	v_mov_b32_e32 v64, 0
	v_mov_b32_e32 v60, 0
	v_mov_b32_e32 v56, 0
	v_mov_b32_e32 v52, 0
	v_mov_b32_e32 v65, 0
	v_mov_b32_e32 v61, 0
	v_mov_b32_e32 v57, 0
	v_mov_b32_e32 v53, 0
	ds_read_b128 v[182:185], v165 offset:0
	v_cmp_lt_i32_e32 vcc, -1, v151
	v_lshlrev_b32_e32 v148, 13, v151
	v_mov_b32_e32 v149, 0
	v_lshl_add_u64 v[148:149], v[148:149], 0, v[86:87]
	v_cndmask_b32_e32 v148, v168, v148, vcc
	v_cndmask_b32_e32 v149, v169, v149, vcc
	s_waitcnt lgkmcnt(0)
	global_store_dwordx4 v[148:149], v[182:185], off nt
	ds_read_b128 v[182:185], v165 offset:8192
	v_cmp_lt_i32_e32 vcc, -1, v166
	v_lshlrev_b32_e32 v148, 13, v166
	v_mov_b32_e32 v149, 0
	v_lshl_add_u64 v[148:149], v[148:149], 0, v[86:87]
	v_cndmask_b32_e32 v148, v168, v148, vcc
	v_cndmask_b32_e32 v149, v169, v149, vcc
	s_waitcnt lgkmcnt(0)
	global_store_dwordx4 v[148:149], v[182:185], off nt
	ds_read_b32 v150, v82 offset:512
	ds_read_b32 v151, v83 offset:512
	ds_read_b32 v166, v83 offset:640
	s_waitcnt lgkmcnt(2)
; #define PG8_LAS __attribute__((address_space(3)))
; __device__ __forceinline__ unsigned cvtpk(float lo, float hi) { f32x2 v = {lo, hi}; bf16x2_t b = __builtin_convertvector(v, bf16x2_t); return __builtin_bit_cast(unsigned, b); }
; __device__ __forceinline__ void moe_down_stream(PG8_LAS unsigned char* lds, int e, int cb0, int slot0, int nv, const bf16_t* HIDp, const float* Wd, bf16_t* Y, const float* slot_w, const int* slot_dst) {
;     ...
;         if (((t + 1) & 7) == 7) {
;             const int cb = cb0 + ((t + 1) >> 3);
; #pragma unroll
;             for (int m = 0; m < DNM; ++m) {
;                 const float w_ = lw[4 * (16 * m + fr) + wr];
; #pragma unroll
;                 for (int p = 0; p < 2; ++p) { const f32x4 v0 = acc[m][2 * p] * w_, v1 = acc[m][2 * p + 1] * w_; u32x4 w; w.x = cvtpk(v0[0], v0[1]); w.y = cvtpk(v0[2], v0[3]); w.z = cvtpk(v1[0], v1[1]); w.w = cvtpk(v1[2], v1[3]);
;                     *(PG8_LAS u32x4*)(stg + fr * 128 + (((4 * p + fq) ^ (fr & 7)) * 16)) = w; }
; #pragma unroll
;                 for (int hh = 0; hh < 2; ++hh) { const int r = (lane >> 3) + 8 * hh, cc = lane & 7; const u32x4 d = *(const PG8_LAS u32x4*)(stg + r * 128 + ((cc ^ (r & 7)) * 16)); const int dst_ = ldst[4 * (16 * m + r) + wr];
;                     if (dst_ >= 0) *(u32x4*)(Y + (size_t)dst_ * D + 128 * cb + 64 * wc + 8 * cc) = d; }
; #pragma unroll
;                 for (int n = 0; n < 4; ++n) acc[m][n] = (f32x4){0.f, 0.f, 0.f, 0.f}; } }
	v_mul_f32_e32 v46, v150, v46
	v_mul_f32_e32 v47, v150, v47
	v_mul_f32_e32 v48, v150, v48
	v_mul_f32_e32 v49, v150, v49
	v_mul_f32_e32 v42, v150, v42
	v_mul_f32_e32 v43, v150, v43
	v_mul_f32_e32 v44, v150, v44
	v_mul_f32_e32 v45, v150, v45
	v_cvt_pk_bf16_f32 v182, v46, v47
	v_cvt_pk_bf16_f32 v183, v48, v49
	v_cvt_pk_bf16_f32 v184, v42, v43
	v_cvt_pk_bf16_f32 v185, v44, v45
	ds_write_b128 v164, v[182:185]
	v_mul_f32_e32 v38, v150, v38
	v_mul_f32_e32 v39, v150, v39
	v_mul_f32_e32 v40, v150, v40
	v_mul_f32_e32 v41, v150, v41
	v_mul_f32_e32 v34, v150, v34
	v_mul_f32_e32 v35, v150, v35
	v_mul_f32_e32 v36, v150, v36
	v_mul_f32_e32 v37, v150, v37
	v_cvt_pk_bf16_f32 v182, v38, v39
	v_cvt_pk_bf16_f32 v183, v40, v41
	v_cvt_pk_bf16_f32 v184, v34, v35
	v_cvt_pk_bf16_f32 v185, v36, v37
	v_xor_b32_e32 v167, 64, v164
	ds_write_b128 v167, v[182:185]
	v_mov_b32_e32 v46, 0
	v_mov_b32_e32 v42, 0
	v_mov_b32_e32 v38, 0
	v_mov_b32_e32 v34, 0
	v_mov_b32_e32 v47, 0
	v_mov_b32_e32 v43, 0
	v_mov_b32_e32 v39, 0
	v_mov_b32_e32 v35, 0
	v_mov_b32_e32 v48, 0
	v_mov_b32_e32 v44, 0
	v_mov_b32_e32 v40, 0
	v_mov_b32_e32 v36, 0
	v_mov_b32_e32 v49, 0
	v_mov_b32_e32 v45, 0
	v_mov_b32_e32 v41, 0
	v_mov_b32_e32 v37, 0
	ds_read_b128 v[182:185], v165 offset:0
	v_cmp_lt_i32_e32 vcc, -1, v151
	v_lshlrev_b32_e32 v148, 13, v151
	v_mov_b32_e32 v149, 0
	v_lshl_add_u64 v[148:149], v[148:149], 0, v[86:87]
	v_cndmask_b32_e32 v148, v168, v148, vcc
	v_cndmask_b32_e32 v149, v169, v149, vcc
	s_waitcnt lgkmcnt(0)
	global_store_dwordx4 v[148:149], v[182:185], off nt
	ds_read_b128 v[182:185], v165 offset:8192
	v_cmp_lt_i32_e32 vcc, -1, v166
	v_lshlrev_b32_e32 v148, 13, v166
	v_mov_b32_e32 v149, 0
	v_lshl_add_u64 v[148:149], v[148:149], 0, v[86:87]
	v_cndmask_b32_e32 v148, v168, v148, vcc
	v_cndmask_b32_e32 v149, v169, v149, vcc
	s_waitcnt lgkmcnt(0)
	global_store_dwordx4 v[148:149], v[182:185], off nt
	ds_read_b32 v150, v82 offset:768
	ds_read_b32 v151, v83 offset:768
	ds_read_b32 v166, v83 offset:896
	s_waitcnt lgkmcnt(2)
	v_mul_f32_e32 v18, v150, v18
	v_mul_f32_e32 v19, v150, v19
	v_mul_f32_e32 v20, v150, v20
	v_mul_f32_e32 v21, v150, v21
	v_mul_f32_e32 v22, v150, v22
	v_mul_f32_e32 v23, v150, v23
	v_mul_f32_e32 v24, v150, v24
	v_mul_f32_e32 v25, v150, v25
	v_cvt_pk_bf16_f32 v182, v18, v19
	v_cvt_pk_bf16_f32 v183, v20, v21
	v_cvt_pk_bf16_f32 v184, v22, v23
	v_cvt_pk_bf16_f32 v185, v24, v25
	ds_write_b128 v164, v[182:185]
	v_mul_f32_e32 v26, v150, v26
	v_mul_f32_e32 v27, v150, v27
	v_mul_f32_e32 v28, v150, v28
	v_mul_f32_e32 v29, v150, v29
	v_mul_f32_e32 v30, v150, v30
	v_mul_f32_e32 v31, v150, v31
	v_mul_f32_e32 v32, v150, v32
	v_mul_f32_e32 v33, v150, v33
	v_cvt_pk_bf16_f32 v182, v26, v27
	v_cvt_pk_bf16_f32 v183, v28, v29
	v_cvt_pk_bf16_f32 v184, v30, v31
	v_cvt_pk_bf16_f32 v185, v32, v33
	v_xor_b32_e32 v167, 64, v164
	ds_write_b128 v167, v[182:185]
	v_mov_b32_e32 v18, 0
	v_mov_b32_e32 v22, 0
	v_mov_b32_e32 v26, 0
	v_mov_b32_e32 v30, 0
	v_mov_b32_e32 v19, 0
	v_mov_b32_e32 v23, 0
	v_mov_b32_e32 v27, 0
	v_mov_b32_e32 v31, 0
	v_mov_b32_e32 v20, 0
	v_mov_b32_e32 v24, 0
	v_mov_b32_e32 v28, 0
	v_mov_b32_e32 v32, 0
	v_mov_b32_e32 v21, 0
	v_mov_b32_e32 v25, 0
	v_mov_b32_e32 v29, 0
	v_mov_b32_e32 v33, 0
	ds_read_b128 v[182:185], v165 offset:0
	v_cmp_lt_i32_e32 vcc, -1, v151
	v_lshlrev_b32_e32 v148, 13, v151
	v_mov_b32_e32 v149, 0
	v_lshl_add_u64 v[148:149], v[148:149], 0, v[86:87]
	v_cndmask_b32_e32 v148, v168, v148, vcc
	v_cndmask_b32_e32 v149, v169, v149, vcc
	s_waitcnt lgkmcnt(0)
	global_store_dwordx4 v[148:149], v[182:185], off nt
	ds_read_b128 v[182:185], v165 offset:8192
	v_cmp_lt_i32_e32 vcc, -1, v166
	v_lshlrev_b32_e32 v148, 13, v166
	v_mov_b32_e32 v149, 0
	v_lshl_add_u64 v[148:149], v[148:149], 0, v[86:87]
	v_cndmask_b32_e32 v148, v168, v148, vcc
	v_cndmask_b32_e32 v149, v169, v149, vcc
	s_waitcnt lgkmcnt(0)
	global_store_dwordx4 v[148:149], v[182:185], off nt
	ds_read_b32 v150, v82 offset:1024
	ds_read_b32 v151, v83 offset:1024
	ds_read_b32 v166, v83 offset:1152
	s_waitcnt lgkmcnt(2)
	v_mul_f32_e32 v2, v150, v2
	v_mul_f32_e32 v3, v150, v3
	v_mul_f32_e32 v4, v150, v4
	v_mul_f32_e32 v5, v150, v5
	v_mul_f32_e32 v6, v150, v6
	v_mul_f32_e32 v7, v150, v7
	v_mul_f32_e32 v8, v150, v8
	v_mul_f32_e32 v9, v150, v9
	v_cvt_pk_bf16_f32 v182, v2, v3
	v_cvt_pk_bf16_f32 v183, v4, v5
	v_cvt_pk_bf16_f32 v184, v6, v7
	v_cvt_pk_bf16_f32 v185, v8, v9
	ds_write_b128 v164, v[182:185]
	v_mul_f32_e32 v10, v150, v10
	v_mul_f32_e32 v11, v150, v11
	v_mul_f32_e32 v12, v150, v12
	v_mul_f32_e32 v13, v150, v13
	v_mul_f32_e32 v14, v150, v14
	v_mul_f32_e32 v15, v150, v15
	v_mul_f32_e32 v16, v150, v16
	v_mul_f32_e32 v17, v150, v17
	v_cvt_pk_bf16_f32 v182, v10, v11
	v_cvt_pk_bf16_f32 v183, v12, v13
	v_cvt_pk_bf16_f32 v184, v14, v15
	v_cvt_pk_bf16_f32 v185, v16, v17
	v_xor_b32_e32 v167, 64, v164
	ds_write_b128 v167, v[182:185]
	v_mov_b32_e32 v2, 0
	v_mov_b32_e32 v6, 0
	v_mov_b32_e32 v10, 0
	v_mov_b32_e32 v14, 0
	v_mov_b32_e32 v3, 0
	v_mov_b32_e32 v7, 0
	v_mov_b32_e32 v11, 0
	v_mov_b32_e32 v15, 0
	v_mov_b32_e32 v4, 0
	v_mov_b32_e32 v8, 0
	v_mov_b32_e32 v12, 0
	v_mov_b32_e32 v16, 0
	v_mov_b32_e32 v5, 0
	v_mov_b32_e32 v9, 0
	v_mov_b32_e32 v13, 0
	v_mov_b32_e32 v17, 0
	ds_read_b128 v[182:185], v165 offset:0
	v_cmp_lt_i32_e32 vcc, -1, v151
	v_lshlrev_b32_e32 v148, 13, v151
	v_mov_b32_e32 v149, 0
	v_lshl_add_u64 v[148:149], v[148:149], 0, v[86:87]
	v_cndmask_b32_e32 v148, v168, v148, vcc
	v_cndmask_b32_e32 v149, v169, v149, vcc
	s_waitcnt lgkmcnt(0)
	global_store_dwordx4 v[148:149], v[182:185], off nt
	ds_read_b128 v[182:185], v165 offset:8192
	v_cmp_lt_i32_e32 vcc, -1, v166
	v_lshlrev_b32_e32 v148, 13, v166
	v_mov_b32_e32 v149, 0
	v_lshl_add_u64 v[148:149], v[148:149], 0, v[86:87]
	v_cndmask_b32_e32 v148, v168, v148, vcc
	v_cndmask_b32_e32 v149, v169, v149, vcc
	s_waitcnt lgkmcnt(0)
	global_store_dwordx4 v[148:149], v[182:185], off nt
	v_add_co_u32_e32 v86, vcc, 0x400, v86
	s_nop 1
	v_addc_co_u32_e32 v87, vcc, 0, v87, vcc
	s_waitcnt lgkmcnt(0)
; #define MD_GLDS_A(buf, tau) do { _Pragma("unroll") for (int i = 0; i < 5; ++i) if (amask & (1u << i)) \
;         __builtin_amdgcn_global_load_lds((const unsigned*)((const char*)HIDp + aoff[i] + (size_t)((tau) & 7) * 128), (PG8_LAS unsigned*)(MD_SA(buf) + wid * 1024 + i * 8192), 16, 0, 0); } while (0)
; #define MD_B_ISSUE(sb, tau) do { const char* kb_ = Bb + (size_t)((tau) >> 3) * 512 + (size_t)((tau) & 7) * (64 * (size_t)RB); _Pragma("unroll") for (int j = 0; j < 8; ++j) { const char* p_ = kb_ + (size_t)j * RB; \
;         asm volatile("global_load_dwordx2 %0, %1, off" : "=&v"(sb[j]) : "v"(p_) : "memory"); } } while (0)
; #define MD_B_WAIT(sb, N) asm volatile("s_waitcnt vmcnt(%8)" : "+v"(sb[0]), "+v"(sb[1]), "+v"(sb[2]), "+v"(sb[3]), "+v"(sb[4]), "+v"(sb[5]), "+v"(sb[6]), "+v"(sb[7]) : "n"(N) : "memory")
; #define MD_END(last) do { if (last) asm volatile("s_waitcnt vmcnt(0)" ::: "memory"); else asm volatile("s_waitcnt vmcnt(8)" ::: "memory"); \
;         asm volatile("s_waitcnt lgkmcnt(0)" ::: "memory"); __builtin_amdgcn_s_barrier(); asm volatile("" ::: "memory"); } while (0)
; __device__ __forceinline__ void moe_down_stream(PG8_LAS unsigned char* lds, int e, int cb0, int slot0, int nv, const bf16_t* HIDp, const float* Wd, bf16_t* Y, const float* slot_w, const int* slot_dst) {
;     ...
;         if (t + 2 < NT) MD_B_WAIT(s1, 8); else MD_B_WAIT(s1, 0);
;         MD_B_WRITE(s1, 1); __builtin_amdgcn_sched_barrier(0); MD_GLDS_A(1, t + 1); __builtin_amdgcn_sched_barrier(0);
;         if (t + 3 < NT) MD_B_ISSUE(s1, t + 3);
;         MD_COMPUTE(0);
;         MD_END(t + 3 >= NT);
;         if (t + 2 < NT) { MD_B_WAIT(s0, 8); MD_B_WRITE(s0, 0); __builtin_amdgcn_sched_barrier(0); MD_GLDS_A(0, t + 2); __builtin_amdgcn_sched_barrier(0); }
;         if (t + 4 < NT) MD_B_ISSUE(s0, t + 4);
;         MD_COMPUTE(1);
;         MD_END(t + 4 >= NT);
.Lmd_noepi_Y:
	s_add_i32 s49, s48, s74
	s_add_i32 s52, s52, 1
	s_and_b32 s54, s52, 7
	s_cmp_eq_u32 s54, 0
	s_cselect_b32 s54, s53, s32
	s_cselect_b32 s55, -1, 0
	s_add_u32 s30, s30, s54
	s_addc_u32 s31, s31, s55
	s_mov_b32 m0, s49
	s_nop 0
	global_load_lds_dwordx4 v88, s[30:31]
	s_add_i32 m0, s49, 0x2000
	s_nop 0
	global_load_lds_dwordx4 v90, s[30:31]
	s_add_i32 m0, s49, 0x4000
	s_nop 0
	global_load_lds_dwordx4 v92, s[30:31]
	s_add_i32 m0, s49, 0x6000
	s_nop 0
	global_load_lds_dwordx4 v94, s[30:31]
	s_add_i32 m0, s49, 0x8000
	s_nop 0
	global_load_lds_dwordx4 v96, s[30:31]
	v_cvt_pk_bf16_f32 v172, v114, v116
	v_cvt_pk_bf16_f32 v173, v118, v120
	v_cvt_pk_bf16_f32 v174, v122, v124
	v_cvt_pk_bf16_f32 v175, v126, v128
	v_cvt_pk_bf16_f32 v176, v115, v117
	v_cvt_pk_bf16_f32 v177, v119, v121
	v_cvt_pk_bf16_f32 v178, v123, v125
	v_cvt_pk_bf16_f32 v179, v127, v129
	ds_write_b128 v95, v[172:175] offset:19456
	ds_write_b128 v95, v[176:179] offset:19584
	v_add_u32_e32 v91, s46, v135
	v_add_u32_e32 v93, s46, v137
	ds_read_b128 v[238:241], v139 offset:0
	ds_read_b128 v[242:245], v139 offset:2048
	ds_read_b128 v[246:249], v139 offset:4096
	ds_read_b128 v[250:253], v139 offset:6144
	ds_read_b128 v[218:221], v91 offset:0
	ds_read_b128 v[222:225], v91 offset:2048
	ds_read_b128 v[226:229], v91 offset:4096
	ds_read_b128 v[230:233], v91 offset:6144
	ds_read_b128 v[234:237], v91 offset:8192
	s_waitcnt lgkmcnt(0)
	v_mfma_f32_16x16x32_bf16 v[78:81], v[238:241], v[218:221], v[78:81]
	v_mfma_f32_16x16x32_bf16 v[74:77], v[242:245], v[218:221], v[74:77]
	v_mfma_f32_16x16x32_bf16 v[70:73], v[246:249], v[218:221], v[70:73]
	v_mfma_f32_16x16x32_bf16 v[66:69], v[250:253], v[218:221], v[66:69]
	ds_read_b128 v[218:221], v93 offset:0
	ds_read_b128 v[142:145], v141 offset:0
	s_add_i32 s51, s51, 1
	s_and_b32 s54, s51, 7
	s_cmp_eq_u32 s54, 0
	s_cselect_b32 s44, s34, s35
	s_cselect_b32 s45, -1, 0
	v_lshl_add_u64 v[132:133], v[132:133], 0, s[44:45]
	global_load_dwordx2 v[114:115], v[132:133], off
	v_lshl_add_u64 v[180:181], v[132:133], 0, s[24:25]
	global_load_dwordx2 v[116:117], v[180:181], off
	v_mfma_f32_16x16x32_bf16 v[62:65], v[238:241], v[222:225], v[62:65]
	v_mfma_f32_16x16x32_bf16 v[58:61], v[242:245], v[222:225], v[58:61]
	v_mfma_f32_16x16x32_bf16 v[54:57], v[246:249], v[222:225], v[54:57]
	v_mfma_f32_16x16x32_bf16 v[50:53], v[250:253], v[222:225], v[50:53]
	ds_read_b128 v[222:225], v93 offset:2048
	ds_read_b128 v[146:149], v141 offset:2048
	v_lshl_add_u64 v[180:181], v[132:133], 0, s[26:27]
	global_load_dwordx2 v[118:119], v[180:181], off
	v_lshl_add_u64 v[180:181], v[132:133], 0, s[28:29]
	global_load_dwordx2 v[120:121], v[180:181], off
	v_mfma_f32_16x16x32_bf16 v[46:49], v[238:241], v[226:229], v[46:49]
	v_mfma_f32_16x16x32_bf16 v[42:45], v[242:245], v[226:229], v[42:45]
	v_mfma_f32_16x16x32_bf16 v[38:41], v[246:249], v[226:229], v[38:41]
	v_mfma_f32_16x16x32_bf16 v[34:37], v[250:253], v[226:229], v[34:37]
	ds_read_b128 v[226:229], v93 offset:4096
	ds_read_b128 v[156:159], v141 offset:4096
	v_lshl_add_u64 v[180:181], v[132:133], 0, s[36:37]
	global_load_dwordx2 v[122:123], v[180:181], off
	v_lshl_add_u64 v[180:181], v[132:133], 0, s[38:39]
	global_load_dwordx2 v[124:125], v[180:181], off
	v_mfma_f32_16x16x32_bf16 v[18:21], v[238:241], v[230:233], v[18:21]
	v_mfma_f32_16x16x32_bf16 v[22:25], v[242:245], v[230:233], v[22:25]
	v_mfma_f32_16x16x32_bf16 v[26:29], v[246:249], v[230:233], v[26:29]
	v_mfma_f32_16x16x32_bf16 v[30:33], v[250:253], v[230:233], v[30:33]
	ds_read_b128 v[230:233], v93 offset:6144
	ds_read_b128 v[160:163], v141 offset:6144
	v_lshl_add_u64 v[180:181], v[132:133], 0, s[40:41]
	global_load_dwordx2 v[126:127], v[180:181], off
	v_lshl_add_u64 v[180:181], v[132:133], 0, s[42:43]
	global_load_dwordx2 v[128:129], v[180:181], off
	v_mfma_f32_16x16x32_bf16 v[2:5], v[238:241], v[234:237], v[2:5]
	v_mfma_f32_16x16x32_bf16 v[6:9], v[242:245], v[234:237], v[6:9]
	v_mfma_f32_16x16x32_bf16 v[10:13], v[246:249], v[234:237], v[10:13]
	v_mfma_f32_16x16x32_bf16 v[14:17], v[250:253], v[234:237], v[14:17]
	ds_read_b128 v[234:237], v93 offset:8192
	s_waitcnt vmcnt(21)
	s_waitcnt lgkmcnt(0)
	s_barrier
	s_mov_b32 s49, s46
	s_mov_b32 s46, s47
	s_mov_b32 s47, s48
	s_mov_b32 s48, s49
	s_add_i32 s50, s50, 1
	s_add_i32 s49, s48, s74
	s_add_i32 s52, s52, 1
	s_and_b32 s54, s52, 7
	s_cmp_eq_u32 s54, 0
	s_cselect_b32 s54, s53, s32
	s_cselect_b32 s55, -1, 0
	s_add_u32 s30, s30, s54
	s_addc_u32 s31, s31, s55
	v_mfma_f32_16x16x32_bf16 v[78:81], v[142:145], v[218:221], v[78:81]
	v_mfma_f32_16x16x32_bf16 v[74:77], v[146:149], v[218:221], v[74:77]
	v_mfma_f32_16x16x32_bf16 v[70:73], v[156:159], v[218:221], v[70:73]
	v_mfma_f32_16x16x32_bf16 v[66:69], v[160:163], v[218:221], v[66:69]
	s_mov_b32 m0, s49
	s_nop 0
	global_load_lds_dwordx4 v88, s[30:31]
	v_mfma_f32_16x16x32_bf16 v[62:65], v[142:145], v[222:225], v[62:65]
	v_mfma_f32_16x16x32_bf16 v[58:61], v[146:149], v[222:225], v[58:61]
	v_mfma_f32_16x16x32_bf16 v[54:57], v[156:159], v[222:225], v[54:57]
	v_mfma_f32_16x16x32_bf16 v[50:53], v[160:163], v[222:225], v[50:53]
	s_add_i32 m0, s49, 0x2000
	s_nop 0
	global_load_lds_dwordx4 v90, s[30:31]
	v_mfma_f32_16x16x32_bf16 v[46:49], v[142:145], v[226:229], v[46:49]
	v_mfma_f32_16x16x32_bf16 v[42:45], v[146:149], v[226:229], v[42:45]
	v_mfma_f32_16x16x32_bf16 v[38:41], v[156:159], v[226:229], v[38:41]
	v_mfma_f32_16x16x32_bf16 v[34:37], v[160:163], v[226:229], v[34:37]
	s_add_i32 m0, s49, 0x4000
	s_nop 0
	global_load_lds_dwordx4 v92, s[30:31]
	v_mfma_f32_16x16x32_bf16 v[18:21], v[142:145], v[230:233], v[18:21]
	v_mfma_f32_16x16x32_bf16 v[22:25], v[146:149], v[230:233], v[22:25]
	v_mfma_f32_16x16x32_bf16 v[26:29], v[156:159], v[230:233], v[26:29]
	v_mfma_f32_16x16x32_bf16 v[30:33], v[160:163], v[230:233], v[30:33]
	s_add_i32 m0, s49, 0x6000
	s_nop 0
	global_load_lds_dwordx4 v94, s[30:31]
	v_mfma_f32_16x16x32_bf16 v[2:5], v[142:145], v[234:237], v[2:5]
	v_mfma_f32_16x16x32_bf16 v[6:9], v[146:149], v[234:237], v[6:9]
	v_mfma_f32_16x16x32_bf16 v[10:13], v[156:159], v[234:237], v[10:13]
	v_mfma_f32_16x16x32_bf16 v[14:17], v[160:163], v[234:237], v[14:17]
	s_add_i32 m0, s49, 0x8000
	s_nop 0
	global_load_lds_dwordx4 v96, s[30:31]
	v_cvt_pk_bf16_f32 v172, v186, v188
	v_cvt_pk_bf16_f32 v173, v190, v192
	v_cvt_pk_bf16_f32 v174, v194, v196
	v_cvt_pk_bf16_f32 v175, v198, v200
	v_cvt_pk_bf16_f32 v176, v187, v189
	v_cvt_pk_bf16_f32 v177, v191, v193
	v_cvt_pk_bf16_f32 v178, v195, v197
	v_cvt_pk_bf16_f32 v179, v199, v201
	ds_write_b128 v95, v[172:175] offset:0
	ds_write_b128 v95, v[176:179] offset:128
	v_add_u32_e32 v91, s46, v135
	v_add_u32_e32 v93, s46, v137
	ds_read_b128 v[238:241], v139 offset:19456
	ds_read_b128 v[242:245], v139 offset:21504
	ds_read_b128 v[246:249], v139 offset:23552
	ds_read_b128 v[250:253], v139 offset:25600
	ds_read_b128 v[218:221], v91 offset:0
	ds_read_b128 v[222:225], v91 offset:2048
	ds_read_b128 v[226:229], v91 offset:4096
	ds_read_b128 v[230:233], v91 offset:6144
	ds_read_b128 v[234:237], v91 offset:8192
	s_waitcnt lgkmcnt(0)
; #define MD_GLDS_A(buf, tau) do { _Pragma("unroll") for (int i = 0; i < 5; ++i) if (amask & (1u << i)) \
;         __builtin_amdgcn_global_load_lds((const unsigned*)((const char*)HIDp + aoff[i] + (size_t)((tau) & 7) * 128), (PG8_LAS unsigned*)(MD_SA(buf) + wid * 1024 + i * 8192), 16, 0, 0); } while (0)
; #define MD_B_ISSUE(sb, tau) do { const char* kb_ = Bb + (size_t)((tau) >> 3) * 512 + (size_t)((tau) & 7) * (64 * (size_t)RB); _Pragma("unroll") for (int j = 0; j < 8; ++j) { const char* p_ = kb_ + (size_t)j * RB; \
;         asm volatile("global_load_dwordx2 %0, %1, off" : "=&v"(sb[j]) : "v"(p_) : "memory"); } } while (0)
; #define MD_B_WAIT(sb, N) asm volatile("s_waitcnt vmcnt(%8)" : "+v"(sb[0]), "+v"(sb[1]), "+v"(sb[2]), "+v"(sb[3]), "+v"(sb[4]), "+v"(sb[5]), "+v"(sb[6]), "+v"(sb[7]) : "n"(N) : "memory")
; #define MD_END(last) do { if (last) asm volatile("s_waitcnt vmcnt(0)" ::: "memory"); else asm volatile("s_waitcnt vmcnt(8)" ::: "memory"); \
;         asm volatile("s_waitcnt lgkmcnt(0)" ::: "memory"); __builtin_amdgcn_s_barrier(); asm volatile("" ::: "memory"); } while (0)
; __device__ __forceinline__ void moe_down_stream(PG8_LAS unsigned char* lds, int e, int cb0, int slot0, int nv, const bf16_t* HIDp, const float* Wd, bf16_t* Y, const float* slot_w, const int* slot_dst) {
;     ...
;         if (t + 2 < NT) MD_B_WAIT(s1, 8); else MD_B_WAIT(s1, 0);
;         MD_B_WRITE(s1, 1); __builtin_amdgcn_sched_barrier(0); MD_GLDS_A(1, t + 1); __builtin_amdgcn_sched_barrier(0);
;         if (t + 3 < NT) MD_B_ISSUE(s1, t + 3);
;         MD_COMPUTE(0);
;         MD_END(t + 3 >= NT);
;         if (t + 2 < NT) { MD_B_WAIT(s0, 8); MD_B_WRITE(s0, 0); __builtin_amdgcn_sched_barrier(0); MD_GLDS_A(0, t + 2); __builtin_amdgcn_sched_barrier(0); }
;         if (t + 4 < NT) MD_B_ISSUE(s0, t + 4);
;         MD_COMPUTE(1);
;         MD_END(t + 4 >= NT);
	v_mfma_f32_16x16x32_bf16 v[78:81], v[238:241], v[218:221], v[78:81]
	v_mfma_f32_16x16x32_bf16 v[74:77], v[242:245], v[218:221], v[74:77]
	v_mfma_f32_16x16x32_bf16 v[70:73], v[246:249], v[218:221], v[70:73]
	v_mfma_f32_16x16x32_bf16 v[66:69], v[250:253], v[218:221], v[66:69]
	ds_read_b128 v[218:221], v93 offset:0
	ds_read_b128 v[142:145], v141 offset:19456
	s_add_i32 s51, s51, 1
	s_and_b32 s54, s51, 7
	s_cmp_eq_u32 s54, 0
	s_cselect_b32 s44, s34, s35
	s_cselect_b32 s45, -1, 0
	v_lshl_add_u64 v[132:133], v[132:133], 0, s[44:45]
	global_load_dwordx2 v[186:187], v[132:133], off
	v_lshl_add_u64 v[180:181], v[132:133], 0, s[24:25]
	global_load_dwordx2 v[188:189], v[180:181], off
	v_mfma_f32_16x16x32_bf16 v[62:65], v[238:241], v[222:225], v[62:65]
	v_mfma_f32_16x16x32_bf16 v[58:61], v[242:245], v[222:225], v[58:61]
	v_mfma_f32_16x16x32_bf16 v[54:57], v[246:249], v[222:225], v[54:57]
	v_mfma_f32_16x16x32_bf16 v[50:53], v[250:253], v[222:225], v[50:53]
	ds_read_b128 v[222:225], v93 offset:2048
	ds_read_b128 v[146:149], v141 offset:21504
	v_lshl_add_u64 v[180:181], v[132:133], 0, s[26:27]
	global_load_dwordx2 v[190:191], v[180:181], off
	v_lshl_add_u64 v[180:181], v[132:133], 0, s[28:29]
	global_load_dwordx2 v[192:193], v[180:181], off
	v_mfma_f32_16x16x32_bf16 v[46:49], v[238:241], v[226:229], v[46:49]
	v_mfma_f32_16x16x32_bf16 v[42:45], v[242:245], v[226:229], v[42:45]
	v_mfma_f32_16x16x32_bf16 v[38:41], v[246:249], v[226:229], v[38:41]
	v_mfma_f32_16x16x32_bf16 v[34:37], v[250:253], v[226:229], v[34:37]
	ds_read_b128 v[226:229], v93 offset:4096
	ds_read_b128 v[156:159], v141 offset:23552
	v_lshl_add_u64 v[180:181], v[132:133], 0, s[36:37]
	global_load_dwordx2 v[194:195], v[180:181], off
	v_lshl_add_u64 v[180:181], v[132:133], 0, s[38:39]
	global_load_dwordx2 v[196:197], v[180:181], off
	v_mfma_f32_16x16x32_bf16 v[18:21], v[238:241], v[230:233], v[18:21]
	v_mfma_f32_16x16x32_bf16 v[22:25], v[242:245], v[230:233], v[22:25]
	v_mfma_f32_16x16x32_bf16 v[26:29], v[246:249], v[230:233], v[26:29]
	v_mfma_f32_16x16x32_bf16 v[30:33], v[250:253], v[230:233], v[30:33]
	ds_read_b128 v[230:233], v93 offset:6144
	ds_read_b128 v[160:163], v141 offset:25600
	v_lshl_add_u64 v[180:181], v[132:133], 0, s[40:41]
	global_load_dwordx2 v[198:199], v[180:181], off
	v_lshl_add_u64 v[180:181], v[132:133], 0, s[42:43]
	global_load_dwordx2 v[200:201], v[180:181], off
	v_mfma_f32_16x16x32_bf16 v[2:5], v[238:241], v[234:237], v[2:5]
	v_mfma_f32_16x16x32_bf16 v[6:9], v[242:245], v[234:237], v[6:9]
	v_mfma_f32_16x16x32_bf16 v[10:13], v[246:249], v[234:237], v[10:13]
	v_mfma_f32_16x16x32_bf16 v[14:17], v[250:253], v[234:237], v[14:17]
	ds_read_b128 v[234:237], v93 offset:8192
	s_waitcnt vmcnt(21)
	s_waitcnt lgkmcnt(0)
	s_barrier
	s_mov_b32 s49, s46
	s_mov_b32 s46, s47
	s_mov_b32 s47, s48
	s_mov_b32 s48, s49
	s_add_i32 s50, s50, 1
	s_add_i32 s49, s48, s74
	s_add_i32 s52, s52, 1
	s_and_b32 s54, s52, 7
	s_cmp_eq_u32 s54, 0
	s_cselect_b32 s54, s53, s32
	s_cselect_b32 s55, -1, 0
	s_add_u32 s30, s30, s54
	s_addc_u32 s31, s31, s55
	v_mfma_f32_16x16x32_bf16 v[78:81], v[142:145], v[218:221], v[78:81]
	v_mfma_f32_16x16x32_bf16 v[74:77], v[146:149], v[218:221], v[74:77]
	v_mfma_f32_16x16x32_bf16 v[70:73], v[156:159], v[218:221], v[70:73]
	v_mfma_f32_16x16x32_bf16 v[66:69], v[160:163], v[218:221], v[66:69]
	s_mov_b32 m0, s49
	s_nop 0
	global_load_lds_dwordx4 v88, s[30:31]
	v_mfma_f32_16x16x32_bf16 v[62:65], v[142:145], v[222:225], v[62:65]
	v_mfma_f32_16x16x32_bf16 v[58:61], v[146:149], v[222:225], v[58:61]
	v_mfma_f32_16x16x32_bf16 v[54:57], v[156:159], v[222:225], v[54:57]
	v_mfma_f32_16x16x32_bf16 v[50:53], v[160:163], v[222:225], v[50:53]
	s_add_i32 m0, s49, 0x2000
	s_nop 0
	global_load_lds_dwordx4 v90, s[30:31]
	v_mfma_f32_16x16x32_bf16 v[46:49], v[142:145], v[226:229], v[46:49]
	v_mfma_f32_16x16x32_bf16 v[42:45], v[146:149], v[226:229], v[42:45]
	v_mfma_f32_16x16x32_bf16 v[38:41], v[156:159], v[226:229], v[38:41]
	v_mfma_f32_16x16x32_bf16 v[34:37], v[160:163], v[226:229], v[34:37]
	s_add_i32 m0, s49, 0x4000
	s_nop 0
	global_load_lds_dwordx4 v92, s[30:31]
	v_mfma_f32_16x16x32_bf16 v[18:21], v[142:145], v[230:233], v[18:21]
	v_mfma_f32_16x16x32_bf16 v[22:25], v[146:149], v[230:233], v[22:25]
	v_mfma_f32_16x16x32_bf16 v[26:29], v[156:159], v[230:233], v[26:29]
	v_mfma_f32_16x16x32_bf16 v[30:33], v[160:163], v[230:233], v[30:33]
	s_add_i32 m0, s49, 0x6000
	s_nop 0
	global_load_lds_dwordx4 v94, s[30:31]
	v_mfma_f32_16x16x32_bf16 v[2:5], v[142:145], v[234:237], v[2:5]
	v_mfma_f32_16x16x32_bf16 v[6:9], v[146:149], v[234:237], v[6:9]
	v_mfma_f32_16x16x32_bf16 v[10:13], v[156:159], v[234:237], v[10:13]
	v_mfma_f32_16x16x32_bf16 v[14:17], v[160:163], v[234:237], v[14:17]
	s_add_i32 m0, s49, 0x8000
	s_nop 0
	global_load_lds_dwordx4 v96, s[30:31]
	v_cvt_pk_bf16_f32 v172, v202, v204
	v_cvt_pk_bf16_f32 v173, v206, v208
	v_cvt_pk_bf16_f32 v174, v210, v212
	v_cvt_pk_bf16_f32 v175, v214, v216
	v_cvt_pk_bf16_f32 v176, v203, v205
	v_cvt_pk_bf16_f32 v177, v207, v209
	v_cvt_pk_bf16_f32 v178, v211, v213
	v_cvt_pk_bf16_f32 v179, v215, v217
	ds_write_b128 v95, v[172:175] offset:19456
	ds_write_b128 v95, v[176:179] offset:19584
	v_add_u32_e32 v91, s46, v135
	v_add_u32_e32 v93, s46, v137
	ds_read_b128 v[238:241], v139 offset:0
	ds_read_b128 v[242:245], v139 offset:2048
	ds_read_b128 v[246:249], v139 offset:4096
	ds_read_b128 v[250:253], v139 offset:6144
	ds_read_b128 v[218:221], v91 offset:0
	ds_read_b128 v[222:225], v91 offset:2048
	ds_read_b128 v[226:229], v91 offset:4096
	ds_read_b128 v[230:233], v91 offset:6144
	ds_read_b128 v[234:237], v91 offset:8192
	s_waitcnt lgkmcnt(0)
; #define MD_GLDS_A(buf, tau) do { _Pragma("unroll") for (int i = 0; i < 5; ++i) if (amask & (1u << i)) \
;         __builtin_amdgcn_global_load_lds((const unsigned*)((const char*)HIDp + aoff[i] + (size_t)((tau) & 7) * 128), (PG8_LAS unsigned*)(MD_SA(buf) + wid * 1024 + i * 8192), 16, 0, 0); } while (0)
; #define MD_B_ISSUE(sb, tau) do { const char* kb_ = Bb + (size_t)((tau) >> 3) * 512 + (size_t)((tau) & 7) * (64 * (size_t)RB); _Pragma("unroll") for (int j = 0; j < 8; ++j) { const char* p_ = kb_ + (size_t)j * RB; \
;         asm volatile("global_load_dwordx2 %0, %1, off" : "=&v"(sb[j]) : "v"(p_) : "memory"); } } while (0)
; #define MD_B_WAIT(sb, N) asm volatile("s_waitcnt vmcnt(%8)" : "+v"(sb[0]), "+v"(sb[1]), "+v"(sb[2]), "+v"(sb[3]), "+v"(sb[4]), "+v"(sb[5]), "+v"(sb[6]), "+v"(sb[7]) : "n"(N) : "memory")
; #define MD_END(last) do { if (last) asm volatile("s_waitcnt vmcnt(0)" ::: "memory"); else asm volatile("s_waitcnt vmcnt(8)" ::: "memory"); \
;         asm volatile("s_waitcnt lgkmcnt(0)" ::: "memory"); __builtin_amdgcn_s_barrier(); asm volatile("" ::: "memory"); } while (0)
; __device__ __forceinline__ void moe_down_stream(PG8_LAS unsigned char* lds, int e, int cb0, int slot0, int nv, const bf16_t* HIDp, const float* Wd, bf16_t* Y, const float* slot_w, const int* slot_dst) {
;     ...
;         if (t + 2 < NT) MD_B_WAIT(s1, 8); else MD_B_WAIT(s1, 0);
;         MD_B_WRITE(s1, 1); __builtin_amdgcn_sched_barrier(0); MD_GLDS_A(1, t + 1); __builtin_amdgcn_sched_barrier(0);
;         if (t + 3 < NT) MD_B_ISSUE(s1, t + 3);
;         MD_COMPUTE(0);
;         MD_END(t + 3 >= NT);
;         if (t + 2 < NT) { MD_B_WAIT(s0, 8); MD_B_WRITE(s0, 0); __builtin_amdgcn_sched_barrier(0); MD_GLDS_A(0, t + 2); __builtin_amdgcn_sched_barrier(0); }
;         if (t + 4 < NT) MD_B_ISSUE(s0, t + 4);
;         MD_COMPUTE(1);
;         MD_END(t + 4 >= NT);
	v_mfma_f32_16x16x32_bf16 v[78:81], v[238:241], v[218:221], v[78:81]
	v_mfma_f32_16x16x32_bf16 v[74:77], v[242:245], v[218:221], v[74:77]
	v_mfma_f32_16x16x32_bf16 v[70:73], v[246:249], v[218:221], v[70:73]
	v_mfma_f32_16x16x32_bf16 v[66:69], v[250:253], v[218:221], v[66:69]
	ds_read_b128 v[218:221], v93 offset:0
	ds_read_b128 v[142:145], v141 offset:0
	s_add_i32 s51, s51, 1
	s_and_b32 s54, s51, 7
	s_cmp_eq_u32 s54, 0
	s_cselect_b32 s44, s34, s35
	s_cselect_b32 s45, -1, 0
	v_lshl_add_u64 v[132:133], v[132:133], 0, s[44:45]
	global_load_dwordx2 v[202:203], v[132:133], off
	v_lshl_add_u64 v[180:181], v[132:133], 0, s[24:25]
	global_load_dwordx2 v[204:205], v[180:181], off
	v_mfma_f32_16x16x32_bf16 v[62:65], v[238:241], v[222:225], v[62:65]
	v_mfma_f32_16x16x32_bf16 v[58:61], v[242:245], v[222:225], v[58:61]
	v_mfma_f32_16x16x32_bf16 v[54:57], v[246:249], v[222:225], v[54:57]
	v_mfma_f32_16x16x32_bf16 v[50:53], v[250:253], v[222:225], v[50:53]
	ds_read_b128 v[222:225], v93 offset:2048
	ds_read_b128 v[146:149], v141 offset:2048
	v_lshl_add_u64 v[180:181], v[132:133], 0, s[26:27]
	global_load_dwordx2 v[206:207], v[180:181], off
	v_lshl_add_u64 v[180:181], v[132:133], 0, s[28:29]
	global_load_dwordx2 v[208:209], v[180:181], off
	v_mfma_f32_16x16x32_bf16 v[46:49], v[238:241], v[226:229], v[46:49]
	v_mfma_f32_16x16x32_bf16 v[42:45], v[242:245], v[226:229], v[42:45]
	v_mfma_f32_16x16x32_bf16 v[38:41], v[246:249], v[226:229], v[38:41]
	v_mfma_f32_16x16x32_bf16 v[34:37], v[250:253], v[226:229], v[34:37]
	ds_read_b128 v[226:229], v93 offset:4096
	ds_read_b128 v[156:159], v141 offset:4096
	v_lshl_add_u64 v[180:181], v[132:133], 0, s[36:37]
	global_load_dwordx2 v[210:211], v[180:181], off
	v_lshl_add_u64 v[180:181], v[132:133], 0, s[38:39]
	global_load_dwordx2 v[212:213], v[180:181], off
	v_mfma_f32_16x16x32_bf16 v[18:21], v[238:241], v[230:233], v[18:21]
	v_mfma_f32_16x16x32_bf16 v[22:25], v[242:245], v[230:233], v[22:25]
	v_mfma_f32_16x16x32_bf16 v[26:29], v[246:249], v[230:233], v[26:29]
	v_mfma_f32_16x16x32_bf16 v[30:33], v[250:253], v[230:233], v[30:33]
	ds_read_b128 v[230:233], v93 offset:6144
	ds_read_b128 v[160:163], v141 offset:6144
	v_lshl_add_u64 v[180:181], v[132:133], 0, s[40:41]
	global_load_dwordx2 v[214:215], v[180:181], off
	v_lshl_add_u64 v[180:181], v[132:133], 0, s[42:43]
	global_load_dwordx2 v[216:217], v[180:181], off
	v_mfma_f32_16x16x32_bf16 v[2:5], v[238:241], v[234:237], v[2:5]
	v_mfma_f32_16x16x32_bf16 v[6:9], v[242:245], v[234:237], v[6:9]
	v_mfma_f32_16x16x32_bf16 v[10:13], v[246:249], v[234:237], v[10:13]
	v_mfma_f32_16x16x32_bf16 v[14:17], v[250:253], v[234:237], v[14:17]
	ds_read_b128 v[234:237], v93 offset:8192
	s_waitcnt vmcnt(21)
	s_waitcnt lgkmcnt(0)
	s_barrier
	s_mov_b32 s49, s46
	s_mov_b32 s46, s47
	s_mov_b32 s47, s48
	s_mov_b32 s48, s49
	s_add_i32 s50, s50, 1
	s_add_i32 s49, s48, s74
	s_add_i32 s52, s52, 1
	s_and_b32 s54, s52, 7
	s_cmp_eq_u32 s54, 0
	s_cselect_b32 s54, s53, s32
	s_cselect_b32 s55, -1, 0
	s_add_u32 s30, s30, s54
	s_addc_u32 s31, s31, s55
	v_mfma_f32_16x16x32_bf16 v[78:81], v[142:145], v[218:221], v[78:81]
	v_mfma_f32_16x16x32_bf16 v[74:77], v[146:149], v[218:221], v[74:77]
	v_mfma_f32_16x16x32_bf16 v[70:73], v[156:159], v[218:221], v[70:73]
	v_mfma_f32_16x16x32_bf16 v[66:69], v[160:163], v[218:221], v[66:69]
	s_mov_b32 m0, s49
	s_nop 0
	global_load_lds_dwordx4 v88, s[30:31]
	v_mfma_f32_16x16x32_bf16 v[62:65], v[142:145], v[222:225], v[62:65]
	v_mfma_f32_16x16x32_bf16 v[58:61], v[146:149], v[222:225], v[58:61]
	v_mfma_f32_16x16x32_bf16 v[54:57], v[156:159], v[222:225], v[54:57]
	v_mfma_f32_16x16x32_bf16 v[50:53], v[160:163], v[222:225], v[50:53]
	s_add_i32 m0, s49, 0x2000
	s_nop 0
	global_load_lds_dwordx4 v90, s[30:31]
	v_mfma_f32_16x16x32_bf16 v[46:49], v[142:145], v[226:229], v[46:49]
	v_mfma_f32_16x16x32_bf16 v[42:45], v[146:149], v[226:229], v[42:45]
	v_mfma_f32_16x16x32_bf16 v[38:41], v[156:159], v[226:229], v[38:41]
	v_mfma_f32_16x16x32_bf16 v[34:37], v[160:163], v[226:229], v[34:37]
	s_add_i32 m0, s49, 0x4000
	s_nop 0
	global_load_lds_dwordx4 v92, s[30:31]
	v_mfma_f32_16x16x32_bf16 v[18:21], v[142:145], v[230:233], v[18:21]
	v_mfma_f32_16x16x32_bf16 v[22:25], v[146:149], v[230:233], v[22:25]
	v_mfma_f32_16x16x32_bf16 v[26:29], v[156:159], v[230:233], v[26:29]
	v_mfma_f32_16x16x32_bf16 v[30:33], v[160:163], v[230:233], v[30:33]
	s_add_i32 m0, s49, 0x6000
	s_nop 0
	global_load_lds_dwordx4 v94, s[30:31]
	v_mfma_f32_16x16x32_bf16 v[2:5], v[142:145], v[234:237], v[2:5]
	v_mfma_f32_16x16x32_bf16 v[6:9], v[146:149], v[234:237], v[6:9]
	v_mfma_f32_16x16x32_bf16 v[10:13], v[156:159], v[234:237], v[10:13]
	v_mfma_f32_16x16x32_bf16 v[14:17], v[160:163], v[234:237], v[14:17]
	s_add_i32 m0, s49, 0x8000
	s_nop 0
	global_load_lds_dwordx4 v96, s[30:31]
	v_cvt_pk_bf16_f32 v172, v98, v100
	v_cvt_pk_bf16_f32 v173, v102, v104
	v_cvt_pk_bf16_f32 v174, v106, v108
	v_cvt_pk_bf16_f32 v175, v110, v112
	v_cvt_pk_bf16_f32 v176, v99, v101
	v_cvt_pk_bf16_f32 v177, v103, v105
	v_cvt_pk_bf16_f32 v178, v107, v109
	v_cvt_pk_bf16_f32 v179, v111, v113
	ds_write_b128 v95, v[172:175] offset:0
	ds_write_b128 v95, v[176:179] offset:128
	v_add_u32_e32 v91, s46, v135
	v_add_u32_e32 v93, s46, v137
	ds_read_b128 v[238:241], v139 offset:19456
	ds_read_b128 v[242:245], v139 offset:21504
	ds_read_b128 v[246:249], v139 offset:23552
	ds_read_b128 v[250:253], v139 offset:25600
	ds_read_b128 v[218:221], v91 offset:0
	ds_read_b128 v[222:225], v91 offset:2048
	ds_read_b128 v[226:229], v91 offset:4096
	ds_read_b128 v[230:233], v91 offset:6144
	ds_read_b128 v[234:237], v91 offset:8192
	s_waitcnt lgkmcnt(0)
; #define PG8_LAS __attribute__((address_space(3)))
; __device__ __forceinline__ unsigned cvtpk(float lo, float hi) { f32x2 v = {lo, hi}; bf16x2_t b = __builtin_convertvector(v, bf16x2_t); return __builtin_bit_cast(unsigned, b); }
; #define MD_GLDS_A(buf, tau) do { _Pragma("unroll") for (int i = 0; i < 5; ++i) if (amask & (1u << i)) \
;         __builtin_amdgcn_global_load_lds((const unsigned*)((const char*)HIDp + aoff[i] + (size_t)((tau) & 7) * 128), (PG8_LAS unsigned*)(MD_SA(buf) + wid * 1024 + i * 8192), 16, 0, 0); } while (0)
; __device__ __forceinline__ void moe_down_stream(PG8_LAS unsigned char* lds, int e, int cb0, int slot0, int nv, const bf16_t* HIDp, const float* Wd, bf16_t* Y, const float* slot_w, const int* slot_dst) {
;     ...
;         if (t + 2 < NT) MD_B_WAIT(s1, 8); else MD_B_WAIT(s1, 0);
;         MD_B_WRITE(s1, 1); __builtin_amdgcn_sched_barrier(0); MD_GLDS_A(1, t + 1); __builtin_amdgcn_sched_barrier(0);
;         if (t + 3 < NT) MD_B_ISSUE(s1, t + 3);
;         MD_COMPUTE(0);
;         MD_END(t + 3 >= NT);
;         if (t + 2 < NT) { MD_B_WAIT(s0, 8); MD_B_WRITE(s0, 0); __builtin_amdgcn_sched_barrier(0); MD_GLDS_A(0, t + 2); __builtin_amdgcn_sched_barrier(0); }
;         if (t + 4 < NT) MD_B_ISSUE(s0, t + 4);
;         MD_COMPUTE(1);
;         MD_END(t + 4 >= NT);
;         if (((t + 1) & 7) == 7) {
;             const int cb = cb0 + ((t + 1) >> 3);
; #pragma unroll
;             for (int m = 0; m < DNM; ++m) {
;                 const float w_ = lw[4 * (16 * m + fr) + wr];
; #pragma unroll
;                 for (int p = 0; p < 2; ++p) { const f32x4 v0 = acc[m][2 * p] * w_, v1 = acc[m][2 * p + 1] * w_; u32x4 w; w.x = cvtpk(v0[0], v0[1]); w.y = cvtpk(v0[2], v0[3]); w.z = cvtpk(v1[0], v1[1]); w.w = cvtpk(v1[2], v1[3]);
;                     *(PG8_LAS u32x4*)(stg + fr * 128 + (((4 * p + fq) ^ (fr & 7)) * 16)) = w; }
; #pragma unroll
;                 for (int hh = 0; hh < 2; ++hh) { const int r = (lane >> 3) + 8 * hh, cc = lane & 7; const u32x4 d = *(const PG8_LAS u32x4*)(stg + r * 128 + ((cc ^ (r & 7)) * 16)); const int dst_ = ldst[4 * (16 * m + r) + wr];
;                     if (dst_ >= 0) *(u32x4*)(Y + (size_t)dst_ * D + 128 * cb + 64 * wc + 8 * cc) = d; }
; #pragma unroll
;                 for (int n = 0; n < 4; ++n) acc[m][n] = (f32x4){0.f, 0.f, 0.f, 0.f}; } }
	v_mfma_f32_16x16x32_bf16 v[78:81], v[238:241], v[218:221], v[78:81]
	v_mfma_f32_16x16x32_bf16 v[74:77], v[242:245], v[218:221], v[74:77]
	v_mfma_f32_16x16x32_bf16 v[70:73], v[246:249], v[218:221], v[70:73]
	v_mfma_f32_16x16x32_bf16 v[66:69], v[250:253], v[218:221], v[66:69]
	ds_read_b128 v[218:221], v93 offset:0
	ds_read_b128 v[142:145], v141 offset:19456
	s_add_i32 s51, s51, 1
	s_and_b32 s54, s51, 7
	s_cmp_eq_u32 s54, 0
	s_cselect_b32 s44, s34, s35
	s_cselect_b32 s45, -1, 0
	v_lshl_add_u64 v[132:133], v[132:133], 0, s[44:45]
	global_load_dwordx2 v[98:99], v[132:133], off
	v_lshl_add_u64 v[180:181], v[132:133], 0, s[24:25]
	global_load_dwordx2 v[100:101], v[180:181], off
	v_mfma_f32_16x16x32_bf16 v[62:65], v[238:241], v[222:225], v[62:65]
	v_mfma_f32_16x16x32_bf16 v[58:61], v[242:245], v[222:225], v[58:61]
	v_mfma_f32_16x16x32_bf16 v[54:57], v[246:249], v[222:225], v[54:57]
	v_mfma_f32_16x16x32_bf16 v[50:53], v[250:253], v[222:225], v[50:53]
	ds_read_b128 v[222:225], v93 offset:2048
	ds_read_b128 v[146:149], v141 offset:21504
	v_lshl_add_u64 v[180:181], v[132:133], 0, s[26:27]
	global_load_dwordx2 v[102:103], v[180:181], off
	v_lshl_add_u64 v[180:181], v[132:133], 0, s[28:29]
	global_load_dwordx2 v[104:105], v[180:181], off
	v_mfma_f32_16x16x32_bf16 v[46:49], v[238:241], v[226:229], v[46:49]
	v_mfma_f32_16x16x32_bf16 v[42:45], v[242:245], v[226:229], v[42:45]
	v_mfma_f32_16x16x32_bf16 v[38:41], v[246:249], v[226:229], v[38:41]
	v_mfma_f32_16x16x32_bf16 v[34:37], v[250:253], v[226:229], v[34:37]
	ds_read_b128 v[226:229], v93 offset:4096
	ds_read_b128 v[156:159], v141 offset:23552
	v_lshl_add_u64 v[180:181], v[132:133], 0, s[36:37]
	global_load_dwordx2 v[106:107], v[180:181], off
	v_lshl_add_u64 v[180:181], v[132:133], 0, s[38:39]
	global_load_dwordx2 v[108:109], v[180:181], off
	v_mfma_f32_16x16x32_bf16 v[18:21], v[238:241], v[230:233], v[18:21]
	v_mfma_f32_16x16x32_bf16 v[22:25], v[242:245], v[230:233], v[22:25]
	v_mfma_f32_16x16x32_bf16 v[26:29], v[246:249], v[230:233], v[26:29]
	v_mfma_f32_16x16x32_bf16 v[30:33], v[250:253], v[230:233], v[30:33]
	ds_read_b128 v[230:233], v93 offset:6144
	ds_read_b128 v[160:163], v141 offset:25600
	v_lshl_add_u64 v[180:181], v[132:133], 0, s[40:41]
	global_load_dwordx2 v[110:111], v[180:181], off
	v_lshl_add_u64 v[180:181], v[132:133], 0, s[42:43]
	global_load_dwordx2 v[112:113], v[180:181], off
	v_mfma_f32_16x16x32_bf16 v[2:5], v[238:241], v[234:237], v[2:5]
	v_mfma_f32_16x16x32_bf16 v[6:9], v[242:245], v[234:237], v[6:9]
	v_mfma_f32_16x16x32_bf16 v[10:13], v[246:249], v[234:237], v[10:13]
	v_mfma_f32_16x16x32_bf16 v[14:17], v[250:253], v[234:237], v[14:17]
	ds_read_b128 v[234:237], v93 offset:8192
	s_waitcnt vmcnt(21)
	s_waitcnt lgkmcnt(0)
	s_barrier
	s_mov_b32 s49, s46
	s_mov_b32 s46, s47
	s_mov_b32 s47, s48
	s_mov_b32 s48, s49
	s_add_i32 s50, s50, 1
	s_sub_u32 s56, s56, 1
	s_cmp_lg_u32 s56, 0
	s_cbranch_scc1 .Lmd_loop_Y
	v_mfma_f32_16x16x32_bf16 v[78:81], v[142:145], v[218:221], v[78:81]
	v_mfma_f32_16x16x32_bf16 v[74:77], v[146:149], v[218:221], v[74:77]
	v_mfma_f32_16x16x32_bf16 v[70:73], v[156:159], v[218:221], v[70:73]
	v_mfma_f32_16x16x32_bf16 v[66:69], v[160:163], v[218:221], v[66:69]
	v_mfma_f32_16x16x32_bf16 v[62:65], v[142:145], v[222:225], v[62:65]
	v_mfma_f32_16x16x32_bf16 v[58:61], v[146:149], v[222:225], v[58:61]
	v_mfma_f32_16x16x32_bf16 v[54:57], v[156:159], v[222:225], v[54:57]
	v_mfma_f32_16x16x32_bf16 v[50:53], v[160:163], v[222:225], v[50:53]
	v_mfma_f32_16x16x32_bf16 v[46:49], v[142:145], v[226:229], v[46:49]
	v_mfma_f32_16x16x32_bf16 v[42:45], v[146:149], v[226:229], v[42:45]
	v_mfma_f32_16x16x32_bf16 v[38:41], v[156:159], v[226:229], v[38:41]
	v_mfma_f32_16x16x32_bf16 v[34:37], v[160:163], v[226:229], v[34:37]
	v_mfma_f32_16x16x32_bf16 v[18:21], v[142:145], v[230:233], v[18:21]
	v_mfma_f32_16x16x32_bf16 v[22:25], v[146:149], v[230:233], v[22:25]
	v_mfma_f32_16x16x32_bf16 v[26:29], v[156:159], v[230:233], v[26:29]
	v_mfma_f32_16x16x32_bf16 v[30:33], v[160:163], v[230:233], v[30:33]
	v_mfma_f32_16x16x32_bf16 v[2:5], v[142:145], v[234:237], v[2:5]
	v_mfma_f32_16x16x32_bf16 v[6:9], v[146:149], v[234:237], v[6:9]
	v_mfma_f32_16x16x32_bf16 v[10:13], v[156:159], v[234:237], v[10:13]
	v_mfma_f32_16x16x32_bf16 v[14:17], v[160:163], v[234:237], v[14:17]
	s_add_i32 s54, s48, s74
	v_add_u32_e32 v164, s54, v84
	v_add_u32_e32 v165, s54, v85
	ds_read_b32 v150, v82 offset:0
	ds_read_b32 v151, v83 offset:0
	ds_read_b32 v166, v83 offset:128
	s_waitcnt lgkmcnt(2)
	v_mul_f32_e32 v78, v150, v78
	v_mul_f32_e32 v79, v150, v79
	v_mul_f32_e32 v80, v150, v80
	v_mul_f32_e32 v81, v150, v81
	v_mul_f32_e32 v74, v150, v74
	v_mul_f32_e32 v75, v150, v75
	v_mul_f32_e32 v76, v150, v76
	v_mul_f32_e32 v77, v150, v77
	v_cvt_pk_bf16_f32 v182, v78, v79
	v_cvt_pk_bf16_f32 v183, v80, v81
	v_cvt_pk_bf16_f32 v184, v74, v75
	v_cvt_pk_bf16_f32 v185, v76, v77
	ds_write_b128 v164, v[182:185]
	v_mul_f32_e32 v70, v150, v70
	v_mul_f32_e32 v71, v150, v71
	v_mul_f32_e32 v72, v150, v72
	v_mul_f32_e32 v73, v150, v73
	v_mul_f32_e32 v66, v150, v66
	v_mul_f32_e32 v67, v150, v67
	v_mul_f32_e32 v68, v150, v68
	v_mul_f32_e32 v69, v150, v69
	v_cvt_pk_bf16_f32 v182, v70, v71
	v_cvt_pk_bf16_f32 v183, v72, v73
	v_cvt_pk_bf16_f32 v184, v66, v67
	v_cvt_pk_bf16_f32 v185, v68, v69
	v_xor_b32_e32 v167, 64, v164
	ds_write_b128 v167, v[182:185]
	v_mov_b32_e32 v78, 0
	v_mov_b32_e32 v74, 0
	v_mov_b32_e32 v70, 0
	v_mov_b32_e32 v66, 0
	v_mov_b32_e32 v79, 0
	v_mov_b32_e32 v75, 0
	v_mov_b32_e32 v71, 0
	v_mov_b32_e32 v67, 0
	v_mov_b32_e32 v80, 0
	v_mov_b32_e32 v76, 0
	v_mov_b32_e32 v72, 0
	v_mov_b32_e32 v68, 0
	v_mov_b32_e32 v81, 0
	v_mov_b32_e32 v77, 0
	v_mov_b32_e32 v73, 0
	v_mov_b32_e32 v69, 0
	ds_read_b128 v[182:185], v165 offset:0
	v_cmp_lt_i32_e32 vcc, -1, v151
	v_lshlrev_b32_e32 v148, 13, v151
	v_mov_b32_e32 v149, 0
	v_lshl_add_u64 v[148:149], v[148:149], 0, v[86:87]
	v_cndmask_b32_e32 v148, v168, v148, vcc
	v_cndmask_b32_e32 v149, v169, v149, vcc
	s_waitcnt lgkmcnt(0)
; #define PG8_LAS __attribute__((address_space(3)))
; __device__ __forceinline__ unsigned cvtpk(float lo, float hi) { f32x2 v = {lo, hi}; bf16x2_t b = __builtin_convertvector(v, bf16x2_t); return __builtin_bit_cast(unsigned, b); }
; __device__ __forceinline__ void moe_down_stream(PG8_LAS unsigned char* lds, int e, int cb0, int slot0, int nv, const bf16_t* HIDp, const float* Wd, bf16_t* Y, const float* slot_w, const int* slot_dst) {
;     ...
;         if (((t + 1) & 7) == 7) {
;             const int cb = cb0 + ((t + 1) >> 3);
; #pragma unroll
;             for (int m = 0; m < DNM; ++m) {
;                 const float w_ = lw[4 * (16 * m + fr) + wr];
; #pragma unroll
;                 for (int p = 0; p < 2; ++p) { const f32x4 v0 = acc[m][2 * p] * w_, v1 = acc[m][2 * p + 1] * w_; u32x4 w; w.x = cvtpk(v0[0], v0[1]); w.y = cvtpk(v0[2], v0[3]); w.z = cvtpk(v1[0], v1[1]); w.w = cvtpk(v1[2], v1[3]);
;                     *(PG8_LAS u32x4*)(stg + fr * 128 + (((4 * p + fq) ^ (fr & 7)) * 16)) = w; }
; #pragma unroll
;                 for (int hh = 0; hh < 2; ++hh) { const int r = (lane >> 3) + 8 * hh, cc = lane & 7; const u32x4 d = *(const PG8_LAS u32x4*)(stg + r * 128 + ((cc ^ (r & 7)) * 16)); const int dst_ = ldst[4 * (16 * m + r) + wr];
;                     if (dst_ >= 0) *(u32x4*)(Y + (size_t)dst_ * D + 128 * cb + 64 * wc + 8 * cc) = d; }
; #pragma unroll
;                 for (int n = 0; n < 4; ++n) acc[m][n] = (f32x4){0.f, 0.f, 0.f, 0.f}; } }
	global_store_dwordx4 v[148:149], v[182:185], off nt
	ds_read_b128 v[182:185], v165 offset:8192
	v_cmp_lt_i32_e32 vcc, -1, v166
	v_lshlrev_b32_e32 v148, 13, v166
	v_mov_b32_e32 v149, 0
	v_lshl_add_u64 v[148:149], v[148:149], 0, v[86:87]
	v_cndmask_b32_e32 v148, v168, v148, vcc
	v_cndmask_b32_e32 v149, v169, v149, vcc
	s_waitcnt lgkmcnt(0)
	global_store_dwordx4 v[148:149], v[182:185], off nt
	ds_read_b32 v150, v82 offset:256
	ds_read_b32 v151, v83 offset:256
	ds_read_b32 v166, v83 offset:384
	s_waitcnt lgkmcnt(2)
	v_mul_f32_e32 v62, v150, v62
	v_mul_f32_e32 v63, v150, v63
	v_mul_f32_e32 v64, v150, v64
	v_mul_f32_e32 v65, v150, v65
	v_mul_f32_e32 v58, v150, v58
	v_mul_f32_e32 v59, v150, v59
	v_mul_f32_e32 v60, v150, v60
	v_mul_f32_e32 v61, v150, v61
	v_cvt_pk_bf16_f32 v182, v62, v63
	v_cvt_pk_bf16_f32 v183, v64, v65
	v_cvt_pk_bf16_f32 v184, v58, v59
	v_cvt_pk_bf16_f32 v185, v60, v61
	ds_write_b128 v164, v[182:185]
	v_mul_f32_e32 v54, v150, v54
	v_mul_f32_e32 v55, v150, v55
	v_mul_f32_e32 v56, v150, v56
	v_mul_f32_e32 v57, v150, v57
	v_mul_f32_e32 v50, v150, v50
	v_mul_f32_e32 v51, v150, v51
	v_mul_f32_e32 v52, v150, v52
	v_mul_f32_e32 v53, v150, v53
	v_cvt_pk_bf16_f32 v182, v54, v55
	v_cvt_pk_bf16_f32 v183, v56, v57
	v_cvt_pk_bf16_f32 v184, v50, v51
	v_cvt_pk_bf16_f32 v185, v52, v53
	v_xor_b32_e32 v167, 64, v164
	ds_write_b128 v167, v[182:185]
	v_mov_b32_e32 v62, 0
	v_mov_b32_e32 v58, 0
	v_mov_b32_e32 v54, 0
	v_mov_b32_e32 v50, 0
	v_mov_b32_e32 v63, 0
	v_mov_b32_e32 v59, 0
	v_mov_b32_e32 v55, 0
	v_mov_b32_e32 v51, 0
	v_mov_b32_e32 v64, 0
	v_mov_b32_e32 v60, 0
	v_mov_b32_e32 v56, 0
	v_mov_b32_e32 v52, 0
	v_mov_b32_e32 v65, 0
	v_mov_b32_e32 v61, 0
	v_mov_b32_e32 v57, 0
	v_mov_b32_e32 v53, 0
	ds_read_b128 v[182:185], v165 offset:0
	v_cmp_lt_i32_e32 vcc, -1, v151
	v_lshlrev_b32_e32 v148, 13, v151
	v_mov_b32_e32 v149, 0
	v_lshl_add_u64 v[148:149], v[148:149], 0, v[86:87]
	v_cndmask_b32_e32 v148, v168, v148, vcc
	v_cndmask_b32_e32 v149, v169, v149, vcc
	s_waitcnt lgkmcnt(0)
	global_store_dwordx4 v[148:149], v[182:185], off nt
	ds_read_b128 v[182:185], v165 offset:8192
	v_cmp_lt_i32_e32 vcc, -1, v166
	v_lshlrev_b32_e32 v148, 13, v166
	v_mov_b32_e32 v149, 0
	v_lshl_add_u64 v[148:149], v[148:149], 0, v[86:87]
	v_cndmask_b32_e32 v148, v168, v148, vcc
	v_cndmask_b32_e32 v149, v169, v149, vcc
	s_waitcnt lgkmcnt(0)
	global_store_dwordx4 v[148:149], v[182:185], off nt
	ds_read_b32 v150, v82 offset:512
	ds_read_b32 v151, v83 offset:512
	ds_read_b32 v166, v83 offset:640
	s_waitcnt lgkmcnt(2)
	v_mul_f32_e32 v46, v150, v46
	v_mul_f32_e32 v47, v150, v47
	v_mul_f32_e32 v48, v150, v48
	v_mul_f32_e32 v49, v150, v49
	v_mul_f32_e32 v42, v150, v42
	v_mul_f32_e32 v43, v150, v43
	v_mul_f32_e32 v44, v150, v44
	v_mul_f32_e32 v45, v150, v45
	v_cvt_pk_bf16_f32 v182, v46, v47
	v_cvt_pk_bf16_f32 v183, v48, v49
	v_cvt_pk_bf16_f32 v184, v42, v43
	v_cvt_pk_bf16_f32 v185, v44, v45
	ds_write_b128 v164, v[182:185]
	v_mul_f32_e32 v38, v150, v38
	v_mul_f32_e32 v39, v150, v39
	v_mul_f32_e32 v40, v150, v40
	v_mul_f32_e32 v41, v150, v41
	v_mul_f32_e32 v34, v150, v34
	v_mul_f32_e32 v35, v150, v35
	v_mul_f32_e32 v36, v150, v36
	v_mul_f32_e32 v37, v150, v37
	v_cvt_pk_bf16_f32 v182, v38, v39
	v_cvt_pk_bf16_f32 v183, v40, v41
	v_cvt_pk_bf16_f32 v184, v34, v35
	v_cvt_pk_bf16_f32 v185, v36, v37
	v_xor_b32_e32 v167, 64, v164
	ds_write_b128 v167, v[182:185]
	v_mov_b32_e32 v46, 0
	v_mov_b32_e32 v42, 0
	v_mov_b32_e32 v38, 0
	v_mov_b32_e32 v34, 0
	v_mov_b32_e32 v47, 0
	v_mov_b32_e32 v43, 0
	v_mov_b32_e32 v39, 0
	v_mov_b32_e32 v35, 0
	v_mov_b32_e32 v48, 0
	v_mov_b32_e32 v44, 0
	v_mov_b32_e32 v40, 0
	v_mov_b32_e32 v36, 0
	v_mov_b32_e32 v49, 0
	v_mov_b32_e32 v45, 0
	v_mov_b32_e32 v41, 0
	v_mov_b32_e32 v37, 0
	ds_read_b128 v[182:185], v165 offset:0
	v_cmp_lt_i32_e32 vcc, -1, v151
	v_lshlrev_b32_e32 v148, 13, v151
	v_mov_b32_e32 v149, 0
	v_lshl_add_u64 v[148:149], v[148:149], 0, v[86:87]
	v_cndmask_b32_e32 v148, v168, v148, vcc
	v_cndmask_b32_e32 v149, v169, v149, vcc
	s_waitcnt lgkmcnt(0)
	global_store_dwordx4 v[148:149], v[182:185], off nt
	ds_read_b128 v[182:185], v165 offset:8192
	v_cmp_lt_i32_e32 vcc, -1, v166
	v_lshlrev_b32_e32 v148, 13, v166
	v_mov_b32_e32 v149, 0
	v_lshl_add_u64 v[148:149], v[148:149], 0, v[86:87]
	v_cndmask_b32_e32 v148, v168, v148, vcc
	v_cndmask_b32_e32 v149, v169, v149, vcc
	s_waitcnt lgkmcnt(0)
	global_store_dwordx4 v[148:149], v[182:185], off nt
	ds_read_b32 v150, v82 offset:768
	ds_read_b32 v151, v83 offset:768
	ds_read_b32 v166, v83 offset:896
	s_waitcnt lgkmcnt(2)
	v_mul_f32_e32 v18, v150, v18
	v_mul_f32_e32 v19, v150, v19
	v_mul_f32_e32 v20, v150, v20
	v_mul_f32_e32 v21, v150, v21
	v_mul_f32_e32 v22, v150, v22
	v_mul_f32_e32 v23, v150, v23
	v_mul_f32_e32 v24, v150, v24
	v_mul_f32_e32 v25, v150, v25
	v_cvt_pk_bf16_f32 v182, v18, v19
	v_cvt_pk_bf16_f32 v183, v20, v21
	v_cvt_pk_bf16_f32 v184, v22, v23
	v_cvt_pk_bf16_f32 v185, v24, v25
	ds_write_b128 v164, v[182:185]
	v_mul_f32_e32 v26, v150, v26
	v_mul_f32_e32 v27, v150, v27
	v_mul_f32_e32 v28, v150, v28
	v_mul_f32_e32 v29, v150, v29
	v_mul_f32_e32 v30, v150, v30
	v_mul_f32_e32 v31, v150, v31
	v_mul_f32_e32 v32, v150, v32
	v_mul_f32_e32 v33, v150, v33
	v_cvt_pk_bf16_f32 v182, v26, v27
	v_cvt_pk_bf16_f32 v183, v28, v29
	v_cvt_pk_bf16_f32 v184, v30, v31
	v_cvt_pk_bf16_f32 v185, v32, v33
	v_xor_b32_e32 v167, 64, v164
	ds_write_b128 v167, v[182:185]
	v_mov_b32_e32 v18, 0
	v_mov_b32_e32 v22, 0
	v_mov_b32_e32 v26, 0
	v_mov_b32_e32 v30, 0
	v_mov_b32_e32 v19, 0
	v_mov_b32_e32 v23, 0
	v_mov_b32_e32 v27, 0
	v_mov_b32_e32 v31, 0
	v_mov_b32_e32 v20, 0
	v_mov_b32_e32 v24, 0
	v_mov_b32_e32 v28, 0
	v_mov_b32_e32 v32, 0
	v_mov_b32_e32 v21, 0
	v_mov_b32_e32 v25, 0
	v_mov_b32_e32 v29, 0
	v_mov_b32_e32 v33, 0
	ds_read_b128 v[182:185], v165 offset:0
	v_cmp_lt_i32_e32 vcc, -1, v151
	v_lshlrev_b32_e32 v148, 13, v151
	v_mov_b32_e32 v149, 0
	v_lshl_add_u64 v[148:149], v[148:149], 0, v[86:87]
	v_cndmask_b32_e32 v148, v168, v148, vcc
	v_cndmask_b32_e32 v149, v169, v149, vcc
	s_waitcnt lgkmcnt(0)
; #define PG8_LAS __attribute__((address_space(3)))
; __device__ __forceinline__ unsigned cvtpk(float lo, float hi) { f32x2 v = {lo, hi}; bf16x2_t b = __builtin_convertvector(v, bf16x2_t); return __builtin_bit_cast(unsigned, b); }
; #define MD_GLDS_A(buf, tau) do { _Pragma("unroll") for (int i = 0; i < 5; ++i) if (amask & (1u << i)) \
;         __builtin_amdgcn_global_load_lds((const unsigned*)((const char*)HIDp + aoff[i] + (size_t)((tau) & 7) * 128), (PG8_LAS unsigned*)(MD_SA(buf) + wid * 1024 + i * 8192), 16, 0, 0); } while (0)
; __device__ __forceinline__ void moe_down_stream(PG8_LAS unsigned char* lds, int e, int cb0, int slot0, int nv, const bf16_t* HIDp, const float* Wd, bf16_t* Y, const float* slot_w, const int* slot_dst) {
;     ...
;         if (t + 2 < NT) MD_B_WAIT(s1, 8); else MD_B_WAIT(s1, 0);
;         MD_B_WRITE(s1, 1); __builtin_amdgcn_sched_barrier(0); MD_GLDS_A(1, t + 1); __builtin_amdgcn_sched_barrier(0);
;         if (t + 3 < NT) MD_B_ISSUE(s1, t + 3);
;         MD_COMPUTE(0);
;         MD_END(t + 3 >= NT);
;         if (t + 2 < NT) { MD_B_WAIT(s0, 8); MD_B_WRITE(s0, 0); __builtin_amdgcn_sched_barrier(0); MD_GLDS_A(0, t + 2); __builtin_amdgcn_sched_barrier(0); }
;         if (t + 4 < NT) MD_B_ISSUE(s0, t + 4);
;         MD_COMPUTE(1);
;         MD_END(t + 4 >= NT);
;         if (((t + 1) & 7) == 7) {
;             const int cb = cb0 + ((t + 1) >> 3);
; #pragma unroll
;             for (int m = 0; m < DNM; ++m) {
;                 const float w_ = lw[4 * (16 * m + fr) + wr];
; #pragma unroll
;                 for (int p = 0; p < 2; ++p) { const f32x4 v0 = acc[m][2 * p] * w_, v1 = acc[m][2 * p + 1] * w_; u32x4 w; w.x = cvtpk(v0[0], v0[1]); w.y = cvtpk(v0[2], v0[3]); w.z = cvtpk(v1[0], v1[1]); w.w = cvtpk(v1[2], v1[3]);
;                     *(PG8_LAS u32x4*)(stg + fr * 128 + (((4 * p + fq) ^ (fr & 7)) * 16)) = w; }
; #pragma unroll
;                 for (int hh = 0; hh < 2; ++hh) { const int r = (lane >> 3) + 8 * hh, cc = lane & 7; const u32x4 d = *(const PG8_LAS u32x4*)(stg + r * 128 + ((cc ^ (r & 7)) * 16)); const int dst_ = ldst[4 * (16 * m + r) + wr];
;                     if (dst_ >= 0) *(u32x4*)(Y + (size_t)dst_ * D + 128 * cb + 64 * wc + 8 * cc) = d; }
; #pragma unroll
;                 for (int n = 0; n < 4; ++n) acc[m][n] = (f32x4){0.f, 0.f, 0.f, 0.f}; } }
	global_store_dwordx4 v[148:149], v[182:185], off nt
	ds_read_b128 v[182:185], v165 offset:8192
	v_cmp_lt_i32_e32 vcc, -1, v166
	v_lshlrev_b32_e32 v148, 13, v166
	v_mov_b32_e32 v149, 0
	v_lshl_add_u64 v[148:149], v[148:149], 0, v[86:87]
	v_cndmask_b32_e32 v148, v168, v148, vcc
	v_cndmask_b32_e32 v149, v169, v149, vcc
	s_waitcnt lgkmcnt(0)
	global_store_dwordx4 v[148:149], v[182:185], off nt
	ds_read_b32 v150, v82 offset:1024
	ds_read_b32 v151, v83 offset:1024
	ds_read_b32 v166, v83 offset:1152
	s_waitcnt lgkmcnt(2)
	v_mul_f32_e32 v2, v150, v2
	v_mul_f32_e32 v3, v150, v3
	v_mul_f32_e32 v4, v150, v4
	v_mul_f32_e32 v5, v150, v5
	v_mul_f32_e32 v6, v150, v6
	v_mul_f32_e32 v7, v150, v7
	v_mul_f32_e32 v8, v150, v8
	v_mul_f32_e32 v9, v150, v9
	v_cvt_pk_bf16_f32 v182, v2, v3
	v_cvt_pk_bf16_f32 v183, v4, v5
	v_cvt_pk_bf16_f32 v184, v6, v7
	v_cvt_pk_bf16_f32 v185, v8, v9
	ds_write_b128 v164, v[182:185]
	v_mul_f32_e32 v10, v150, v10
	v_mul_f32_e32 v11, v150, v11
	v_mul_f32_e32 v12, v150, v12
	v_mul_f32_e32 v13, v150, v13
	v_mul_f32_e32 v14, v150, v14
	v_mul_f32_e32 v15, v150, v15
	v_mul_f32_e32 v16, v150, v16
	v_mul_f32_e32 v17, v150, v17
	v_cvt_pk_bf16_f32 v182, v10, v11
	v_cvt_pk_bf16_f32 v183, v12, v13
	v_cvt_pk_bf16_f32 v184, v14, v15
	v_cvt_pk_bf16_f32 v185, v16, v17
	v_xor_b32_e32 v167, 64, v164
	ds_write_b128 v167, v[182:185]
	v_mov_b32_e32 v2, 0
	v_mov_b32_e32 v6, 0
	v_mov_b32_e32 v10, 0
	v_mov_b32_e32 v14, 0
	v_mov_b32_e32 v3, 0
	v_mov_b32_e32 v7, 0
	v_mov_b32_e32 v11, 0
	v_mov_b32_e32 v15, 0
	v_mov_b32_e32 v4, 0
	v_mov_b32_e32 v8, 0
	v_mov_b32_e32 v12, 0
	v_mov_b32_e32 v16, 0
	v_mov_b32_e32 v5, 0
	v_mov_b32_e32 v9, 0
	v_mov_b32_e32 v13, 0
	v_mov_b32_e32 v17, 0
	ds_read_b128 v[182:185], v165 offset:0
	v_cmp_lt_i32_e32 vcc, -1, v151
	v_lshlrev_b32_e32 v148, 13, v151
	v_mov_b32_e32 v149, 0
	v_lshl_add_u64 v[148:149], v[148:149], 0, v[86:87]
	v_cndmask_b32_e32 v148, v168, v148, vcc
	v_cndmask_b32_e32 v149, v169, v149, vcc
	s_waitcnt lgkmcnt(0)
	global_store_dwordx4 v[148:149], v[182:185], off nt
	ds_read_b128 v[182:185], v165 offset:8192
	v_cmp_lt_i32_e32 vcc, -1, v166
	v_lshlrev_b32_e32 v148, 13, v166
	v_mov_b32_e32 v149, 0
	v_lshl_add_u64 v[148:149], v[148:149], 0, v[86:87]
	v_cndmask_b32_e32 v148, v168, v148, vcc
	v_cndmask_b32_e32 v149, v169, v149, vcc
	s_waitcnt lgkmcnt(0)
	global_store_dwordx4 v[148:149], v[182:185], off nt
	v_add_co_u32_e32 v86, vcc, 0x400, v86
	s_nop 1
	v_addc_co_u32_e32 v87, vcc, 0, v87, vcc
	s_waitcnt lgkmcnt(0)
	s_add_i32 s49, s48, s74
	s_add_i32 s52, s52, 1
	s_and_b32 s54, s52, 7
	s_cmp_eq_u32 s54, 0
	s_cselect_b32 s54, s53, s32
	s_cselect_b32 s55, -1, 0
	s_add_u32 s30, s30, s54
	s_addc_u32 s31, s31, s55
	s_mov_b32 m0, s49
	s_nop 0
	global_load_lds_dwordx4 v88, s[30:31]
	s_add_i32 m0, s49, 0x2000
	s_nop 0
	global_load_lds_dwordx4 v90, s[30:31]
	s_add_i32 m0, s49, 0x4000
	s_nop 0
	global_load_lds_dwordx4 v92, s[30:31]
	s_add_i32 m0, s49, 0x6000
	s_nop 0
	global_load_lds_dwordx4 v94, s[30:31]
	s_add_i32 m0, s49, 0x8000
	s_nop 0
	global_load_lds_dwordx4 v96, s[30:31]
	v_cvt_pk_bf16_f32 v172, v114, v116
	v_cvt_pk_bf16_f32 v173, v118, v120
	v_cvt_pk_bf16_f32 v174, v122, v124
	v_cvt_pk_bf16_f32 v175, v126, v128
	v_cvt_pk_bf16_f32 v176, v115, v117
	v_cvt_pk_bf16_f32 v177, v119, v121
	v_cvt_pk_bf16_f32 v178, v123, v125
	v_cvt_pk_bf16_f32 v179, v127, v129
	ds_write_b128 v95, v[172:175] offset:19456
	ds_write_b128 v95, v[176:179] offset:19584
	v_add_u32_e32 v91, s46, v135
	v_add_u32_e32 v93, s46, v137
	ds_read_b128 v[238:241], v139 offset:0
	ds_read_b128 v[242:245], v139 offset:2048
	ds_read_b128 v[246:249], v139 offset:4096
	ds_read_b128 v[250:253], v139 offset:6144
	ds_read_b128 v[218:221], v91 offset:0
	ds_read_b128 v[222:225], v91 offset:2048
	ds_read_b128 v[226:229], v91 offset:4096
	ds_read_b128 v[230:233], v91 offset:6144
	ds_read_b128 v[234:237], v91 offset:8192
	s_waitcnt lgkmcnt(0)
	v_mfma_f32_16x16x32_bf16 v[78:81], v[238:241], v[218:221], v[78:81]
	v_mfma_f32_16x16x32_bf16 v[74:77], v[242:245], v[218:221], v[74:77]
	v_mfma_f32_16x16x32_bf16 v[70:73], v[246:249], v[218:221], v[70:73]
	v_mfma_f32_16x16x32_bf16 v[66:69], v[250:253], v[218:221], v[66:69]
	ds_read_b128 v[218:221], v93 offset:0
	ds_read_b128 v[142:145], v141 offset:0
	s_add_i32 s51, s51, 1
	s_and_b32 s54, s51, 7
	s_cmp_eq_u32 s54, 0
	s_cselect_b32 s44, s34, s35
	s_cselect_b32 s45, -1, 0
	v_lshl_add_u64 v[132:133], v[132:133], 0, s[44:45]
	global_load_dwordx2 v[114:115], v[132:133], off
	v_lshl_add_u64 v[180:181], v[132:133], 0, s[24:25]
	global_load_dwordx2 v[116:117], v[180:181], off
	v_mfma_f32_16x16x32_bf16 v[62:65], v[238:241], v[222:225], v[62:65]
	v_mfma_f32_16x16x32_bf16 v[58:61], v[242:245], v[222:225], v[58:61]
	v_mfma_f32_16x16x32_bf16 v[54:57], v[246:249], v[222:225], v[54:57]
	v_mfma_f32_16x16x32_bf16 v[50:53], v[250:253], v[222:225], v[50:53]
	ds_read_b128 v[222:225], v93 offset:2048
	ds_read_b128 v[146:149], v141 offset:2048
	v_lshl_add_u64 v[180:181], v[132:133], 0, s[26:27]
	global_load_dwordx2 v[118:119], v[180:181], off
	v_lshl_add_u64 v[180:181], v[132:133], 0, s[28:29]
	global_load_dwordx2 v[120:121], v[180:181], off
	v_mfma_f32_16x16x32_bf16 v[46:49], v[238:241], v[226:229], v[46:49]
	v_mfma_f32_16x16x32_bf16 v[42:45], v[242:245], v[226:229], v[42:45]
	v_mfma_f32_16x16x32_bf16 v[38:41], v[246:249], v[226:229], v[38:41]
	v_mfma_f32_16x16x32_bf16 v[34:37], v[250:253], v[226:229], v[34:37]
	ds_read_b128 v[226:229], v93 offset:4096
	ds_read_b128 v[156:159], v141 offset:4096
	v_lshl_add_u64 v[180:181], v[132:133], 0, s[36:37]
	global_load_dwordx2 v[122:123], v[180:181], off
	v_lshl_add_u64 v[180:181], v[132:133], 0, s[38:39]
	global_load_dwordx2 v[124:125], v[180:181], off
	v_mfma_f32_16x16x32_bf16 v[18:21], v[238:241], v[230:233], v[18:21]
	v_mfma_f32_16x16x32_bf16 v[22:25], v[242:245], v[230:233], v[22:25]
	v_mfma_f32_16x16x32_bf16 v[26:29], v[246:249], v[230:233], v[26:29]
	v_mfma_f32_16x16x32_bf16 v[30:33], v[250:253], v[230:233], v[30:33]
	ds_read_b128 v[230:233], v93 offset:6144
	ds_read_b128 v[160:163], v141 offset:6144
	v_lshl_add_u64 v[180:181], v[132:133], 0, s[40:41]
	global_load_dwordx2 v[126:127], v[180:181], off
	v_lshl_add_u64 v[180:181], v[132:133], 0, s[42:43]
	global_load_dwordx2 v[128:129], v[180:181], off
	v_mfma_f32_16x16x32_bf16 v[2:5], v[238:241], v[234:237], v[2:5]
	v_mfma_f32_16x16x32_bf16 v[6:9], v[242:245], v[234:237], v[6:9]
	v_mfma_f32_16x16x32_bf16 v[10:13], v[246:249], v[234:237], v[10:13]
	v_mfma_f32_16x16x32_bf16 v[14:17], v[250:253], v[234:237], v[14:17]
	ds_read_b128 v[234:237], v93 offset:8192
	s_waitcnt vmcnt(31)
	s_waitcnt lgkmcnt(0)
	s_barrier
; #define MD_GLDS_A(buf, tau) do { _Pragma("unroll") for (int i = 0; i < 5; ++i) if (amask & (1u << i)) \
;         __builtin_amdgcn_global_load_lds((const unsigned*)((const char*)HIDp + aoff[i] + (size_t)((tau) & 7) * 128), (PG8_LAS unsigned*)(MD_SA(buf) + wid * 1024 + i * 8192), 16, 0, 0); } while (0)
; #define MD_B_ISSUE(sb, tau) do { const char* kb_ = Bb + (size_t)((tau) >> 3) * 512 + (size_t)((tau) & 7) * (64 * (size_t)RB); _Pragma("unroll") for (int j = 0; j < 8; ++j) { const char* p_ = kb_ + (size_t)j * RB; \
;         asm volatile("global_load_dwordx2 %0, %1, off" : "=&v"(sb[j]) : "v"(p_) : "memory"); } } while (0)
; #define MD_B_WAIT(sb, N) asm volatile("s_waitcnt vmcnt(%8)" : "+v"(sb[0]), "+v"(sb[1]), "+v"(sb[2]), "+v"(sb[3]), "+v"(sb[4]), "+v"(sb[5]), "+v"(sb[6]), "+v"(sb[7]) : "n"(N) : "memory")
; #define MD_END(last) do { if (last) asm volatile("s_waitcnt vmcnt(0)" ::: "memory"); else asm volatile("s_waitcnt vmcnt(8)" ::: "memory"); \
;         asm volatile("s_waitcnt lgkmcnt(0)" ::: "memory"); __builtin_amdgcn_s_barrier(); asm volatile("" ::: "memory"); } while (0)
; __device__ __forceinline__ void moe_down_stream(PG8_LAS unsigned char* lds, int e, int cb0, int slot0, int nv, const bf16_t* HIDp, const float* Wd, bf16_t* Y, const float* slot_w, const int* slot_dst) {
;     ...
;         if (t + 2 < NT) MD_B_WAIT(s1, 8); else MD_B_WAIT(s1, 0);
;         MD_B_WRITE(s1, 1); __builtin_amdgcn_sched_barrier(0); MD_GLDS_A(1, t + 1); __builtin_amdgcn_sched_barrier(0);
;         if (t + 3 < NT) MD_B_ISSUE(s1, t + 3);
;         MD_COMPUTE(0);
;         MD_END(t + 3 >= NT);
;         if (t + 2 < NT) { MD_B_WAIT(s0, 8); MD_B_WRITE(s0, 0); __builtin_amdgcn_sched_barrier(0); MD_GLDS_A(0, t + 2); __builtin_amdgcn_sched_barrier(0); }
;         if (t + 4 < NT) MD_B_ISSUE(s0, t + 4);
;         MD_COMPUTE(1);
;         MD_END(t + 4 >= NT);
	s_mov_b32 s49, s46
	s_mov_b32 s46, s47
	s_mov_b32 s47, s48
	s_mov_b32 s48, s49
	s_add_i32 s50, s50, 1
	s_add_i32 s49, s48, s74
	s_add_i32 s52, s52, 1
	s_and_b32 s54, s52, 7
	s_cmp_eq_u32 s54, 0
	s_cselect_b32 s54, s53, s32
	s_cselect_b32 s55, -1, 0
	s_add_u32 s30, s30, s54
	s_addc_u32 s31, s31, s55
	v_mfma_f32_16x16x32_bf16 v[78:81], v[142:145], v[218:221], v[78:81]
	v_mfma_f32_16x16x32_bf16 v[74:77], v[146:149], v[218:221], v[74:77]
	v_mfma_f32_16x16x32_bf16 v[70:73], v[156:159], v[218:221], v[70:73]
	v_mfma_f32_16x16x32_bf16 v[66:69], v[160:163], v[218:221], v[66:69]
	s_mov_b32 m0, s49
	s_nop 0
	global_load_lds_dwordx4 v88, s[30:31]
	v_mfma_f32_16x16x32_bf16 v[62:65], v[142:145], v[222:225], v[62:65]
	v_mfma_f32_16x16x32_bf16 v[58:61], v[146:149], v[222:225], v[58:61]
	v_mfma_f32_16x16x32_bf16 v[54:57], v[156:159], v[222:225], v[54:57]
	v_mfma_f32_16x16x32_bf16 v[50:53], v[160:163], v[222:225], v[50:53]
	s_add_i32 m0, s49, 0x2000
	s_nop 0
	global_load_lds_dwordx4 v90, s[30:31]
	v_mfma_f32_16x16x32_bf16 v[46:49], v[142:145], v[226:229], v[46:49]
	v_mfma_f32_16x16x32_bf16 v[42:45], v[146:149], v[226:229], v[42:45]
	v_mfma_f32_16x16x32_bf16 v[38:41], v[156:159], v[226:229], v[38:41]
	v_mfma_f32_16x16x32_bf16 v[34:37], v[160:163], v[226:229], v[34:37]
	s_add_i32 m0, s49, 0x4000
	s_nop 0
	global_load_lds_dwordx4 v92, s[30:31]
	v_mfma_f32_16x16x32_bf16 v[18:21], v[142:145], v[230:233], v[18:21]
	v_mfma_f32_16x16x32_bf16 v[22:25], v[146:149], v[230:233], v[22:25]
	v_mfma_f32_16x16x32_bf16 v[26:29], v[156:159], v[230:233], v[26:29]
	v_mfma_f32_16x16x32_bf16 v[30:33], v[160:163], v[230:233], v[30:33]
	s_add_i32 m0, s49, 0x6000
	s_nop 0
	global_load_lds_dwordx4 v94, s[30:31]
	v_mfma_f32_16x16x32_bf16 v[2:5], v[142:145], v[234:237], v[2:5]
	v_mfma_f32_16x16x32_bf16 v[6:9], v[146:149], v[234:237], v[6:9]
	v_mfma_f32_16x16x32_bf16 v[10:13], v[156:159], v[234:237], v[10:13]
	v_mfma_f32_16x16x32_bf16 v[14:17], v[160:163], v[234:237], v[14:17]
	s_add_i32 m0, s49, 0x8000
	s_nop 0
	global_load_lds_dwordx4 v96, s[30:31]
	v_cvt_pk_bf16_f32 v172, v186, v188
	v_cvt_pk_bf16_f32 v173, v190, v192
	v_cvt_pk_bf16_f32 v174, v194, v196
	v_cvt_pk_bf16_f32 v175, v198, v200
	v_cvt_pk_bf16_f32 v176, v187, v189
	v_cvt_pk_bf16_f32 v177, v191, v193
	v_cvt_pk_bf16_f32 v178, v195, v197
	v_cvt_pk_bf16_f32 v179, v199, v201
	ds_write_b128 v95, v[172:175] offset:0
	ds_write_b128 v95, v[176:179] offset:128
	v_add_u32_e32 v91, s46, v135
	v_add_u32_e32 v93, s46, v137
	ds_read_b128 v[238:241], v139 offset:19456
	ds_read_b128 v[242:245], v139 offset:21504
	ds_read_b128 v[246:249], v139 offset:23552
	ds_read_b128 v[250:253], v139 offset:25600
	ds_read_b128 v[218:221], v91 offset:0
	ds_read_b128 v[222:225], v91 offset:2048
	ds_read_b128 v[226:229], v91 offset:4096
	ds_read_b128 v[230:233], v91 offset:6144
	ds_read_b128 v[234:237], v91 offset:8192
	s_waitcnt lgkmcnt(0)
	v_mfma_f32_16x16x32_bf16 v[78:81], v[238:241], v[218:221], v[78:81]
	v_mfma_f32_16x16x32_bf16 v[74:77], v[242:245], v[218:221], v[74:77]
	v_mfma_f32_16x16x32_bf16 v[70:73], v[246:249], v[218:221], v[70:73]
	v_mfma_f32_16x16x32_bf16 v[66:69], v[250:253], v[218:221], v[66:69]
	ds_read_b128 v[218:221], v93 offset:0
	ds_read_b128 v[142:145], v141 offset:19456
	s_add_i32 s51, s51, 1
	s_and_b32 s54, s51, 7
	s_cmp_eq_u32 s54, 0
	s_cselect_b32 s44, s34, s35
	s_cselect_b32 s45, -1, 0
	v_lshl_add_u64 v[132:133], v[132:133], 0, s[44:45]
	global_load_dwordx2 v[186:187], v[132:133], off
	v_lshl_add_u64 v[180:181], v[132:133], 0, s[24:25]
	global_load_dwordx2 v[188:189], v[180:181], off
	v_mfma_f32_16x16x32_bf16 v[62:65], v[238:241], v[222:225], v[62:65]
	v_mfma_f32_16x16x32_bf16 v[58:61], v[242:245], v[222:225], v[58:61]
	v_mfma_f32_16x16x32_bf16 v[54:57], v[246:249], v[222:225], v[54:57]
	v_mfma_f32_16x16x32_bf16 v[50:53], v[250:253], v[222:225], v[50:53]
	ds_read_b128 v[222:225], v93 offset:2048
	ds_read_b128 v[146:149], v141 offset:21504
	v_lshl_add_u64 v[180:181], v[132:133], 0, s[26:27]
	global_load_dwordx2 v[190:191], v[180:181], off
	v_lshl_add_u64 v[180:181], v[132:133], 0, s[28:29]
	global_load_dwordx2 v[192:193], v[180:181], off
	v_mfma_f32_16x16x32_bf16 v[46:49], v[238:241], v[226:229], v[46:49]
	v_mfma_f32_16x16x32_bf16 v[42:45], v[242:245], v[226:229], v[42:45]
	v_mfma_f32_16x16x32_bf16 v[38:41], v[246:249], v[226:229], v[38:41]
	v_mfma_f32_16x16x32_bf16 v[34:37], v[250:253], v[226:229], v[34:37]
	ds_read_b128 v[226:229], v93 offset:4096
	ds_read_b128 v[156:159], v141 offset:23552
	v_lshl_add_u64 v[180:181], v[132:133], 0, s[36:37]
	global_load_dwordx2 v[194:195], v[180:181], off
	v_lshl_add_u64 v[180:181], v[132:133], 0, s[38:39]
	global_load_dwordx2 v[196:197], v[180:181], off
	v_mfma_f32_16x16x32_bf16 v[18:21], v[238:241], v[230:233], v[18:21]
	v_mfma_f32_16x16x32_bf16 v[22:25], v[242:245], v[230:233], v[22:25]
	v_mfma_f32_16x16x32_bf16 v[26:29], v[246:249], v[230:233], v[26:29]
	v_mfma_f32_16x16x32_bf16 v[30:33], v[250:253], v[230:233], v[30:33]
	ds_read_b128 v[230:233], v93 offset:6144
	ds_read_b128 v[160:163], v141 offset:25600
	v_lshl_add_u64 v[180:181], v[132:133], 0, s[40:41]
	global_load_dwordx2 v[198:199], v[180:181], off
	v_lshl_add_u64 v[180:181], v[132:133], 0, s[42:43]
	global_load_dwordx2 v[200:201], v[180:181], off
	v_mfma_f32_16x16x32_bf16 v[2:5], v[238:241], v[234:237], v[2:5]
	v_mfma_f32_16x16x32_bf16 v[6:9], v[242:245], v[234:237], v[6:9]
	v_mfma_f32_16x16x32_bf16 v[10:13], v[246:249], v[234:237], v[10:13]
	v_mfma_f32_16x16x32_bf16 v[14:17], v[250:253], v[234:237], v[14:17]
	ds_read_b128 v[234:237], v93 offset:8192
	s_waitcnt vmcnt(21)
	s_waitcnt lgkmcnt(0)
	s_barrier
; #define MD_GLDS_A(buf, tau) do { _Pragma("unroll") for (int i = 0; i < 5; ++i) if (amask & (1u << i)) \
;         __builtin_amdgcn_global_load_lds((const unsigned*)((const char*)HIDp + aoff[i] + (size_t)((tau) & 7) * 128), (PG8_LAS unsigned*)(MD_SA(buf) + wid * 1024 + i * 8192), 16, 0, 0); } while (0)
; #define MD_B_ISSUE(sb, tau) do { const char* kb_ = Bb + (size_t)((tau) >> 3) * 512 + (size_t)((tau) & 7) * (64 * (size_t)RB); _Pragma("unroll") for (int j = 0; j < 8; ++j) { const char* p_ = kb_ + (size_t)j * RB; \
;         asm volatile("global_load_dwordx2 %0, %1, off" : "=&v"(sb[j]) : "v"(p_) : "memory"); } } while (0)
; #define MD_B_WAIT(sb, N) asm volatile("s_waitcnt vmcnt(%8)" : "+v"(sb[0]), "+v"(sb[1]), "+v"(sb[2]), "+v"(sb[3]), "+v"(sb[4]), "+v"(sb[5]), "+v"(sb[6]), "+v"(sb[7]) : "n"(N) : "memory")
; #define MD_END(last) do { if (last) asm volatile("s_waitcnt vmcnt(0)" ::: "memory"); else asm volatile("s_waitcnt vmcnt(8)" ::: "memory"); \
;         asm volatile("s_waitcnt lgkmcnt(0)" ::: "memory"); __builtin_amdgcn_s_barrier(); asm volatile("" ::: "memory"); } while (0)
; __device__ __forceinline__ void moe_down_stream(PG8_LAS unsigned char* lds, int e, int cb0, int slot0, int nv, const bf16_t* HIDp, const float* Wd, bf16_t* Y, const float* slot_w, const int* slot_dst) {
;     ...
;         if (t + 2 < NT) MD_B_WAIT(s1, 8); else MD_B_WAIT(s1, 0);
;         MD_B_WRITE(s1, 1); __builtin_amdgcn_sched_barrier(0); MD_GLDS_A(1, t + 1); __builtin_amdgcn_sched_barrier(0);
;         if (t + 3 < NT) MD_B_ISSUE(s1, t + 3);
;         MD_COMPUTE(0);
;         MD_END(t + 3 >= NT);
;         if (t + 2 < NT) { MD_B_WAIT(s0, 8); MD_B_WRITE(s0, 0); __builtin_amdgcn_sched_barrier(0); MD_GLDS_A(0, t + 2); __builtin_amdgcn_sched_barrier(0); }
;         if (t + 4 < NT) MD_B_ISSUE(s0, t + 4);
;         MD_COMPUTE(1);
;         MD_END(t + 4 >= NT);
	s_mov_b32 s49, s46
	s_mov_b32 s46, s47
	s_mov_b32 s47, s48
	s_mov_b32 s48, s49
	s_add_i32 s50, s50, 1
	s_add_i32 s49, s48, s74
	s_add_i32 s52, s52, 1
	s_and_b32 s54, s52, 7
	s_cmp_eq_u32 s54, 0
	s_cselect_b32 s54, s53, s32
	s_cselect_b32 s55, -1, 0
	s_add_u32 s30, s30, s54
	s_addc_u32 s31, s31, s55
	v_mfma_f32_16x16x32_bf16 v[78:81], v[142:145], v[218:221], v[78:81]
	v_mfma_f32_16x16x32_bf16 v[74:77], v[146:149], v[218:221], v[74:77]
	v_mfma_f32_16x16x32_bf16 v[70:73], v[156:159], v[218:221], v[70:73]
	v_mfma_f32_16x16x32_bf16 v[66:69], v[160:163], v[218:221], v[66:69]
	s_mov_b32 m0, s49
	s_nop 0
	global_load_lds_dwordx4 v88, s[30:31]
	v_mfma_f32_16x16x32_bf16 v[62:65], v[142:145], v[222:225], v[62:65]
	v_mfma_f32_16x16x32_bf16 v[58:61], v[146:149], v[222:225], v[58:61]
	v_mfma_f32_16x16x32_bf16 v[54:57], v[156:159], v[222:225], v[54:57]
	v_mfma_f32_16x16x32_bf16 v[50:53], v[160:163], v[222:225], v[50:53]
	s_add_i32 m0, s49, 0x2000
	s_nop 0
	global_load_lds_dwordx4 v90, s[30:31]
	v_mfma_f32_16x16x32_bf16 v[46:49], v[142:145], v[226:229], v[46:49]
	v_mfma_f32_16x16x32_bf16 v[42:45], v[146:149], v[226:229], v[42:45]
	v_mfma_f32_16x16x32_bf16 v[38:41], v[156:159], v[226:229], v[38:41]
	v_mfma_f32_16x16x32_bf16 v[34:37], v[160:163], v[226:229], v[34:37]
	s_add_i32 m0, s49, 0x4000
	s_nop 0
	global_load_lds_dwordx4 v92, s[30:31]
	v_mfma_f32_16x16x32_bf16 v[18:21], v[142:145], v[230:233], v[18:21]
	v_mfma_f32_16x16x32_bf16 v[22:25], v[146:149], v[230:233], v[22:25]
	v_mfma_f32_16x16x32_bf16 v[26:29], v[156:159], v[230:233], v[26:29]
	v_mfma_f32_16x16x32_bf16 v[30:33], v[160:163], v[230:233], v[30:33]
	s_add_i32 m0, s49, 0x6000
	s_nop 0
	global_load_lds_dwordx4 v94, s[30:31]
	v_mfma_f32_16x16x32_bf16 v[2:5], v[142:145], v[234:237], v[2:5]
	v_mfma_f32_16x16x32_bf16 v[6:9], v[146:149], v[234:237], v[6:9]
	v_mfma_f32_16x16x32_bf16 v[10:13], v[156:159], v[234:237], v[10:13]
	v_mfma_f32_16x16x32_bf16 v[14:17], v[160:163], v[234:237], v[14:17]
	s_add_i32 m0, s49, 0x8000
	s_nop 0
	global_load_lds_dwordx4 v96, s[30:31]
	v_cvt_pk_bf16_f32 v172, v202, v204
	v_cvt_pk_bf16_f32 v173, v206, v208
	v_cvt_pk_bf16_f32 v174, v210, v212
	v_cvt_pk_bf16_f32 v175, v214, v216
	v_cvt_pk_bf16_f32 v176, v203, v205
	v_cvt_pk_bf16_f32 v177, v207, v209
	v_cvt_pk_bf16_f32 v178, v211, v213
	v_cvt_pk_bf16_f32 v179, v215, v217
	ds_write_b128 v95, v[172:175] offset:19456
	ds_write_b128 v95, v[176:179] offset:19584
	v_add_u32_e32 v91, s46, v135
	v_add_u32_e32 v93, s46, v137
	ds_read_b128 v[238:241], v139 offset:0
	ds_read_b128 v[242:245], v139 offset:2048
	ds_read_b128 v[246:249], v139 offset:4096
	ds_read_b128 v[250:253], v139 offset:6144
	ds_read_b128 v[218:221], v91 offset:0
	ds_read_b128 v[222:225], v91 offset:2048
	ds_read_b128 v[226:229], v91 offset:4096
	ds_read_b128 v[230:233], v91 offset:6144
	ds_read_b128 v[234:237], v91 offset:8192
	s_waitcnt lgkmcnt(0)
	v_mfma_f32_16x16x32_bf16 v[78:81], v[238:241], v[218:221], v[78:81]
	v_mfma_f32_16x16x32_bf16 v[74:77], v[242:245], v[218:221], v[74:77]
	v_mfma_f32_16x16x32_bf16 v[70:73], v[246:249], v[218:221], v[70:73]
	v_mfma_f32_16x16x32_bf16 v[66:69], v[250:253], v[218:221], v[66:69]
	ds_read_b128 v[218:221], v93 offset:0
	ds_read_b128 v[142:145], v141 offset:0
	s_add_i32 s51, s51, 1
	s_and_b32 s54, s51, 7
	s_cmp_eq_u32 s54, 0
	s_cselect_b32 s44, s34, s35
	s_cselect_b32 s45, -1, 0
	v_lshl_add_u64 v[132:133], v[132:133], 0, s[44:45]
	global_load_dwordx2 v[202:203], v[132:133], off
	v_lshl_add_u64 v[180:181], v[132:133], 0, s[24:25]
	global_load_dwordx2 v[204:205], v[180:181], off
	v_mfma_f32_16x16x32_bf16 v[62:65], v[238:241], v[222:225], v[62:65]
	v_mfma_f32_16x16x32_bf16 v[58:61], v[242:245], v[222:225], v[58:61]
	v_mfma_f32_16x16x32_bf16 v[54:57], v[246:249], v[222:225], v[54:57]
	v_mfma_f32_16x16x32_bf16 v[50:53], v[250:253], v[222:225], v[50:53]
	ds_read_b128 v[222:225], v93 offset:2048
	ds_read_b128 v[146:149], v141 offset:2048
	v_lshl_add_u64 v[180:181], v[132:133], 0, s[26:27]
	global_load_dwordx2 v[206:207], v[180:181], off
	v_lshl_add_u64 v[180:181], v[132:133], 0, s[28:29]
	global_load_dwordx2 v[208:209], v[180:181], off
	v_mfma_f32_16x16x32_bf16 v[46:49], v[238:241], v[226:229], v[46:49]
	v_mfma_f32_16x16x32_bf16 v[42:45], v[242:245], v[226:229], v[42:45]
	v_mfma_f32_16x16x32_bf16 v[38:41], v[246:249], v[226:229], v[38:41]
	v_mfma_f32_16x16x32_bf16 v[34:37], v[250:253], v[226:229], v[34:37]
	ds_read_b128 v[226:229], v93 offset:4096
	ds_read_b128 v[156:159], v141 offset:4096
	v_lshl_add_u64 v[180:181], v[132:133], 0, s[36:37]
	global_load_dwordx2 v[210:211], v[180:181], off
	v_lshl_add_u64 v[180:181], v[132:133], 0, s[38:39]
	global_load_dwordx2 v[212:213], v[180:181], off
	v_mfma_f32_16x16x32_bf16 v[18:21], v[238:241], v[230:233], v[18:21]
	v_mfma_f32_16x16x32_bf16 v[22:25], v[242:245], v[230:233], v[22:25]
	v_mfma_f32_16x16x32_bf16 v[26:29], v[246:249], v[230:233], v[26:29]
	v_mfma_f32_16x16x32_bf16 v[30:33], v[250:253], v[230:233], v[30:33]
	ds_read_b128 v[230:233], v93 offset:6144
	ds_read_b128 v[160:163], v141 offset:6144
	v_lshl_add_u64 v[180:181], v[132:133], 0, s[40:41]
	global_load_dwordx2 v[214:215], v[180:181], off
	v_lshl_add_u64 v[180:181], v[132:133], 0, s[42:43]
	global_load_dwordx2 v[216:217], v[180:181], off
	v_mfma_f32_16x16x32_bf16 v[2:5], v[238:241], v[234:237], v[2:5]
	v_mfma_f32_16x16x32_bf16 v[6:9], v[242:245], v[234:237], v[6:9]
	v_mfma_f32_16x16x32_bf16 v[10:13], v[246:249], v[234:237], v[10:13]
	v_mfma_f32_16x16x32_bf16 v[14:17], v[250:253], v[234:237], v[14:17]
	ds_read_b128 v[234:237], v93 offset:8192
	s_waitcnt vmcnt(21)
	s_waitcnt lgkmcnt(0)
	s_barrier
; #define MD_GLDS_A(buf, tau) do { _Pragma("unroll") for (int i = 0; i < 5; ++i) if (amask & (1u << i)) \
;         __builtin_amdgcn_global_load_lds((const unsigned*)((const char*)HIDp + aoff[i] + (size_t)((tau) & 7) * 128), (PG8_LAS unsigned*)(MD_SA(buf) + wid * 1024 + i * 8192), 16, 0, 0); } while (0)
; #define MD_B_ISSUE(sb, tau) do { const char* kb_ = Bb + (size_t)((tau) >> 3) * 512 + (size_t)((tau) & 7) * (64 * (size_t)RB); _Pragma("unroll") for (int j = 0; j < 8; ++j) { const char* p_ = kb_ + (size_t)j * RB; \
;         asm volatile("global_load_dwordx2 %0, %1, off" : "=&v"(sb[j]) : "v"(p_) : "memory"); } } while (0)
; #define MD_B_WAIT(sb, N) asm volatile("s_waitcnt vmcnt(%8)" : "+v"(sb[0]), "+v"(sb[1]), "+v"(sb[2]), "+v"(sb[3]), "+v"(sb[4]), "+v"(sb[5]), "+v"(sb[6]), "+v"(sb[7]) : "n"(N) : "memory")
; #define MD_END(last) do { if (last) asm volatile("s_waitcnt vmcnt(0)" ::: "memory"); else asm volatile("s_waitcnt vmcnt(8)" ::: "memory"); \
;         asm volatile("s_waitcnt lgkmcnt(0)" ::: "memory"); __builtin_amdgcn_s_barrier(); asm volatile("" ::: "memory"); } while (0)
; __device__ __forceinline__ void moe_down_stream(PG8_LAS unsigned char* lds, int e, int cb0, int slot0, int nv, const bf16_t* HIDp, const float* Wd, bf16_t* Y, const float* slot_w, const int* slot_dst) {
;     ...
;         if (t + 2 < NT) MD_B_WAIT(s1, 8); else MD_B_WAIT(s1, 0);
;         MD_B_WRITE(s1, 1); __builtin_amdgcn_sched_barrier(0); MD_GLDS_A(1, t + 1); __builtin_amdgcn_sched_barrier(0);
;         if (t + 3 < NT) MD_B_ISSUE(s1, t + 3);
;         MD_COMPUTE(0);
;         MD_END(t + 3 >= NT);
;         if (t + 2 < NT) { MD_B_WAIT(s0, 8); MD_B_WRITE(s0, 0); __builtin_amdgcn_sched_barrier(0); MD_GLDS_A(0, t + 2); __builtin_amdgcn_sched_barrier(0); }
;         if (t + 4 < NT) MD_B_ISSUE(s0, t + 4);
;         MD_COMPUTE(1);
;         MD_END(t + 4 >= NT);
	s_mov_b32 s49, s46
	s_mov_b32 s46, s47
	s_mov_b32 s47, s48
	s_mov_b32 s48, s49
	s_add_i32 s50, s50, 1
	s_add_i32 s49, s48, s74
	s_add_i32 s52, s52, 1
	s_and_b32 s54, s52, 7
	s_cmp_eq_u32 s54, 0
	s_cselect_b32 s54, s53, s32
	s_cselect_b32 s55, -1, 0
	s_add_u32 s30, s30, s54
	s_addc_u32 s31, s31, s55
	v_mfma_f32_16x16x32_bf16 v[78:81], v[142:145], v[218:221], v[78:81]
	v_mfma_f32_16x16x32_bf16 v[74:77], v[146:149], v[218:221], v[74:77]
	v_mfma_f32_16x16x32_bf16 v[70:73], v[156:159], v[218:221], v[70:73]
	v_mfma_f32_16x16x32_bf16 v[66:69], v[160:163], v[218:221], v[66:69]
	s_mov_b32 m0, s49
	s_nop 0
	global_load_lds_dwordx4 v88, s[30:31]
	v_mfma_f32_16x16x32_bf16 v[62:65], v[142:145], v[222:225], v[62:65]
	v_mfma_f32_16x16x32_bf16 v[58:61], v[146:149], v[222:225], v[58:61]
	v_mfma_f32_16x16x32_bf16 v[54:57], v[156:159], v[222:225], v[54:57]
	v_mfma_f32_16x16x32_bf16 v[50:53], v[160:163], v[222:225], v[50:53]
	s_add_i32 m0, s49, 0x2000
	s_nop 0
	global_load_lds_dwordx4 v90, s[30:31]
	v_mfma_f32_16x16x32_bf16 v[46:49], v[142:145], v[226:229], v[46:49]
	v_mfma_f32_16x16x32_bf16 v[42:45], v[146:149], v[226:229], v[42:45]
	v_mfma_f32_16x16x32_bf16 v[38:41], v[156:159], v[226:229], v[38:41]
	v_mfma_f32_16x16x32_bf16 v[34:37], v[160:163], v[226:229], v[34:37]
	s_add_i32 m0, s49, 0x4000
	s_nop 0
	global_load_lds_dwordx4 v92, s[30:31]
	v_mfma_f32_16x16x32_bf16 v[18:21], v[142:145], v[230:233], v[18:21]
	v_mfma_f32_16x16x32_bf16 v[22:25], v[146:149], v[230:233], v[22:25]
	v_mfma_f32_16x16x32_bf16 v[26:29], v[156:159], v[230:233], v[26:29]
	v_mfma_f32_16x16x32_bf16 v[30:33], v[160:163], v[230:233], v[30:33]
	s_add_i32 m0, s49, 0x6000
	s_nop 0
	global_load_lds_dwordx4 v94, s[30:31]
	v_mfma_f32_16x16x32_bf16 v[2:5], v[142:145], v[234:237], v[2:5]
	v_mfma_f32_16x16x32_bf16 v[6:9], v[146:149], v[234:237], v[6:9]
	v_mfma_f32_16x16x32_bf16 v[10:13], v[156:159], v[234:237], v[10:13]
	v_mfma_f32_16x16x32_bf16 v[14:17], v[160:163], v[234:237], v[14:17]
	s_add_i32 m0, s49, 0x8000
	s_nop 0
	global_load_lds_dwordx4 v96, s[30:31]
	v_cvt_pk_bf16_f32 v172, v98, v100
	v_cvt_pk_bf16_f32 v173, v102, v104
	v_cvt_pk_bf16_f32 v174, v106, v108
	v_cvt_pk_bf16_f32 v175, v110, v112
	v_cvt_pk_bf16_f32 v176, v99, v101
	v_cvt_pk_bf16_f32 v177, v103, v105
	v_cvt_pk_bf16_f32 v178, v107, v109
	v_cvt_pk_bf16_f32 v179, v111, v113
	ds_write_b128 v95, v[172:175] offset:0
	ds_write_b128 v95, v[176:179] offset:128
	v_add_u32_e32 v91, s46, v135
	v_add_u32_e32 v93, s46, v137
	ds_read_b128 v[238:241], v139 offset:19456
	ds_read_b128 v[242:245], v139 offset:21504
	ds_read_b128 v[246:249], v139 offset:23552
	ds_read_b128 v[250:253], v139 offset:25600
	ds_read_b128 v[218:221], v91 offset:0
	ds_read_b128 v[222:225], v91 offset:2048
	ds_read_b128 v[226:229], v91 offset:4096
	ds_read_b128 v[230:233], v91 offset:6144
	ds_read_b128 v[234:237], v91 offset:8192
	s_waitcnt lgkmcnt(0)
	v_mfma_f32_16x16x32_bf16 v[78:81], v[238:241], v[218:221], v[78:81]
	v_mfma_f32_16x16x32_bf16 v[74:77], v[242:245], v[218:221], v[74:77]
	v_mfma_f32_16x16x32_bf16 v[70:73], v[246:249], v[218:221], v[70:73]
	v_mfma_f32_16x16x32_bf16 v[66:69], v[250:253], v[218:221], v[66:69]
	ds_read_b128 v[218:221], v93 offset:0
	ds_read_b128 v[142:145], v141 offset:19456
	v_mfma_f32_16x16x32_bf16 v[62:65], v[238:241], v[222:225], v[62:65]
	v_mfma_f32_16x16x32_bf16 v[58:61], v[242:245], v[222:225], v[58:61]
	v_mfma_f32_16x16x32_bf16 v[54:57], v[246:249], v[222:225], v[54:57]
	v_mfma_f32_16x16x32_bf16 v[50:53], v[250:253], v[222:225], v[50:53]
	ds_read_b128 v[222:225], v93 offset:2048
	ds_read_b128 v[146:149], v141 offset:21504
	v_mfma_f32_16x16x32_bf16 v[46:49], v[238:241], v[226:229], v[46:49]
	v_mfma_f32_16x16x32_bf16 v[42:45], v[242:245], v[226:229], v[42:45]
	v_mfma_f32_16x16x32_bf16 v[38:41], v[246:249], v[226:229], v[38:41]
	v_mfma_f32_16x16x32_bf16 v[34:37], v[250:253], v[226:229], v[34:37]
	ds_read_b128 v[226:229], v93 offset:4096
	ds_read_b128 v[156:159], v141 offset:23552
	v_mfma_f32_16x16x32_bf16 v[18:21], v[238:241], v[230:233], v[18:21]
	v_mfma_f32_16x16x32_bf16 v[22:25], v[242:245], v[230:233], v[22:25]
	v_mfma_f32_16x16x32_bf16 v[26:29], v[246:249], v[230:233], v[26:29]
	v_mfma_f32_16x16x32_bf16 v[30:33], v[250:253], v[230:233], v[30:33]
	ds_read_b128 v[230:233], v93 offset:6144
	ds_read_b128 v[160:163], v141 offset:25600
	v_mfma_f32_16x16x32_bf16 v[2:5], v[238:241], v[234:237], v[2:5]
	v_mfma_f32_16x16x32_bf16 v[6:9], v[242:245], v[234:237], v[6:9]
	v_mfma_f32_16x16x32_bf16 v[10:13], v[246:249], v[234:237], v[10:13]
	v_mfma_f32_16x16x32_bf16 v[14:17], v[250:253], v[234:237], v[14:17]
	ds_read_b128 v[234:237], v93 offset:8192
	s_waitcnt vmcnt(13)
	s_waitcnt lgkmcnt(0)
	s_barrier
; #define MD_GLDS_A(buf, tau) do { _Pragma("unroll") for (int i = 0; i < 5; ++i) if (amask & (1u << i)) \
;         __builtin_amdgcn_global_load_lds((const unsigned*)((const char*)HIDp + aoff[i] + (size_t)((tau) & 7) * 128), (PG8_LAS unsigned*)(MD_SA(buf) + wid * 1024 + i * 8192), 16, 0, 0); } while (0)
; #define MD_B_ISSUE(sb, tau) do { const char* kb_ = Bb + (size_t)((tau) >> 3) * 512 + (size_t)((tau) & 7) * (64 * (size_t)RB); _Pragma("unroll") for (int j = 0; j < 8; ++j) { const char* p_ = kb_ + (size_t)j * RB; \
;         asm volatile("global_load_dwordx2 %0, %1, off" : "=&v"(sb[j]) : "v"(p_) : "memory"); } } while (0)
; #define MD_B_WAIT(sb, N) asm volatile("s_waitcnt vmcnt(%8)" : "+v"(sb[0]), "+v"(sb[1]), "+v"(sb[2]), "+v"(sb[3]), "+v"(sb[4]), "+v"(sb[5]), "+v"(sb[6]), "+v"(sb[7]) : "n"(N) : "memory")
; #define MD_END(last) do { if (last) asm volatile("s_waitcnt vmcnt(0)" ::: "memory"); else asm volatile("s_waitcnt vmcnt(8)" ::: "memory"); \
;         asm volatile("s_waitcnt lgkmcnt(0)" ::: "memory"); __builtin_amdgcn_s_barrier(); asm volatile("" ::: "memory"); } while (0)
; __device__ __forceinline__ void moe_down_stream(PG8_LAS unsigned char* lds, int e, int cb0, int slot0, int nv, const bf16_t* HIDp, const float* Wd, bf16_t* Y, const float* slot_w, const int* slot_dst) {
;     ...
;         if (t + 2 < NT) MD_B_WAIT(s1, 8); else MD_B_WAIT(s1, 0);
;         MD_B_WRITE(s1, 1); __builtin_amdgcn_sched_barrier(0); MD_GLDS_A(1, t + 1); __builtin_amdgcn_sched_barrier(0);
;         if (t + 3 < NT) MD_B_ISSUE(s1, t + 3);
;         MD_COMPUTE(0);
;         MD_END(t + 3 >= NT);
;         if (t + 2 < NT) { MD_B_WAIT(s0, 8); MD_B_WRITE(s0, 0); __builtin_amdgcn_sched_barrier(0); MD_GLDS_A(0, t + 2); __builtin_amdgcn_sched_barrier(0); }
;         if (t + 4 < NT) MD_B_ISSUE(s0, t + 4);
;         MD_COMPUTE(1);
;         MD_END(t + 4 >= NT);
	s_mov_b32 s49, s46
	s_mov_b32 s46, s47
	s_mov_b32 s47, s48
	s_mov_b32 s48, s49
	s_add_i32 s50, s50, 1
	s_add_i32 s49, s48, s74
	s_add_i32 s52, s52, 1
	s_and_b32 s54, s52, 7
	s_cmp_eq_u32 s54, 0
	s_cselect_b32 s54, s53, s32
	s_cselect_b32 s55, -1, 0
	s_add_u32 s30, s30, s54
	s_addc_u32 s31, s31, s55
	v_mfma_f32_16x16x32_bf16 v[78:81], v[142:145], v[218:221], v[78:81]
	v_mfma_f32_16x16x32_bf16 v[74:77], v[146:149], v[218:221], v[74:77]
	v_mfma_f32_16x16x32_bf16 v[70:73], v[156:159], v[218:221], v[70:73]
	v_mfma_f32_16x16x32_bf16 v[66:69], v[160:163], v[218:221], v[66:69]
	s_mov_b32 m0, s49
	s_nop 0
	global_load_lds_dwordx4 v88, s[30:31]
	v_mfma_f32_16x16x32_bf16 v[62:65], v[142:145], v[222:225], v[62:65]
	v_mfma_f32_16x16x32_bf16 v[58:61], v[146:149], v[222:225], v[58:61]
	v_mfma_f32_16x16x32_bf16 v[54:57], v[156:159], v[222:225], v[54:57]
	v_mfma_f32_16x16x32_bf16 v[50:53], v[160:163], v[222:225], v[50:53]
	s_add_i32 m0, s49, 0x2000
	s_nop 0
	global_load_lds_dwordx4 v90, s[30:31]
	v_mfma_f32_16x16x32_bf16 v[46:49], v[142:145], v[226:229], v[46:49]
	v_mfma_f32_16x16x32_bf16 v[42:45], v[146:149], v[226:229], v[42:45]
	v_mfma_f32_16x16x32_bf16 v[38:41], v[156:159], v[226:229], v[38:41]
	v_mfma_f32_16x16x32_bf16 v[34:37], v[160:163], v[226:229], v[34:37]
	s_add_i32 m0, s49, 0x4000
	s_nop 0
	global_load_lds_dwordx4 v92, s[30:31]
	v_mfma_f32_16x16x32_bf16 v[18:21], v[142:145], v[230:233], v[18:21]
	v_mfma_f32_16x16x32_bf16 v[22:25], v[146:149], v[230:233], v[22:25]
	v_mfma_f32_16x16x32_bf16 v[26:29], v[156:159], v[230:233], v[26:29]
	v_mfma_f32_16x16x32_bf16 v[30:33], v[160:163], v[230:233], v[30:33]
	s_add_i32 m0, s49, 0x6000
	s_nop 0
	global_load_lds_dwordx4 v94, s[30:31]
	v_mfma_f32_16x16x32_bf16 v[2:5], v[142:145], v[234:237], v[2:5]
	v_mfma_f32_16x16x32_bf16 v[6:9], v[146:149], v[234:237], v[6:9]
	v_mfma_f32_16x16x32_bf16 v[10:13], v[156:159], v[234:237], v[10:13]
	v_mfma_f32_16x16x32_bf16 v[14:17], v[160:163], v[234:237], v[14:17]
	s_add_i32 m0, s49, 0x8000
	s_nop 0
	global_load_lds_dwordx4 v96, s[30:31]
	v_cvt_pk_bf16_f32 v172, v114, v116
	v_cvt_pk_bf16_f32 v173, v118, v120
	v_cvt_pk_bf16_f32 v174, v122, v124
	v_cvt_pk_bf16_f32 v175, v126, v128
	v_cvt_pk_bf16_f32 v176, v115, v117
	v_cvt_pk_bf16_f32 v177, v119, v121
	v_cvt_pk_bf16_f32 v178, v123, v125
	v_cvt_pk_bf16_f32 v179, v127, v129
	ds_write_b128 v95, v[172:175] offset:19456
	ds_write_b128 v95, v[176:179] offset:19584
	v_add_u32_e32 v91, s46, v135
	v_add_u32_e32 v93, s46, v137
	ds_read_b128 v[238:241], v139 offset:0
	ds_read_b128 v[242:245], v139 offset:2048
	ds_read_b128 v[246:249], v139 offset:4096
	ds_read_b128 v[250:253], v139 offset:6144
	ds_read_b128 v[218:221], v91 offset:0
	ds_read_b128 v[222:225], v91 offset:2048
	ds_read_b128 v[226:229], v91 offset:4096
	ds_read_b128 v[230:233], v91 offset:6144
	ds_read_b128 v[234:237], v91 offset:8192
	s_waitcnt lgkmcnt(0)
	v_mfma_f32_16x16x32_bf16 v[78:81], v[238:241], v[218:221], v[78:81]
	v_mfma_f32_16x16x32_bf16 v[74:77], v[242:245], v[218:221], v[74:77]
	v_mfma_f32_16x16x32_bf16 v[70:73], v[246:249], v[218:221], v[70:73]
	v_mfma_f32_16x16x32_bf16 v[66:69], v[250:253], v[218:221], v[66:69]
	ds_read_b128 v[218:221], v93 offset:0
	ds_read_b128 v[142:145], v141 offset:0
	v_mfma_f32_16x16x32_bf16 v[62:65], v[238:241], v[222:225], v[62:65]
	v_mfma_f32_16x16x32_bf16 v[58:61], v[242:245], v[222:225], v[58:61]
	v_mfma_f32_16x16x32_bf16 v[54:57], v[246:249], v[222:225], v[54:57]
	v_mfma_f32_16x16x32_bf16 v[50:53], v[250:253], v[222:225], v[50:53]
	ds_read_b128 v[222:225], v93 offset:2048
	ds_read_b128 v[146:149], v141 offset:2048
	v_mfma_f32_16x16x32_bf16 v[46:49], v[238:241], v[226:229], v[46:49]
	v_mfma_f32_16x16x32_bf16 v[42:45], v[242:245], v[226:229], v[42:45]
	v_mfma_f32_16x16x32_bf16 v[38:41], v[246:249], v[226:229], v[38:41]
	v_mfma_f32_16x16x32_bf16 v[34:37], v[250:253], v[226:229], v[34:37]
	ds_read_b128 v[226:229], v93 offset:4096
	ds_read_b128 v[156:159], v141 offset:4096
	v_mfma_f32_16x16x32_bf16 v[18:21], v[238:241], v[230:233], v[18:21]
	v_mfma_f32_16x16x32_bf16 v[22:25], v[242:245], v[230:233], v[22:25]
	v_mfma_f32_16x16x32_bf16 v[26:29], v[246:249], v[230:233], v[26:29]
	v_mfma_f32_16x16x32_bf16 v[30:33], v[250:253], v[230:233], v[30:33]
	ds_read_b128 v[230:233], v93 offset:6144
	ds_read_b128 v[160:163], v141 offset:6144
	v_mfma_f32_16x16x32_bf16 v[2:5], v[238:241], v[234:237], v[2:5]
	v_mfma_f32_16x16x32_bf16 v[6:9], v[242:245], v[234:237], v[6:9]
	v_mfma_f32_16x16x32_bf16 v[10:13], v[246:249], v[234:237], v[10:13]
	v_mfma_f32_16x16x32_bf16 v[14:17], v[250:253], v[234:237], v[14:17]
	ds_read_b128 v[234:237], v93 offset:8192
	s_waitcnt vmcnt(5)
	s_waitcnt lgkmcnt(0)
	s_barrier
; #define MD_GLDS_A(buf, tau) do { _Pragma("unroll") for (int i = 0; i < 5; ++i) if (amask & (1u << i)) \
;         __builtin_amdgcn_global_load_lds((const unsigned*)((const char*)HIDp + aoff[i] + (size_t)((tau) & 7) * 128), (PG8_LAS unsigned*)(MD_SA(buf) + wid * 1024 + i * 8192), 16, 0, 0); } while (0)
; #define MD_B_ISSUE(sb, tau) do { const char* kb_ = Bb + (size_t)((tau) >> 3) * 512 + (size_t)((tau) & 7) * (64 * (size_t)RB); _Pragma("unroll") for (int j = 0; j < 8; ++j) { const char* p_ = kb_ + (size_t)j * RB; \
;         asm volatile("global_load_dwordx2 %0, %1, off" : "=&v"(sb[j]) : "v"(p_) : "memory"); } } while (0)
; #define MD_B_WAIT(sb, N) asm volatile("s_waitcnt vmcnt(%8)" : "+v"(sb[0]), "+v"(sb[1]), "+v"(sb[2]), "+v"(sb[3]), "+v"(sb[4]), "+v"(sb[5]), "+v"(sb[6]), "+v"(sb[7]) : "n"(N) : "memory")
; #define MD_END(last) do { if (last) asm volatile("s_waitcnt vmcnt(0)" ::: "memory"); else asm volatile("s_waitcnt vmcnt(8)" ::: "memory"); \
;         asm volatile("s_waitcnt lgkmcnt(0)" ::: "memory"); __builtin_amdgcn_s_barrier(); asm volatile("" ::: "memory"); } while (0)
; __device__ __forceinline__ void moe_down_stream(PG8_LAS unsigned char* lds, int e, int cb0, int slot0, int nv, const bf16_t* HIDp, const float* Wd, bf16_t* Y, const float* slot_w, const int* slot_dst) {
;     ...
;         if (t + 2 < NT) MD_B_WAIT(s1, 8); else MD_B_WAIT(s1, 0);
;         MD_B_WRITE(s1, 1); __builtin_amdgcn_sched_barrier(0); MD_GLDS_A(1, t + 1); __builtin_amdgcn_sched_barrier(0);
;         if (t + 3 < NT) MD_B_ISSUE(s1, t + 3);
;         MD_COMPUTE(0);
;         MD_END(t + 3 >= NT);
;         if (t + 2 < NT) { MD_B_WAIT(s0, 8); MD_B_WRITE(s0, 0); __builtin_amdgcn_sched_barrier(0); MD_GLDS_A(0, t + 2); __builtin_amdgcn_sched_barrier(0); }
;         if (t + 4 < NT) MD_B_ISSUE(s0, t + 4);
;         MD_COMPUTE(1);
;         MD_END(t + 4 >= NT);
	s_mov_b32 s49, s46
	s_mov_b32 s46, s47
	s_mov_b32 s47, s48
	s_mov_b32 s48, s49
	s_add_i32 s50, s50, 1
	s_add_i32 s49, s48, s74
	s_add_i32 s52, s52, 1
	s_and_b32 s54, s52, 7
	s_cmp_eq_u32 s54, 0
	s_cselect_b32 s54, s53, s32
	s_cselect_b32 s55, -1, 0
	s_add_u32 s30, s30, s54
	s_addc_u32 s31, s31, s55
	v_mfma_f32_16x16x32_bf16 v[78:81], v[142:145], v[218:221], v[78:81]
	v_mfma_f32_16x16x32_bf16 v[74:77], v[146:149], v[218:221], v[74:77]
	v_mfma_f32_16x16x32_bf16 v[70:73], v[156:159], v[218:221], v[70:73]
	v_mfma_f32_16x16x32_bf16 v[66:69], v[160:163], v[218:221], v[66:69]
	s_mov_b32 m0, s49
	s_nop 0
	global_load_lds_dwordx4 v88, s[30:31]
	v_mfma_f32_16x16x32_bf16 v[62:65], v[142:145], v[222:225], v[62:65]
	v_mfma_f32_16x16x32_bf16 v[58:61], v[146:149], v[222:225], v[58:61]
	v_mfma_f32_16x16x32_bf16 v[54:57], v[156:159], v[222:225], v[54:57]
	v_mfma_f32_16x16x32_bf16 v[50:53], v[160:163], v[222:225], v[50:53]
	s_add_i32 m0, s49, 0x2000
	s_nop 0
	global_load_lds_dwordx4 v90, s[30:31]
	v_mfma_f32_16x16x32_bf16 v[46:49], v[142:145], v[226:229], v[46:49]
	v_mfma_f32_16x16x32_bf16 v[42:45], v[146:149], v[226:229], v[42:45]
	v_mfma_f32_16x16x32_bf16 v[38:41], v[156:159], v[226:229], v[38:41]
	v_mfma_f32_16x16x32_bf16 v[34:37], v[160:163], v[226:229], v[34:37]
	s_add_i32 m0, s49, 0x4000
	s_nop 0
	global_load_lds_dwordx4 v92, s[30:31]
	v_mfma_f32_16x16x32_bf16 v[18:21], v[142:145], v[230:233], v[18:21]
	v_mfma_f32_16x16x32_bf16 v[22:25], v[146:149], v[230:233], v[22:25]
	v_mfma_f32_16x16x32_bf16 v[26:29], v[156:159], v[230:233], v[26:29]
	v_mfma_f32_16x16x32_bf16 v[30:33], v[160:163], v[230:233], v[30:33]
	s_add_i32 m0, s49, 0x6000
	s_nop 0
	global_load_lds_dwordx4 v94, s[30:31]
	v_mfma_f32_16x16x32_bf16 v[2:5], v[142:145], v[234:237], v[2:5]
	v_mfma_f32_16x16x32_bf16 v[6:9], v[146:149], v[234:237], v[6:9]
	v_mfma_f32_16x16x32_bf16 v[10:13], v[156:159], v[234:237], v[10:13]
	v_mfma_f32_16x16x32_bf16 v[14:17], v[160:163], v[234:237], v[14:17]
	s_add_i32 m0, s49, 0x8000
	s_nop 0
	global_load_lds_dwordx4 v96, s[30:31]
	v_cvt_pk_bf16_f32 v172, v186, v188
	v_cvt_pk_bf16_f32 v173, v190, v192
	v_cvt_pk_bf16_f32 v174, v194, v196
	v_cvt_pk_bf16_f32 v175, v198, v200
	v_cvt_pk_bf16_f32 v176, v187, v189
	v_cvt_pk_bf16_f32 v177, v191, v193
	v_cvt_pk_bf16_f32 v178, v195, v197
	v_cvt_pk_bf16_f32 v179, v199, v201
	ds_write_b128 v95, v[172:175] offset:0
	ds_write_b128 v95, v[176:179] offset:128
	v_add_u32_e32 v91, s46, v135
	v_add_u32_e32 v93, s46, v137
	ds_read_b128 v[238:241], v139 offset:19456
	ds_read_b128 v[242:245], v139 offset:21504
	ds_read_b128 v[246:249], v139 offset:23552
	ds_read_b128 v[250:253], v139 offset:25600
	ds_read_b128 v[218:221], v91 offset:0
	ds_read_b128 v[222:225], v91 offset:2048
	ds_read_b128 v[226:229], v91 offset:4096
	ds_read_b128 v[230:233], v91 offset:6144
	ds_read_b128 v[234:237], v91 offset:8192
	s_waitcnt lgkmcnt(0)
	v_mfma_f32_16x16x32_bf16 v[78:81], v[238:241], v[218:221], v[78:81]
	v_mfma_f32_16x16x32_bf16 v[74:77], v[242:245], v[218:221], v[74:77]
	v_mfma_f32_16x16x32_bf16 v[70:73], v[246:249], v[218:221], v[70:73]
	v_mfma_f32_16x16x32_bf16 v[66:69], v[250:253], v[218:221], v[66:69]
	ds_read_b128 v[218:221], v93 offset:0
	ds_read_b128 v[142:145], v141 offset:19456
	v_mfma_f32_16x16x32_bf16 v[62:65], v[238:241], v[222:225], v[62:65]
	v_mfma_f32_16x16x32_bf16 v[58:61], v[242:245], v[222:225], v[58:61]
	v_mfma_f32_16x16x32_bf16 v[54:57], v[246:249], v[222:225], v[54:57]
	v_mfma_f32_16x16x32_bf16 v[50:53], v[250:253], v[222:225], v[50:53]
	ds_read_b128 v[222:225], v93 offset:2048
	ds_read_b128 v[146:149], v141 offset:21504
	v_mfma_f32_16x16x32_bf16 v[46:49], v[238:241], v[226:229], v[46:49]
	v_mfma_f32_16x16x32_bf16 v[42:45], v[242:245], v[226:229], v[42:45]
	v_mfma_f32_16x16x32_bf16 v[38:41], v[246:249], v[226:229], v[38:41]
	v_mfma_f32_16x16x32_bf16 v[34:37], v[250:253], v[226:229], v[34:37]
	ds_read_b128 v[226:229], v93 offset:4096
	ds_read_b128 v[156:159], v141 offset:23552
	v_mfma_f32_16x16x32_bf16 v[18:21], v[238:241], v[230:233], v[18:21]
	v_mfma_f32_16x16x32_bf16 v[22:25], v[242:245], v[230:233], v[22:25]
	v_mfma_f32_16x16x32_bf16 v[26:29], v[246:249], v[230:233], v[26:29]
	v_mfma_f32_16x16x32_bf16 v[30:33], v[250:253], v[230:233], v[30:33]
	ds_read_b128 v[230:233], v93 offset:6144
	ds_read_b128 v[160:163], v141 offset:25600
	v_mfma_f32_16x16x32_bf16 v[2:5], v[238:241], v[234:237], v[2:5]
	v_mfma_f32_16x16x32_bf16 v[6:9], v[242:245], v[234:237], v[6:9]
	v_mfma_f32_16x16x32_bf16 v[10:13], v[246:249], v[234:237], v[10:13]
	v_mfma_f32_16x16x32_bf16 v[14:17], v[250:253], v[234:237], v[14:17]
	ds_read_b128 v[234:237], v93 offset:8192
	s_waitcnt vmcnt(5)
	s_waitcnt lgkmcnt(0)
	s_barrier
; #define MD_GLDS_A(buf, tau) do { _Pragma("unroll") for (int i = 0; i < 5; ++i) if (amask & (1u << i)) \
;         __builtin_amdgcn_global_load_lds((const unsigned*)((const char*)HIDp + aoff[i] + (size_t)((tau) & 7) * 128), (PG8_LAS unsigned*)(MD_SA(buf) + wid * 1024 + i * 8192), 16, 0, 0); } while (0)
; #define MD_B_ISSUE(sb, tau) do { const char* kb_ = Bb + (size_t)((tau) >> 3) * 512 + (size_t)((tau) & 7) * (64 * (size_t)RB); _Pragma("unroll") for (int j = 0; j < 8; ++j) { const char* p_ = kb_ + (size_t)j * RB; \
;         asm volatile("global_load_dwordx2 %0, %1, off" : "=&v"(sb[j]) : "v"(p_) : "memory"); } } while (0)
; #define MD_B_WAIT(sb, N) asm volatile("s_waitcnt vmcnt(%8)" : "+v"(sb[0]), "+v"(sb[1]), "+v"(sb[2]), "+v"(sb[3]), "+v"(sb[4]), "+v"(sb[5]), "+v"(sb[6]), "+v"(sb[7]) : "n"(N) : "memory")
; #define MD_END(last) do { if (last) asm volatile("s_waitcnt vmcnt(0)" ::: "memory"); else asm volatile("s_waitcnt vmcnt(8)" ::: "memory"); \
;         asm volatile("s_waitcnt lgkmcnt(0)" ::: "memory"); __builtin_amdgcn_s_barrier(); asm volatile("" ::: "memory"); } while (0)
; __device__ __forceinline__ void moe_down_stream(PG8_LAS unsigned char* lds, int e, int cb0, int slot0, int nv, const bf16_t* HIDp, const float* Wd, bf16_t* Y, const float* slot_w, const int* slot_dst) {
;     ...
;         if (t + 2 < NT) MD_B_WAIT(s1, 8); else MD_B_WAIT(s1, 0);
;         MD_B_WRITE(s1, 1); __builtin_amdgcn_sched_barrier(0); MD_GLDS_A(1, t + 1); __builtin_amdgcn_sched_barrier(0);
;         if (t + 3 < NT) MD_B_ISSUE(s1, t + 3);
;         MD_COMPUTE(0);
;         MD_END(t + 3 >= NT);
;         if (t + 2 < NT) { MD_B_WAIT(s0, 8); MD_B_WRITE(s0, 0); __builtin_amdgcn_sched_barrier(0); MD_GLDS_A(0, t + 2); __builtin_amdgcn_sched_barrier(0); }
;         if (t + 4 < NT) MD_B_ISSUE(s0, t + 4);
;         MD_COMPUTE(1);
;         MD_END(t + 4 >= NT);
	s_mov_b32 s49, s46
	s_mov_b32 s46, s47
	s_mov_b32 s47, s48
	s_mov_b32 s48, s49
	s_add_i32 s50, s50, 1
	v_mfma_f32_16x16x32_bf16 v[78:81], v[142:145], v[218:221], v[78:81]
	v_mfma_f32_16x16x32_bf16 v[74:77], v[146:149], v[218:221], v[74:77]
	v_mfma_f32_16x16x32_bf16 v[70:73], v[156:159], v[218:221], v[70:73]
	v_mfma_f32_16x16x32_bf16 v[66:69], v[160:163], v[218:221], v[66:69]
	v_mfma_f32_16x16x32_bf16 v[62:65], v[142:145], v[222:225], v[62:65]
	v_mfma_f32_16x16x32_bf16 v[58:61], v[146:149], v[222:225], v[58:61]
	v_mfma_f32_16x16x32_bf16 v[54:57], v[156:159], v[222:225], v[54:57]
	v_mfma_f32_16x16x32_bf16 v[50:53], v[160:163], v[222:225], v[50:53]
	v_mfma_f32_16x16x32_bf16 v[46:49], v[142:145], v[226:229], v[46:49]
	v_mfma_f32_16x16x32_bf16 v[42:45], v[146:149], v[226:229], v[42:45]
	v_mfma_f32_16x16x32_bf16 v[38:41], v[156:159], v[226:229], v[38:41]
	v_mfma_f32_16x16x32_bf16 v[34:37], v[160:163], v[226:229], v[34:37]
	v_mfma_f32_16x16x32_bf16 v[18:21], v[142:145], v[230:233], v[18:21]
	v_mfma_f32_16x16x32_bf16 v[22:25], v[146:149], v[230:233], v[22:25]
	v_mfma_f32_16x16x32_bf16 v[26:29], v[156:159], v[230:233], v[26:29]
	v_mfma_f32_16x16x32_bf16 v[30:33], v[160:163], v[230:233], v[30:33]
	v_mfma_f32_16x16x32_bf16 v[2:5], v[142:145], v[234:237], v[2:5]
	v_mfma_f32_16x16x32_bf16 v[6:9], v[146:149], v[234:237], v[6:9]
	v_mfma_f32_16x16x32_bf16 v[10:13], v[156:159], v[234:237], v[10:13]
	v_mfma_f32_16x16x32_bf16 v[14:17], v[160:163], v[234:237], v[14:17]
	v_cvt_pk_bf16_f32 v172, v202, v204
	v_cvt_pk_bf16_f32 v173, v206, v208
	v_cvt_pk_bf16_f32 v174, v210, v212
	v_cvt_pk_bf16_f32 v175, v214, v216
	v_cvt_pk_bf16_f32 v176, v203, v205
	v_cvt_pk_bf16_f32 v177, v207, v209
	v_cvt_pk_bf16_f32 v178, v211, v213
	v_cvt_pk_bf16_f32 v179, v215, v217
	ds_write_b128 v95, v[172:175] offset:19456
	ds_write_b128 v95, v[176:179] offset:19584
	v_add_u32_e32 v91, s46, v135
	v_add_u32_e32 v93, s46, v137
	ds_read_b128 v[238:241], v139 offset:0
	ds_read_b128 v[242:245], v139 offset:2048
	ds_read_b128 v[246:249], v139 offset:4096
	ds_read_b128 v[250:253], v139 offset:6144
	ds_read_b128 v[218:221], v91 offset:0
	ds_read_b128 v[222:225], v91 offset:2048
	ds_read_b128 v[226:229], v91 offset:4096
	ds_read_b128 v[230:233], v91 offset:6144
	ds_read_b128 v[234:237], v91 offset:8192
	s_waitcnt lgkmcnt(0)
	v_mfma_f32_16x16x32_bf16 v[78:81], v[238:241], v[218:221], v[78:81]
	v_mfma_f32_16x16x32_bf16 v[74:77], v[242:245], v[218:221], v[74:77]
	v_mfma_f32_16x16x32_bf16 v[70:73], v[246:249], v[218:221], v[70:73]
	v_mfma_f32_16x16x32_bf16 v[66:69], v[250:253], v[218:221], v[66:69]
	ds_read_b128 v[218:221], v93 offset:0
	ds_read_b128 v[142:145], v141 offset:0
	v_mfma_f32_16x16x32_bf16 v[62:65], v[238:241], v[222:225], v[62:65]
	v_mfma_f32_16x16x32_bf16 v[58:61], v[242:245], v[222:225], v[58:61]
	v_mfma_f32_16x16x32_bf16 v[54:57], v[246:249], v[222:225], v[54:57]
	v_mfma_f32_16x16x32_bf16 v[50:53], v[250:253], v[222:225], v[50:53]
	ds_read_b128 v[222:225], v93 offset:2048
	ds_read_b128 v[146:149], v141 offset:2048
	v_mfma_f32_16x16x32_bf16 v[46:49], v[238:241], v[226:229], v[46:49]
	v_mfma_f32_16x16x32_bf16 v[42:45], v[242:245], v[226:229], v[42:45]
	v_mfma_f32_16x16x32_bf16 v[38:41], v[246:249], v[226:229], v[38:41]
	v_mfma_f32_16x16x32_bf16 v[34:37], v[250:253], v[226:229], v[34:37]
	ds_read_b128 v[226:229], v93 offset:4096
	ds_read_b128 v[156:159], v141 offset:4096
	v_mfma_f32_16x16x32_bf16 v[18:21], v[238:241], v[230:233], v[18:21]
	v_mfma_f32_16x16x32_bf16 v[22:25], v[242:245], v[230:233], v[22:25]
	v_mfma_f32_16x16x32_bf16 v[26:29], v[246:249], v[230:233], v[26:29]
	v_mfma_f32_16x16x32_bf16 v[30:33], v[250:253], v[230:233], v[30:33]
	ds_read_b128 v[230:233], v93 offset:6144
	ds_read_b128 v[160:163], v141 offset:6144
	v_mfma_f32_16x16x32_bf16 v[2:5], v[238:241], v[234:237], v[2:5]
	v_mfma_f32_16x16x32_bf16 v[6:9], v[242:245], v[234:237], v[6:9]
	v_mfma_f32_16x16x32_bf16 v[10:13], v[246:249], v[234:237], v[10:13]
	v_mfma_f32_16x16x32_bf16 v[14:17], v[250:253], v[234:237], v[14:17]
	ds_read_b128 v[234:237], v93 offset:8192
	s_waitcnt vmcnt(0)
	s_waitcnt lgkmcnt(0)
	s_barrier
	s_mov_b32 s49, s46
	s_mov_b32 s46, s47
	s_mov_b32 s47, s48
	s_mov_b32 s48, s49
	s_add_i32 s50, s50, 1
	v_mfma_f32_16x16x32_bf16 v[78:81], v[142:145], v[218:221], v[78:81]
	v_mfma_f32_16x16x32_bf16 v[74:77], v[146:149], v[218:221], v[74:77]
	v_mfma_f32_16x16x32_bf16 v[70:73], v[156:159], v[218:221], v[70:73]
	v_mfma_f32_16x16x32_bf16 v[66:69], v[160:163], v[218:221], v[66:69]
	v_mfma_f32_16x16x32_bf16 v[62:65], v[142:145], v[222:225], v[62:65]
	v_mfma_f32_16x16x32_bf16 v[58:61], v[146:149], v[222:225], v[58:61]
	v_mfma_f32_16x16x32_bf16 v[54:57], v[156:159], v[222:225], v[54:57]
	v_mfma_f32_16x16x32_bf16 v[50:53], v[160:163], v[222:225], v[50:53]
	v_mfma_f32_16x16x32_bf16 v[46:49], v[142:145], v[226:229], v[46:49]
	v_mfma_f32_16x16x32_bf16 v[42:45], v[146:149], v[226:229], v[42:45]
	v_mfma_f32_16x16x32_bf16 v[38:41], v[156:159], v[226:229], v[38:41]
	v_mfma_f32_16x16x32_bf16 v[34:37], v[160:163], v[226:229], v[34:37]
	v_mfma_f32_16x16x32_bf16 v[18:21], v[142:145], v[230:233], v[18:21]
	v_mfma_f32_16x16x32_bf16 v[22:25], v[146:149], v[230:233], v[22:25]
	v_mfma_f32_16x16x32_bf16 v[26:29], v[156:159], v[230:233], v[26:29]
	v_mfma_f32_16x16x32_bf16 v[30:33], v[160:163], v[230:233], v[30:33]
	v_mfma_f32_16x16x32_bf16 v[2:5], v[142:145], v[234:237], v[2:5]
	v_mfma_f32_16x16x32_bf16 v[6:9], v[146:149], v[234:237], v[6:9]
	v_mfma_f32_16x16x32_bf16 v[10:13], v[156:159], v[234:237], v[10:13]
	v_mfma_f32_16x16x32_bf16 v[14:17], v[160:163], v[234:237], v[14:17]
	v_add_u32_e32 v91, s46, v135
	v_add_u32_e32 v93, s46, v137
	ds_read_b128 v[238:241], v139 offset:19456
	ds_read_b128 v[242:245], v139 offset:21504
	ds_read_b128 v[246:249], v139 offset:23552
	ds_read_b128 v[250:253], v139 offset:25600
	ds_read_b128 v[218:221], v91 offset:0
	ds_read_b128 v[222:225], v91 offset:2048
	ds_read_b128 v[226:229], v91 offset:4096
	ds_read_b128 v[230:233], v91 offset:6144
	ds_read_b128 v[234:237], v91 offset:8192
	s_waitcnt lgkmcnt(0)
; #define PG8_LAS __attribute__((address_space(3)))
; __device__ __forceinline__ unsigned cvtpk(float lo, float hi) { f32x2 v = {lo, hi}; bf16x2_t b = __builtin_convertvector(v, bf16x2_t); return __builtin_bit_cast(unsigned, b); }
; #define MD_GLDS_A(buf, tau) do { _Pragma("unroll") for (int i = 0; i < 5; ++i) if (amask & (1u << i)) \
;         __builtin_amdgcn_global_load_lds((const unsigned*)((const char*)HIDp + aoff[i] + (size_t)((tau) & 7) * 128), (PG8_LAS unsigned*)(MD_SA(buf) + wid * 1024 + i * 8192), 16, 0, 0); } while (0)
; #define MD_B_ISSUE(sb, tau) do { const char* kb_ = Bb + (size_t)((tau) >> 3) * 512 + (size_t)((tau) & 7) * (64 * (size_t)RB); _Pragma("unroll") for (int j = 0; j < 8; ++j) { const char* p_ = kb_ + (size_t)j * RB; \
;         asm volatile("global_load_dwordx2 %0, %1, off" : "=&v"(sb[j]) : "v"(p_) : "memory"); } } while (0)
; __device__ __forceinline__ void moe_down_stream(PG8_LAS unsigned char* lds, int e, int cb0, int slot0, int nv, const bf16_t* HIDp, const float* Wd, bf16_t* Y, const float* slot_w, const int* slot_dst) {
;     ...
;         MD_END(t + 3 >= NT);
;         if (t + 2 < NT) { MD_B_WAIT(s0, 8); MD_B_WRITE(s0, 0); __builtin_amdgcn_sched_barrier(0); MD_GLDS_A(0, t + 2); __builtin_amdgcn_sched_barrier(0); }
;         if (t + 4 < NT) MD_B_ISSUE(s0, t + 4);
;         MD_COMPUTE(1);
;         MD_END(t + 4 >= NT);
;         if (((t + 1) & 7) == 7) {
;             const int cb = cb0 + ((t + 1) >> 3);
; #pragma unroll
;             for (int m = 0; m < DNM; ++m) {
;                 const float w_ = lw[4 * (16 * m + fr) + wr];
; #pragma unroll
;                 for (int p = 0; p < 2; ++p) { const f32x4 v0 = acc[m][2 * p] * w_, v1 = acc[m][2 * p + 1] * w_; u32x4 w; w.x = cvtpk(v0[0], v0[1]); w.y = cvtpk(v0[2], v0[3]); w.z = cvtpk(v1[0], v1[1]); w.w = cvtpk(v1[2], v1[3]);
;                     *(PG8_LAS u32x4*)(stg + fr * 128 + (((4 * p + fq) ^ (fr & 7)) * 16)) = w; }
; #pragma unroll
;                 for (int hh = 0; hh < 2; ++hh) { const int r = (lane >> 3) + 8 * hh, cc = lane & 7; const u32x4 d = *(const PG8_LAS u32x4*)(stg + r * 128 + ((cc ^ (r & 7)) * 16)); const int dst_ = ldst[4 * (16 * m + r) + wr];
;                     if (dst_ >= 0) *(u32x4*)(Y + (size_t)dst_ * D + 128 * cb + 64 * wc + 8 * cc) = d; }
; #pragma unroll
;                 for (int n = 0; n < 4; ++n) acc[m][n] = (f32x4){0.f, 0.f, 0.f, 0.f}; } }
	v_mfma_f32_16x16x32_bf16 v[78:81], v[238:241], v[218:221], v[78:81]
	v_mfma_f32_16x16x32_bf16 v[74:77], v[242:245], v[218:221], v[74:77]
	v_mfma_f32_16x16x32_bf16 v[70:73], v[246:249], v[218:221], v[70:73]
	v_mfma_f32_16x16x32_bf16 v[66:69], v[250:253], v[218:221], v[66:69]
	ds_read_b128 v[218:221], v93 offset:0
	ds_read_b128 v[142:145], v141 offset:19456
	v_mfma_f32_16x16x32_bf16 v[62:65], v[238:241], v[222:225], v[62:65]
	v_mfma_f32_16x16x32_bf16 v[58:61], v[242:245], v[222:225], v[58:61]
	v_mfma_f32_16x16x32_bf16 v[54:57], v[246:249], v[222:225], v[54:57]
	v_mfma_f32_16x16x32_bf16 v[50:53], v[250:253], v[222:225], v[50:53]
	ds_read_b128 v[222:225], v93 offset:2048
	ds_read_b128 v[146:149], v141 offset:21504
	v_mfma_f32_16x16x32_bf16 v[46:49], v[238:241], v[226:229], v[46:49]
	v_mfma_f32_16x16x32_bf16 v[42:45], v[242:245], v[226:229], v[42:45]
	v_mfma_f32_16x16x32_bf16 v[38:41], v[246:249], v[226:229], v[38:41]
	v_mfma_f32_16x16x32_bf16 v[34:37], v[250:253], v[226:229], v[34:37]
	ds_read_b128 v[226:229], v93 offset:4096
	ds_read_b128 v[156:159], v141 offset:23552
	v_mfma_f32_16x16x32_bf16 v[18:21], v[238:241], v[230:233], v[18:21]
	v_mfma_f32_16x16x32_bf16 v[22:25], v[242:245], v[230:233], v[22:25]
	v_mfma_f32_16x16x32_bf16 v[26:29], v[246:249], v[230:233], v[26:29]
	v_mfma_f32_16x16x32_bf16 v[30:33], v[250:253], v[230:233], v[30:33]
	ds_read_b128 v[230:233], v93 offset:6144
	ds_read_b128 v[160:163], v141 offset:25600
	v_mfma_f32_16x16x32_bf16 v[2:5], v[238:241], v[234:237], v[2:5]
	v_mfma_f32_16x16x32_bf16 v[6:9], v[242:245], v[234:237], v[6:9]
	v_mfma_f32_16x16x32_bf16 v[10:13], v[246:249], v[234:237], v[10:13]
	v_mfma_f32_16x16x32_bf16 v[14:17], v[250:253], v[234:237], v[14:17]
	ds_read_b128 v[234:237], v93 offset:8192
	s_waitcnt lgkmcnt(0)
	s_barrier
	s_mov_b32 s49, s46
	s_mov_b32 s46, s47
	s_mov_b32 s47, s48
	s_mov_b32 s48, s49
	s_add_i32 s50, s50, 1
	v_mfma_f32_16x16x32_bf16 v[78:81], v[142:145], v[218:221], v[78:81]
	v_mfma_f32_16x16x32_bf16 v[74:77], v[146:149], v[218:221], v[74:77]
	v_mfma_f32_16x16x32_bf16 v[70:73], v[156:159], v[218:221], v[70:73]
	v_mfma_f32_16x16x32_bf16 v[66:69], v[160:163], v[218:221], v[66:69]
	v_mfma_f32_16x16x32_bf16 v[62:65], v[142:145], v[222:225], v[62:65]
	v_mfma_f32_16x16x32_bf16 v[58:61], v[146:149], v[222:225], v[58:61]
	v_mfma_f32_16x16x32_bf16 v[54:57], v[156:159], v[222:225], v[54:57]
	v_mfma_f32_16x16x32_bf16 v[50:53], v[160:163], v[222:225], v[50:53]
	v_mfma_f32_16x16x32_bf16 v[46:49], v[142:145], v[226:229], v[46:49]
	v_mfma_f32_16x16x32_bf16 v[42:45], v[146:149], v[226:229], v[42:45]
	v_mfma_f32_16x16x32_bf16 v[38:41], v[156:159], v[226:229], v[38:41]
	v_mfma_f32_16x16x32_bf16 v[34:37], v[160:163], v[226:229], v[34:37]
	v_mfma_f32_16x16x32_bf16 v[18:21], v[142:145], v[230:233], v[18:21]
	v_mfma_f32_16x16x32_bf16 v[22:25], v[146:149], v[230:233], v[22:25]
	v_mfma_f32_16x16x32_bf16 v[26:29], v[156:159], v[230:233], v[26:29]
	v_mfma_f32_16x16x32_bf16 v[30:33], v[160:163], v[230:233], v[30:33]
	v_mfma_f32_16x16x32_bf16 v[2:5], v[142:145], v[234:237], v[2:5]
	v_mfma_f32_16x16x32_bf16 v[6:9], v[146:149], v[234:237], v[6:9]
	v_mfma_f32_16x16x32_bf16 v[10:13], v[156:159], v[234:237], v[10:13]
	v_mfma_f32_16x16x32_bf16 v[14:17], v[160:163], v[234:237], v[14:17]
	s_add_i32 s54, s48, s74
	v_add_u32_e32 v164, s54, v84
	v_add_u32_e32 v165, s54, v85
	ds_read_b32 v150, v82 offset:0
	ds_read_b32 v151, v83 offset:0
	ds_read_b32 v166, v83 offset:128
	s_waitcnt lgkmcnt(2)
	v_mul_f32_e32 v78, v150, v78
	v_mul_f32_e32 v79, v150, v79
	v_mul_f32_e32 v80, v150, v80
	v_mul_f32_e32 v81, v150, v81
	v_mul_f32_e32 v74, v150, v74
	v_mul_f32_e32 v75, v150, v75
	v_mul_f32_e32 v76, v150, v76
	v_mul_f32_e32 v77, v150, v77
	v_cvt_pk_bf16_f32 v182, v78, v79
	v_cvt_pk_bf16_f32 v183, v80, v81
	v_cvt_pk_bf16_f32 v184, v74, v75
	v_cvt_pk_bf16_f32 v185, v76, v77
	ds_write_b128 v164, v[182:185]
	v_mul_f32_e32 v70, v150, v70
	v_mul_f32_e32 v71, v150, v71
	v_mul_f32_e32 v72, v150, v72
	v_mul_f32_e32 v73, v150, v73
	v_mul_f32_e32 v66, v150, v66
	v_mul_f32_e32 v67, v150, v67
	v_mul_f32_e32 v68, v150, v68
	v_mul_f32_e32 v69, v150, v69
	v_cvt_pk_bf16_f32 v182, v70, v71
	v_cvt_pk_bf16_f32 v183, v72, v73
	v_cvt_pk_bf16_f32 v184, v66, v67
	v_cvt_pk_bf16_f32 v185, v68, v69
	v_xor_b32_e32 v167, 64, v164
	ds_write_b128 v167, v[182:185]
	v_mov_b32_e32 v78, 0
	v_mov_b32_e32 v74, 0
	v_mov_b32_e32 v70, 0
	v_mov_b32_e32 v66, 0
	v_mov_b32_e32 v79, 0
	v_mov_b32_e32 v75, 0
	v_mov_b32_e32 v71, 0
	v_mov_b32_e32 v67, 0
	v_mov_b32_e32 v80, 0
	v_mov_b32_e32 v76, 0
	v_mov_b32_e32 v72, 0
	v_mov_b32_e32 v68, 0
	v_mov_b32_e32 v81, 0
	v_mov_b32_e32 v77, 0
	v_mov_b32_e32 v73, 0
	v_mov_b32_e32 v69, 0
	ds_read_b128 v[182:185], v165 offset:0
	v_cmp_lt_i32_e32 vcc, -1, v151
	v_lshlrev_b32_e32 v148, 13, v151
	v_mov_b32_e32 v149, 0
	v_lshl_add_u64 v[148:149], v[148:149], 0, v[86:87]
	v_cndmask_b32_e32 v148, v168, v148, vcc
	v_cndmask_b32_e32 v149, v169, v149, vcc
	s_waitcnt lgkmcnt(0)
	global_store_dwordx4 v[148:149], v[182:185], off nt
	ds_read_b128 v[182:185], v165 offset:8192
	v_cmp_lt_i32_e32 vcc, -1, v166
	v_lshlrev_b32_e32 v148, 13, v166
	v_mov_b32_e32 v149, 0
	v_lshl_add_u64 v[148:149], v[148:149], 0, v[86:87]
	v_cndmask_b32_e32 v148, v168, v148, vcc
	v_cndmask_b32_e32 v149, v169, v149, vcc
	s_waitcnt lgkmcnt(0)
	global_store_dwordx4 v[148:149], v[182:185], off nt
	ds_read_b32 v150, v82 offset:256
	ds_read_b32 v151, v83 offset:256
	ds_read_b32 v166, v83 offset:384
	s_waitcnt lgkmcnt(2)
; #define PG8_LAS __attribute__((address_space(3)))
; __device__ __forceinline__ unsigned cvtpk(float lo, float hi) { f32x2 v = {lo, hi}; bf16x2_t b = __builtin_convertvector(v, bf16x2_t); return __builtin_bit_cast(unsigned, b); }
; __device__ __forceinline__ void moe_down_stream(PG8_LAS unsigned char* lds, int e, int cb0, int slot0, int nv, const bf16_t* HIDp, const float* Wd, bf16_t* Y, const float* slot_w, const int* slot_dst) {
;     ...
;         if (((t + 1) & 7) == 7) {
;             const int cb = cb0 + ((t + 1) >> 3);
; #pragma unroll
;             for (int m = 0; m < DNM; ++m) {
;                 const float w_ = lw[4 * (16 * m + fr) + wr];
; #pragma unroll
;                 for (int p = 0; p < 2; ++p) { const f32x4 v0 = acc[m][2 * p] * w_, v1 = acc[m][2 * p + 1] * w_; u32x4 w; w.x = cvtpk(v0[0], v0[1]); w.y = cvtpk(v0[2], v0[3]); w.z = cvtpk(v1[0], v1[1]); w.w = cvtpk(v1[2], v1[3]);
;                     *(PG8_LAS u32x4*)(stg + fr * 128 + (((4 * p + fq) ^ (fr & 7)) * 16)) = w; }
; #pragma unroll
;                 for (int hh = 0; hh < 2; ++hh) { const int r = (lane >> 3) + 8 * hh, cc = lane & 7; const u32x4 d = *(const PG8_LAS u32x4*)(stg + r * 128 + ((cc ^ (r & 7)) * 16)); const int dst_ = ldst[4 * (16 * m + r) + wr];
;                     if (dst_ >= 0) *(u32x4*)(Y + (size_t)dst_ * D + 128 * cb + 64 * wc + 8 * cc) = d; }
; #pragma unroll
;                 for (int n = 0; n < 4; ++n) acc[m][n] = (f32x4){0.f, 0.f, 0.f, 0.f}; } }
	v_mul_f32_e32 v62, v150, v62
	v_mul_f32_e32 v63, v150, v63
	v_mul_f32_e32 v64, v150, v64
	v_mul_f32_e32 v65, v150, v65
	v_mul_f32_e32 v58, v150, v58
	v_mul_f32_e32 v59, v150, v59
	v_mul_f32_e32 v60, v150, v60
	v_mul_f32_e32 v61, v150, v61
	v_cvt_pk_bf16_f32 v182, v62, v63
	v_cvt_pk_bf16_f32 v183, v64, v65
	v_cvt_pk_bf16_f32 v184, v58, v59
	v_cvt_pk_bf16_f32 v185, v60, v61
	ds_write_b128 v164, v[182:185]
	v_mul_f32_e32 v54, v150, v54
	v_mul_f32_e32 v55, v150, v55
	v_mul_f32_e32 v56, v150, v56
	v_mul_f32_e32 v57, v150, v57
	v_mul_f32_e32 v50, v150, v50
	v_mul_f32_e32 v51, v150, v51
	v_mul_f32_e32 v52, v150, v52
	v_mul_f32_e32 v53, v150, v53
	v_cvt_pk_bf16_f32 v182, v54, v55
	v_cvt_pk_bf16_f32 v183, v56, v57
	v_cvt_pk_bf16_f32 v184, v50, v51
	v_cvt_pk_bf16_f32 v185, v52, v53
	v_xor_b32_e32 v167, 64, v164
	ds_write_b128 v167, v[182:185]
	v_mov_b32_e32 v62, 0
	v_mov_b32_e32 v58, 0
	v_mov_b32_e32 v54, 0
	v_mov_b32_e32 v50, 0
	v_mov_b32_e32 v63, 0
	v_mov_b32_e32 v59, 0
	v_mov_b32_e32 v55, 0
	v_mov_b32_e32 v51, 0
	v_mov_b32_e32 v64, 0
	v_mov_b32_e32 v60, 0
	v_mov_b32_e32 v56, 0
	v_mov_b32_e32 v52, 0
	v_mov_b32_e32 v65, 0
	v_mov_b32_e32 v61, 0
	v_mov_b32_e32 v57, 0
	v_mov_b32_e32 v53, 0
	ds_read_b128 v[182:185], v165 offset:0
	v_cmp_lt_i32_e32 vcc, -1, v151
	v_lshlrev_b32_e32 v148, 13, v151
	v_mov_b32_e32 v149, 0
	v_lshl_add_u64 v[148:149], v[148:149], 0, v[86:87]
	v_cndmask_b32_e32 v148, v168, v148, vcc
	v_cndmask_b32_e32 v149, v169, v149, vcc
	s_waitcnt lgkmcnt(0)
	global_store_dwordx4 v[148:149], v[182:185], off nt
	ds_read_b128 v[182:185], v165 offset:8192
	v_cmp_lt_i32_e32 vcc, -1, v166
	v_lshlrev_b32_e32 v148, 13, v166
	v_mov_b32_e32 v149, 0
	v_lshl_add_u64 v[148:149], v[148:149], 0, v[86:87]
	v_cndmask_b32_e32 v148, v168, v148, vcc
	v_cndmask_b32_e32 v149, v169, v149, vcc
	s_waitcnt lgkmcnt(0)
	global_store_dwordx4 v[148:149], v[182:185], off nt
	ds_read_b32 v150, v82 offset:512
	ds_read_b32 v151, v83 offset:512
	ds_read_b32 v166, v83 offset:640
	s_waitcnt lgkmcnt(2)
	v_mul_f32_e32 v46, v150, v46
	v_mul_f32_e32 v47, v150, v47
	v_mul_f32_e32 v48, v150, v48
	v_mul_f32_e32 v49, v150, v49
	v_mul_f32_e32 v42, v150, v42
	v_mul_f32_e32 v43, v150, v43
	v_mul_f32_e32 v44, v150, v44
	v_mul_f32_e32 v45, v150, v45
	v_cvt_pk_bf16_f32 v182, v46, v47
	v_cvt_pk_bf16_f32 v183, v48, v49
	v_cvt_pk_bf16_f32 v184, v42, v43
	v_cvt_pk_bf16_f32 v185, v44, v45
	ds_write_b128 v164, v[182:185]
	v_mul_f32_e32 v38, v150, v38
	v_mul_f32_e32 v39, v150, v39
	v_mul_f32_e32 v40, v150, v40
	v_mul_f32_e32 v41, v150, v41
	v_mul_f32_e32 v34, v150, v34
	v_mul_f32_e32 v35, v150, v35
	v_mul_f32_e32 v36, v150, v36
	v_mul_f32_e32 v37, v150, v37
	v_cvt_pk_bf16_f32 v182, v38, v39
	v_cvt_pk_bf16_f32 v183, v40, v41
	v_cvt_pk_bf16_f32 v184, v34, v35
	v_cvt_pk_bf16_f32 v185, v36, v37
	v_xor_b32_e32 v167, 64, v164
	ds_write_b128 v167, v[182:185]
	v_mov_b32_e32 v46, 0
	v_mov_b32_e32 v42, 0
	v_mov_b32_e32 v38, 0
	v_mov_b32_e32 v34, 0
	v_mov_b32_e32 v47, 0
	v_mov_b32_e32 v43, 0
	v_mov_b32_e32 v39, 0
	v_mov_b32_e32 v35, 0
	v_mov_b32_e32 v48, 0
	v_mov_b32_e32 v44, 0
	v_mov_b32_e32 v40, 0
	v_mov_b32_e32 v36, 0
	v_mov_b32_e32 v49, 0
	v_mov_b32_e32 v45, 0
	v_mov_b32_e32 v41, 0
	v_mov_b32_e32 v37, 0
	ds_read_b128 v[182:185], v165 offset:0
	v_cmp_lt_i32_e32 vcc, -1, v151
	v_lshlrev_b32_e32 v148, 13, v151
	v_mov_b32_e32 v149, 0
	v_lshl_add_u64 v[148:149], v[148:149], 0, v[86:87]
	v_cndmask_b32_e32 v148, v168, v148, vcc
	v_cndmask_b32_e32 v149, v169, v149, vcc
	s_waitcnt lgkmcnt(0)
	global_store_dwordx4 v[148:149], v[182:185], off nt
	ds_read_b128 v[182:185], v165 offset:8192
	v_cmp_lt_i32_e32 vcc, -1, v166
	v_lshlrev_b32_e32 v148, 13, v166
	v_mov_b32_e32 v149, 0
	v_lshl_add_u64 v[148:149], v[148:149], 0, v[86:87]
	v_cndmask_b32_e32 v148, v168, v148, vcc
	v_cndmask_b32_e32 v149, v169, v149, vcc
	s_waitcnt lgkmcnt(0)
	global_store_dwordx4 v[148:149], v[182:185], off nt
	ds_read_b32 v150, v82 offset:768
	ds_read_b32 v151, v83 offset:768
	ds_read_b32 v166, v83 offset:896
	s_waitcnt lgkmcnt(2)
; #define PG8_LAS __attribute__((address_space(3)))
; __device__ __forceinline__ unsigned cvtpk(float lo, float hi) { f32x2 v = {lo, hi}; bf16x2_t b = __builtin_convertvector(v, bf16x2_t); return __builtin_bit_cast(unsigned, b); }
; __device__ __forceinline__ void moe_down_stream(PG8_LAS unsigned char* lds, int e, int cb0, int slot0, int nv, const bf16_t* HIDp, const float* Wd, bf16_t* Y, const float* slot_w, const int* slot_dst) {
;     ...
;         if (((t + 1) & 7) == 7) {
;             const int cb = cb0 + ((t + 1) >> 3);
; #pragma unroll
;             for (int m = 0; m < DNM; ++m) {
;                 const float w_ = lw[4 * (16 * m + fr) + wr];
; #pragma unroll
;                 for (int p = 0; p < 2; ++p) { const f32x4 v0 = acc[m][2 * p] * w_, v1 = acc[m][2 * p + 1] * w_; u32x4 w; w.x = cvtpk(v0[0], v0[1]); w.y = cvtpk(v0[2], v0[3]); w.z = cvtpk(v1[0], v1[1]); w.w = cvtpk(v1[2], v1[3]);
;                     *(PG8_LAS u32x4*)(stg + fr * 128 + (((4 * p + fq) ^ (fr & 7)) * 16)) = w; }
; #pragma unroll
;                 for (int hh = 0; hh < 2; ++hh) { const int r = (lane >> 3) + 8 * hh, cc = lane & 7; const u32x4 d = *(const PG8_LAS u32x4*)(stg + r * 128 + ((cc ^ (r & 7)) * 16)); const int dst_ = ldst[4 * (16 * m + r) + wr];
;                     if (dst_ >= 0) *(u32x4*)(Y + (size_t)dst_ * D + 128 * cb + 64 * wc + 8 * cc) = d; }
; #pragma unroll
;                 for (int n = 0; n < 4; ++n) acc[m][n] = (f32x4){0.f, 0.f, 0.f, 0.f}; } }
	v_mul_f32_e32 v18, v150, v18
	v_mul_f32_e32 v19, v150, v19
	v_mul_f32_e32 v20, v150, v20
	v_mul_f32_e32 v21, v150, v21
	v_mul_f32_e32 v22, v150, v22
	v_mul_f32_e32 v23, v150, v23
	v_mul_f32_e32 v24, v150, v24
	v_mul_f32_e32 v25, v150, v25
	v_cvt_pk_bf16_f32 v182, v18, v19
	v_cvt_pk_bf16_f32 v183, v20, v21
	v_cvt_pk_bf16_f32 v184, v22, v23
	v_cvt_pk_bf16_f32 v185, v24, v25
	ds_write_b128 v164, v[182:185]
	v_mul_f32_e32 v26, v150, v26
	v_mul_f32_e32 v27, v150, v27
	v_mul_f32_e32 v28, v150, v28
	v_mul_f32_e32 v29, v150, v29
	v_mul_f32_e32 v30, v150, v30
	v_mul_f32_e32 v31, v150, v31
	v_mul_f32_e32 v32, v150, v32
	v_mul_f32_e32 v33, v150, v33
	v_cvt_pk_bf16_f32 v182, v26, v27
	v_cvt_pk_bf16_f32 v183, v28, v29
	v_cvt_pk_bf16_f32 v184, v30, v31
	v_cvt_pk_bf16_f32 v185, v32, v33
	v_xor_b32_e32 v167, 64, v164
	ds_write_b128 v167, v[182:185]
	v_mov_b32_e32 v18, 0
	v_mov_b32_e32 v22, 0
	v_mov_b32_e32 v26, 0
	v_mov_b32_e32 v30, 0
	v_mov_b32_e32 v19, 0
	v_mov_b32_e32 v23, 0
	v_mov_b32_e32 v27, 0
	v_mov_b32_e32 v31, 0
	v_mov_b32_e32 v20, 0
	v_mov_b32_e32 v24, 0
	v_mov_b32_e32 v28, 0
	v_mov_b32_e32 v32, 0
	v_mov_b32_e32 v21, 0
	v_mov_b32_e32 v25, 0
	v_mov_b32_e32 v29, 0
	v_mov_b32_e32 v33, 0
	ds_read_b128 v[182:185], v165 offset:0
	v_cmp_lt_i32_e32 vcc, -1, v151
	v_lshlrev_b32_e32 v148, 13, v151
	v_mov_b32_e32 v149, 0
	v_lshl_add_u64 v[148:149], v[148:149], 0, v[86:87]
	v_cndmask_b32_e32 v148, v168, v148, vcc
	v_cndmask_b32_e32 v149, v169, v149, vcc
	s_waitcnt lgkmcnt(0)
	global_store_dwordx4 v[148:149], v[182:185], off nt
	ds_read_b128 v[182:185], v165 offset:8192
	v_cmp_lt_i32_e32 vcc, -1, v166
	v_lshlrev_b32_e32 v148, 13, v166
	v_mov_b32_e32 v149, 0
	v_lshl_add_u64 v[148:149], v[148:149], 0, v[86:87]
	v_cndmask_b32_e32 v148, v168, v148, vcc
	v_cndmask_b32_e32 v149, v169, v149, vcc
	s_waitcnt lgkmcnt(0)
	global_store_dwordx4 v[148:149], v[182:185], off nt
	ds_read_b32 v150, v82 offset:1024
	ds_read_b32 v151, v83 offset:1024
	ds_read_b32 v166, v83 offset:1152
	s_waitcnt lgkmcnt(2)
	v_mul_f32_e32 v2, v150, v2
	v_mul_f32_e32 v3, v150, v3
	v_mul_f32_e32 v4, v150, v4
	v_mul_f32_e32 v5, v150, v5
	v_mul_f32_e32 v6, v150, v6
	v_mul_f32_e32 v7, v150, v7
	v_mul_f32_e32 v8, v150, v8
	v_mul_f32_e32 v9, v150, v9
	v_cvt_pk_bf16_f32 v182, v2, v3
	v_cvt_pk_bf16_f32 v183, v4, v5
	v_cvt_pk_bf16_f32 v184, v6, v7
	v_cvt_pk_bf16_f32 v185, v8, v9
	ds_write_b128 v164, v[182:185]
	v_mul_f32_e32 v10, v150, v10
	v_mul_f32_e32 v11, v150, v11
	v_mul_f32_e32 v12, v150, v12
	v_mul_f32_e32 v13, v150, v13
	v_mul_f32_e32 v14, v150, v14
	v_mul_f32_e32 v15, v150, v15
	v_mul_f32_e32 v16, v150, v16
	v_mul_f32_e32 v17, v150, v17
	v_cvt_pk_bf16_f32 v182, v10, v11
	v_cvt_pk_bf16_f32 v183, v12, v13
	v_cvt_pk_bf16_f32 v184, v14, v15
	v_cvt_pk_bf16_f32 v185, v16, v17
	v_xor_b32_e32 v167, 64, v164
	ds_write_b128 v167, v[182:185]
	v_mov_b32_e32 v2, 0
	v_mov_b32_e32 v6, 0
	v_mov_b32_e32 v10, 0
	v_mov_b32_e32 v14, 0
	v_mov_b32_e32 v3, 0
	v_mov_b32_e32 v7, 0
	v_mov_b32_e32 v11, 0
	v_mov_b32_e32 v15, 0
	v_mov_b32_e32 v4, 0
	v_mov_b32_e32 v8, 0
	v_mov_b32_e32 v12, 0
	v_mov_b32_e32 v16, 0
	v_mov_b32_e32 v5, 0
	v_mov_b32_e32 v9, 0
	v_mov_b32_e32 v13, 0
	v_mov_b32_e32 v17, 0
	ds_read_b128 v[182:185], v165 offset:0
	v_cmp_lt_i32_e32 vcc, -1, v151
	v_lshlrev_b32_e32 v148, 13, v151
	v_mov_b32_e32 v149, 0
	v_lshl_add_u64 v[148:149], v[148:149], 0, v[86:87]
	v_cndmask_b32_e32 v148, v168, v148, vcc
	v_cndmask_b32_e32 v149, v169, v149, vcc
	s_waitcnt lgkmcnt(0)
	global_store_dwordx4 v[148:149], v[182:185], off nt
	ds_read_b128 v[182:185], v165 offset:8192
	v_cmp_lt_i32_e32 vcc, -1, v166
	v_lshlrev_b32_e32 v148, 13, v166
	v_mov_b32_e32 v149, 0
	v_lshl_add_u64 v[148:149], v[148:149], 0, v[86:87]
	v_cndmask_b32_e32 v148, v168, v148, vcc
	v_cndmask_b32_e32 v149, v169, v149, vcc
	s_waitcnt lgkmcnt(0)
	global_store_dwordx4 v[148:149], v[182:185], off nt
	v_add_co_u32_e32 v86, vcc, 0x400, v86
	s_nop 1
	v_addc_co_u32_e32 v87, vcc, 0, v87, vcc
	s_waitcnt lgkmcnt(0)
